# speedup vs baseline: 1.0323x; 1.0219x over previous
attn_fwd_pwg4x64:
	s_load_dwordx2 s[22:23], s[0:1], 0x0
	s_load_dwordx8 s[4:11], s[0:1], 0x8
	s_load_dwordx2 s[36:37], s[0:1], 0x28
	s_load_dwordx4 s[16:19], s[0:1], 0x30
	s_load_dwordx2 s[20:21], s[0:1], 0x40
	s_and_b32 s3, s2, 15
	s_bfe_u32 s30, s2, 0x30004
	s_lshr_b32 s2, s2, 3
	s_and_b32 s2, s2, 0x1ffffff0
	s_or_b32 s2, s2, s3
	s_mov_b32 s3, 0
	s_lshl_b32 s31, s30, 8
	s_lshl_b64 s[26:27], s[2:3], 19
	s_lshl_b64 s[24:25], s[2:3], 11
	s_lshl_b64 s[38:39], s[2:3], 20
	s_lshl_b32 s43, s30, 17
	s_add_u32 s38, s38, s43
	s_addc_u32 s39, s39, 0
	v_and_b32_e32 v1, 15, v0
	v_lshrrev_b32_e32 v28, 4, v0
	v_lshrrev_b32_e32 v29, 6, v0
	v_lshlrev_b32_e32 v30, 5, v1
	v_lshl_or_b32 v2, v28, 9, v30
	v_bfe_u32 v31, v0, 4, 2
	v_lshl_or_b32 v3, v31, 9, v30
	v_lshl_or_b32 v3, v29, 15, v3
	v_lshlrev_b32_e32 v32, 4, v1
	v_lshl_or_b32 v26, v28, 8, v32
	s_lshl_b32 s43, s30, 16
	v_or_b32_e32 v26, s43, v26
	v_mov_b32_e32 v207, v2
	v_mov_b32_e32 v208, v26
	v_lshlrev_b32_e32 v38, 2, v0
	v_lshlrev_b32_e32 v40, 14, v29
	v_lshlrev_b32_e32 v33, 12, v29
	v_mbcnt_lo_u32_b32 v204, -1, 0
	v_mbcnt_hi_u32_b32 v204, -1, v204
	v_readfirstlane_b32 s28, v33
	v_readfirstlane_b32 s29, v33
	v_mov_b32_e32 v4, 0
	v_mov_b32_e32 v5, 0
	v_mov_b32_e32 v6, 0
	v_mov_b32_e32 v7, 0
	v_mov_b32_e32 v8, 0
	v_mov_b32_e32 v9, 0
	v_mov_b32_e32 v10, 0
	v_mov_b32_e32 v11, 0
	s_mov_b32 s44, 0x3e0293ee
	s_mov_b32 s45, 0x3e0293ee
	s_waitcnt lgkmcnt(0)
	s_add_u32 s12, s4, s26
	s_addc_u32 s13, s5, s27
	s_and_b32 s13, s13, 0xffff
	s_mov_b32 s14, 0x80000
	s_mov_b32 s15, 0x20000
	s_add_u32 s4, s6, s26
	s_addc_u32 s5, s7, s27
	s_and_b32 s5, s5, 0xffff
	s_mov_b32 s6, 0x80000
	s_mov_b32 s7, 0x20000
	s_add_u32 s32, s10, s38
	s_addc_u32 s33, s11, s39
	s_add_u32 s34, s36, s38
	s_addc_u32 s35, s37, s39
	s_add_u32 s40, s22, s38
	s_addc_u32 s41, s23, s39
	s_lshl_b64 s[46:47], s[2:3], 5
	s_add_u32 s10, s16, s46
	s_addc_u32 s11, s17, s47
	s_lshl_b32 s43, s30, 2
	s_add_u32 s46, s10, s43
	s_addc_u32 s47, s11, 0
	s_lshl_b64 s[26:27], s[2:3], 12
	s_add_u32 s26, s18, s26
	s_addc_u32 s27, s19, s27
	s_lshl_b32 s43, s30, 9
	s_add_u32 s26, s26, s43
	s_addc_u32 s27, s27, 0
	global_load_dwordx4 v[42:45], v2, s[32:33] nt
	global_load_dwordx4 v[46:49], v2, s[32:33] offset:16 nt
	s_add_u32 s32, s32, 8192
	s_addc_u32 s33, s33, 0
	global_load_dwordx4 v[50:53], v2, s[32:33] nt
	global_load_dwordx4 v[54:57], v2, s[32:33] offset:16 nt
	s_add_u32 s32, s32, 8192
	s_addc_u32 s33, s33, 0
	global_load_dwordx4 v[58:61], v2, s[32:33] nt
	global_load_dwordx4 v[62:65], v2, s[32:33] offset:16 nt
	s_add_u32 s32, s32, 8192
	s_addc_u32 s33, s33, 0
	global_load_dwordx4 v[66:69], v2, s[32:33] nt
	global_load_dwordx4 v[70:73], v2, s[32:33] offset:16 nt
	s_add_u32 s32, s32, 8192
	s_addc_u32 s33, s33, 0
	global_load_dwordx4 v[74:77], v2, s[32:33] nt
	global_load_dwordx4 v[78:81], v2, s[32:33] offset:16 nt
	s_add_u32 s32, s32, 8192
	s_addc_u32 s33, s33, 0
	global_load_dwordx4 v[82:85], v2, s[32:33] nt
	global_load_dwordx4 v[86:89], v2, s[32:33] offset:16 nt
	s_add_u32 s32, s32, 8192
	s_addc_u32 s33, s33, 0
	global_load_dwordx4 v[90:93], v2, s[32:33] nt
	global_load_dwordx4 v[94:97], v2, s[32:33] offset:16 nt
	s_add_u32 s32, s32, 8192
	s_addc_u32 s33, s33, 0
	global_load_dwordx4 v[98:101], v2, s[32:33] nt
	global_load_dwordx4 v[102:105], v2, s[32:33] offset:16 nt
	s_add_u32 s32, s32, 8192
	s_addc_u32 s33, s33, 0
	global_load_dwordx4 v[248:251], v2, s[32:33] nt
	global_load_dwordx4 v[252:255], v2, s[32:33] offset:16 nt
	s_add_u32 s32, s32, 8192
	s_addc_u32 s33, s33, 0
	global_load_dwordx4 v[106:109], v2, s[34:35] nt
	global_load_dwordx4 v[110:113], v2, s[34:35] offset:16 nt
	s_add_u32 s34, s34, 8192
	s_addc_u32 s35, s35, 0
	global_load_dwordx4 v[114:117], v2, s[34:35] nt
	global_load_dwordx4 v[118:121], v2, s[34:35] offset:16 nt
	s_add_u32 s34, s34, 8192
	s_addc_u32 s35, s35, 0
	global_load_dwordx4 v[122:125], v2, s[34:35] nt
	global_load_dwordx4 v[126:129], v2, s[34:35] offset:16 nt
	s_add_u32 s34, s34, 8192
	s_addc_u32 s35, s35, 0
	global_load_dwordx4 v[130:133], v2, s[34:35] nt
	global_load_dwordx4 v[134:137], v2, s[34:35] offset:16 nt
	s_add_u32 s34, s34, 8192
	s_addc_u32 s35, s35, 0
	global_load_dwordx4 v[138:141], v2, s[34:35] nt
	global_load_dwordx4 v[142:145], v2, s[34:35] offset:16 nt
	s_add_u32 s34, s34, 8192
	s_addc_u32 s35, s35, 0
	global_load_dwordx4 v[146:149], v2, s[34:35] nt
	global_load_dwordx4 v[150:153], v2, s[34:35] offset:16 nt
	s_add_u32 s34, s34, 8192
	s_addc_u32 s35, s35, 0
	global_load_dwordx4 v[154:157], v2, s[34:35] nt
	global_load_dwordx4 v[158:161], v2, s[34:35] offset:16 nt
	s_add_u32 s34, s34, 8192
	s_addc_u32 s35, s35, 0
	global_load_dwordx4 v[162:165], v2, s[34:35] nt
	global_load_dwordx4 v[166:169], v2, s[34:35] offset:16 nt
	s_add_u32 s34, s34, 8192
	s_addc_u32 s35, s35, 0
	global_load_dwordx4 v[170:173], v2, s[34:35] nt
	global_load_dwordx4 v[174:177], v2, s[34:35] offset:16 nt
	s_add_u32 s34, s34, 8192
	s_addc_u32 s35, s35, 0
	global_load_dwordx4 v[178:181], v2, s[34:35] nt
	global_load_dwordx4 v[182:185], v2, s[34:35] offset:16 nt
	s_add_u32 s34, s34, 8192
	s_addc_u32 s35, s35, 0
	global_load_dwordx4 v[186:189], v2, s[34:35] nt
	global_load_dwordx4 v[190:193], v2, s[34:35] offset:16 nt
	s_add_u32 s34, s34, 8192
	s_addc_u32 s35, s35, 0
	global_load_dwordx4 v[194:197], v2, s[34:35] nt
	global_load_dwordx4 v[198:201], v2, s[34:35] offset:16 nt
	s_add_u32 s34, s34, 8192
	s_addc_u32 s35, s35, 0
	s_waitcnt vmcnt(40)
	v_cvt_pk_bf16_f32 v12, v42, v43
	v_cvt_pk_bf16_f32 v13, v44, v45
	v_cvt_pk_bf16_f32 v14, v46, v47
	v_cvt_pk_bf16_f32 v15, v48, v49
	s_mov_b32 s42, 0x0
	buffer_store_dwordx4 v[12:15], v26, s[12:15], s42 offen sc1
	global_load_dwordx4 v[42:45], v2, s[34:35] nt
	global_load_dwordx4 v[46:49], v2, s[34:35] offset:16 nt
	s_add_u32 s34, s34, 8192
	s_addc_u32 s35, s35, 0
	s_waitcnt vmcnt(41)
	v_cvt_pk_bf16_f32 v16, v50, v51
	v_cvt_pk_bf16_f32 v17, v52, v53
	v_cvt_pk_bf16_f32 v18, v54, v55
	v_cvt_pk_bf16_f32 v19, v56, v57
	s_mov_b32 s42, 0x1000
	buffer_store_dwordx4 v[16:19], v26, s[12:15], s42 offen sc1
	global_load_dwordx4 v[50:53], v2, s[34:35] nt
	global_load_dwordx4 v[54:57], v2, s[34:35] offset:16 nt
	s_add_u32 s34, s34, 8192
	s_addc_u32 s35, s35, 0
	s_waitcnt vmcnt(42)
	v_cvt_pk_bf16_f32 v20, v58, v59
	v_cvt_pk_bf16_f32 v21, v60, v61
	v_cvt_pk_bf16_f32 v22, v62, v63
	v_cvt_pk_bf16_f32 v23, v64, v65
	s_mov_b32 s42, 0x2000
	buffer_store_dwordx4 v[20:23], v26, s[12:15], s42 offen sc1
	global_load_dwordx4 v[58:61], v2, s[34:35] nt
	global_load_dwordx4 v[62:65], v2, s[34:35] offset:16 nt
	s_add_u32 s34, s34, 8192
	s_addc_u32 s35, s35, 0
	s_waitcnt vmcnt(43)
	v_cvt_pk_bf16_f32 v12, v66, v67
	v_cvt_pk_bf16_f32 v13, v68, v69
	v_cvt_pk_bf16_f32 v14, v70, v71
	v_cvt_pk_bf16_f32 v15, v72, v73
	s_mov_b32 s42, 0x3000
	buffer_store_dwordx4 v[12:15], v26, s[12:15], s42 offen sc1
	global_load_dwordx4 v[66:69], v2, s[34:35] nt
	global_load_dwordx4 v[70:73], v2, s[34:35] offset:16 nt
	s_sub_u32 s34, s34, 122880
	s_subb_u32 s35, s35, 0
	s_waitcnt vmcnt(44)
	v_cvt_pk_bf16_f32 v16, v74, v75
	v_cvt_pk_bf16_f32 v17, v76, v77
	v_cvt_pk_bf16_f32 v18, v78, v79
	v_cvt_pk_bf16_f32 v19, v80, v81
	s_mov_b32 s42, 0x4000
	buffer_store_dwordx4 v[16:19], v26, s[12:15], s42 offen sc1
	global_load_dwordx4 v[74:77], v3, s[40:41] nt
	global_load_dwordx4 v[78:81], v3, s[40:41] offset:16 nt
	s_add_u32 s40, s40, 2048
	s_addc_u32 s41, s41, 0
	s_waitcnt vmcnt(45)
	v_cvt_pk_bf16_f32 v20, v82, v83
	v_cvt_pk_bf16_f32 v21, v84, v85
	v_cvt_pk_bf16_f32 v22, v86, v87
	v_cvt_pk_bf16_f32 v23, v88, v89
	s_mov_b32 s42, 0x5000
	buffer_store_dwordx4 v[20:23], v26, s[12:15], s42 offen sc1
	global_load_dwordx4 v[82:85], v3, s[40:41] nt
	global_load_dwordx4 v[86:89], v3, s[40:41] offset:16 nt
	s_add_u32 s40, s40, 2048
	s_addc_u32 s41, s41, 0
	s_waitcnt vmcnt(46)
	v_cvt_pk_bf16_f32 v12, v90, v91
	v_cvt_pk_bf16_f32 v13, v92, v93
	v_cvt_pk_bf16_f32 v14, v94, v95
	v_cvt_pk_bf16_f32 v15, v96, v97
	s_mov_b32 s42, 0x6000
	buffer_store_dwordx4 v[12:15], v26, s[12:15], s42 offen sc1
	global_load_dwordx4 v[90:93], v3, s[40:41] nt
	global_load_dwordx4 v[94:97], v3, s[40:41] offset:16 nt
	s_add_u32 s40, s40, 2048
	s_addc_u32 s41, s41, 0
	s_waitcnt vmcnt(47)
	v_cvt_pk_bf16_f32 v16, v98, v99
	v_cvt_pk_bf16_f32 v17, v100, v101
	v_cvt_pk_bf16_f32 v18, v102, v103
	v_cvt_pk_bf16_f32 v19, v104, v105
	s_mov_b32 s42, 0x7000
	buffer_store_dwordx4 v[16:19], v26, s[12:15], s42 offen sc1
	global_load_dwordx4 v[98:101], v3, s[40:41] nt
	global_load_dwordx4 v[102:105], v3, s[40:41] offset:16 nt
	s_add_u32 s40, s40, 2048
	s_addc_u32 s41, s41, 0
	s_waitcnt vmcnt(46)
	v_mov_b32_e32 v4, 0
	v_mov_b32_e32 v5, 0
	v_mov_b32_e32 v6, 0
	v_mov_b32_e32 v7, 0
	v_mov_b32_e32 v8, 0
	v_mov_b32_e32 v9, 0
	v_mov_b32_e32 v10, 0
	v_mov_b32_e32 v11, 0
	v_pk_add_f32 v[4:5], v[106:107], v[4:5]
	v_pk_add_f32 v[6:7], v[108:109], v[6:7]
	v_pk_add_f32 v[8:9], v[110:111], v[8:9]
	v_pk_add_f32 v[10:11], v[112:113], v[10:11]
	v_cvt_pk_bf16_f32 v20, v106, v107
	v_cvt_pk_bf16_f32 v21, v108, v109
	v_cvt_pk_bf16_f32 v22, v110, v111
	v_cvt_pk_bf16_f32 v23, v112, v113
	s_mov_b32 s42, 0x0
	buffer_store_dwordx4 v[20:23], v26, s[4:7], s42 offen sc1
	global_load_dwordx4 v[106:109], v3, s[40:41] nt
	global_load_dwordx4 v[110:113], v3, s[40:41] offset:16 nt
	s_add_u32 s40, s40, 2048
	s_addc_u32 s41, s41, 0
	s_waitcnt vmcnt(47)
	v_pk_add_f32 v[4:5], v[114:115], v[4:5]
	v_pk_add_f32 v[6:7], v[116:117], v[6:7]
	v_pk_add_f32 v[8:9], v[118:119], v[8:9]
	v_pk_add_f32 v[10:11], v[120:121], v[10:11]
	v_cvt_pk_bf16_f32 v12, v114, v115
	v_cvt_pk_bf16_f32 v13, v116, v117
	v_cvt_pk_bf16_f32 v14, v118, v119
	v_cvt_pk_bf16_f32 v15, v120, v121
	s_mov_b32 s42, 0x1000
	buffer_store_dwordx4 v[12:15], v26, s[4:7], s42 offen sc1
	global_load_dwordx4 v[114:117], v3, s[40:41] nt
	global_load_dwordx4 v[118:121], v3, s[40:41] offset:16 nt
	s_add_u32 s40, s40, 2048
	s_addc_u32 s41, s41, 0
	s_waitcnt vmcnt(48)
	v_pk_add_f32 v[4:5], v[122:123], v[4:5]
	v_pk_add_f32 v[6:7], v[124:125], v[6:7]
	v_pk_add_f32 v[8:9], v[126:127], v[8:9]
	v_pk_add_f32 v[10:11], v[128:129], v[10:11]
	v_cvt_pk_bf16_f32 v16, v122, v123
	v_cvt_pk_bf16_f32 v17, v124, v125
	v_cvt_pk_bf16_f32 v18, v126, v127
	v_cvt_pk_bf16_f32 v19, v128, v129
	s_mov_b32 s42, 0x2000
	buffer_store_dwordx4 v[16:19], v26, s[4:7], s42 offen sc1
	global_load_dwordx4 v[122:125], v3, s[40:41] nt
	global_load_dwordx4 v[126:129], v3, s[40:41] offset:16 nt
	s_add_u32 s40, s40, 2048
	s_addc_u32 s41, s41, 0
	s_waitcnt vmcnt(49)
	v_pk_add_f32 v[4:5], v[130:131], v[4:5]
	v_pk_add_f32 v[6:7], v[132:133], v[6:7]
	v_pk_add_f32 v[8:9], v[134:135], v[8:9]
	v_pk_add_f32 v[10:11], v[136:137], v[10:11]
	v_cvt_pk_bf16_f32 v20, v130, v131
	v_cvt_pk_bf16_f32 v21, v132, v133
	v_cvt_pk_bf16_f32 v22, v134, v135
	v_cvt_pk_bf16_f32 v23, v136, v137
	s_mov_b32 s42, 0x3000
	buffer_store_dwordx4 v[20:23], v26, s[4:7], s42 offen sc1
	global_load_dwordx4 v[130:133], v3, s[40:41] nt
	global_load_dwordx4 v[134:137], v3, s[40:41] offset:16 nt
	s_add_u32 s40, s40, 2048
	s_addc_u32 s41, s41, 0
	s_waitcnt vmcnt(50)
	v_pk_add_f32 v[4:5], v[138:139], v[4:5]
	v_pk_add_f32 v[6:7], v[140:141], v[6:7]
	v_pk_add_f32 v[8:9], v[142:143], v[8:9]
	v_pk_add_f32 v[10:11], v[144:145], v[10:11]
	v_cvt_pk_bf16_f32 v12, v138, v139
	v_cvt_pk_bf16_f32 v13, v140, v141
	v_cvt_pk_bf16_f32 v14, v142, v143
	v_cvt_pk_bf16_f32 v15, v144, v145
	s_mov_b32 s42, 0x4000
	buffer_store_dwordx4 v[12:15], v26, s[4:7], s42 offen sc1
	global_load_dwordx4 v[138:141], v3, s[40:41] nt
	global_load_dwordx4 v[142:145], v3, s[40:41] offset:16 nt
	s_add_u32 s40, s40, 2048
	s_addc_u32 s41, s41, 0
	s_waitcnt vmcnt(51)
	v_pk_add_f32 v[4:5], v[146:147], v[4:5]
	v_pk_add_f32 v[6:7], v[148:149], v[6:7]
	v_pk_add_f32 v[8:9], v[150:151], v[8:9]
	v_pk_add_f32 v[10:11], v[152:153], v[10:11]
	v_cvt_pk_bf16_f32 v16, v146, v147
	v_cvt_pk_bf16_f32 v17, v148, v149
	v_cvt_pk_bf16_f32 v18, v150, v151
	v_cvt_pk_bf16_f32 v19, v152, v153
	s_mov_b32 s42, 0x5000
	buffer_store_dwordx4 v[16:19], v26, s[4:7], s42 offen sc1
	global_load_dwordx4 v[146:149], v3, s[40:41] nt
	global_load_dwordx4 v[150:153], v3, s[40:41] offset:16 nt
	s_add_u32 s40, s40, 2048
	s_addc_u32 s41, s41, 0
	s_waitcnt vmcnt(52)
	v_pk_add_f32 v[4:5], v[154:155], v[4:5]
	v_pk_add_f32 v[6:7], v[156:157], v[6:7]
	v_pk_add_f32 v[8:9], v[158:159], v[8:9]
	v_pk_add_f32 v[10:11], v[160:161], v[10:11]
	v_cvt_pk_bf16_f32 v20, v154, v155
	v_cvt_pk_bf16_f32 v21, v156, v157
	v_cvt_pk_bf16_f32 v22, v158, v159
	v_cvt_pk_bf16_f32 v23, v160, v161
	s_mov_b32 s42, 0x6000
	buffer_store_dwordx4 v[20:23], v26, s[4:7], s42 offen sc1
	global_load_dwordx4 v[154:157], v3, s[40:41] nt
	global_load_dwordx4 v[158:161], v3, s[40:41] offset:16 nt
	s_add_u32 s40, s40, 2048
	s_addc_u32 s41, s41, 0
	s_waitcnt vmcnt(53)
	v_pk_add_f32 v[4:5], v[162:163], v[4:5]
	v_pk_add_f32 v[6:7], v[164:165], v[6:7]
	v_pk_add_f32 v[8:9], v[166:167], v[8:9]
	v_pk_add_f32 v[10:11], v[168:169], v[10:11]
	v_cvt_pk_bf16_f32 v12, v162, v163
	v_cvt_pk_bf16_f32 v13, v164, v165
	v_cvt_pk_bf16_f32 v14, v166, v167
	v_cvt_pk_bf16_f32 v15, v168, v169
	s_mov_b32 s42, 0x7000
	buffer_store_dwordx4 v[12:15], v26, s[4:7], s42 offen sc1
	global_load_dwordx4 v[162:165], v3, s[40:41] nt
	global_load_dwordx4 v[166:169], v3, s[40:41] offset:16 nt
	s_add_u32 s40, s40, 2048
	s_addc_u32 s41, s41, 0
	s_waitcnt vmcnt(54)
	v_pk_add_f32 v[4:5], v[170:171], v[4:5]
	v_pk_add_f32 v[6:7], v[172:173], v[6:7]
	v_pk_add_f32 v[8:9], v[174:175], v[8:9]
	v_pk_add_f32 v[10:11], v[176:177], v[10:11]
	v_cvt_pk_bf16_f32 v16, v170, v171
	v_cvt_pk_bf16_f32 v17, v172, v173
	v_cvt_pk_bf16_f32 v18, v174, v175
	v_cvt_pk_bf16_f32 v19, v176, v177
	s_mov_b32 s42, 0x8000
	buffer_store_dwordx4 v[16:19], v26, s[4:7], s42 offen sc1
	global_load_dwordx4 v[170:173], v3, s[40:41] nt
	global_load_dwordx4 v[174:177], v3, s[40:41] offset:16 nt
	s_add_u32 s40, s40, 2048
	s_addc_u32 s41, s41, 0
	s_waitcnt vmcnt(55)
	v_pk_add_f32 v[4:5], v[178:179], v[4:5]
	v_pk_add_f32 v[6:7], v[180:181], v[6:7]
	v_pk_add_f32 v[8:9], v[182:183], v[8:9]
	v_pk_add_f32 v[10:11], v[184:185], v[10:11]
	v_cvt_pk_bf16_f32 v20, v178, v179
	v_cvt_pk_bf16_f32 v21, v180, v181
	v_cvt_pk_bf16_f32 v22, v182, v183
	v_cvt_pk_bf16_f32 v23, v184, v185
	s_mov_b32 s42, 0x9000
	buffer_store_dwordx4 v[20:23], v26, s[4:7], s42 offen sc1
	global_load_dwordx4 v[178:181], v3, s[40:41] nt
	global_load_dwordx4 v[182:185], v3, s[40:41] offset:16 nt
	s_add_u32 s40, s40, 2048
	s_addc_u32 s41, s41, 0
	s_waitcnt vmcnt(56)
	v_pk_add_f32 v[4:5], v[186:187], v[4:5]
	v_pk_add_f32 v[6:7], v[188:189], v[6:7]
	v_pk_add_f32 v[8:9], v[190:191], v[8:9]
	v_pk_add_f32 v[10:11], v[192:193], v[10:11]
	v_cvt_pk_bf16_f32 v12, v186, v187
	v_cvt_pk_bf16_f32 v13, v188, v189
	v_cvt_pk_bf16_f32 v14, v190, v191
	v_cvt_pk_bf16_f32 v15, v192, v193
	s_mov_b32 s42, 0xa000
	buffer_store_dwordx4 v[12:15], v26, s[4:7], s42 offen sc1
	global_load_dwordx4 v[186:189], v3, s[40:41] nt
	global_load_dwordx4 v[190:193], v3, s[40:41] offset:16 nt
	s_add_u32 s40, s40, 2048
	s_addc_u32 s41, s41, 0
	s_waitcnt vmcnt(57)
	v_pk_add_f32 v[4:5], v[194:195], v[4:5]
	v_pk_add_f32 v[6:7], v[196:197], v[6:7]
	v_pk_add_f32 v[8:9], v[198:199], v[8:9]
	v_pk_add_f32 v[10:11], v[200:201], v[10:11]
	v_cvt_pk_bf16_f32 v16, v194, v195
	v_cvt_pk_bf16_f32 v17, v196, v197
	v_cvt_pk_bf16_f32 v18, v198, v199
	v_cvt_pk_bf16_f32 v19, v200, v201
	s_mov_b32 s42, 0xb000
	buffer_store_dwordx4 v[16:19], v26, s[4:7], s42 offen sc1
	global_load_dwordx4 v[194:197], v3, s[40:41] nt
	global_load_dwordx4 v[198:201], v3, s[40:41] offset:16 nt
	s_add_u32 s40, s40, 2048
	s_addc_u32 s41, s41, 0
	s_waitcnt vmcnt(57)
	v_pk_add_f32 v[4:5], v[42:43], v[4:5]
	v_pk_add_f32 v[6:7], v[44:45], v[6:7]
	v_pk_add_f32 v[8:9], v[46:47], v[8:9]
	v_pk_add_f32 v[10:11], v[48:49], v[10:11]
	v_cvt_pk_bf16_f32 v20, v42, v43
	v_cvt_pk_bf16_f32 v21, v44, v45
	v_cvt_pk_bf16_f32 v22, v46, v47
	v_cvt_pk_bf16_f32 v23, v48, v49
	s_mov_b32 s42, 0xc000
	buffer_store_dwordx4 v[20:23], v26, s[4:7], s42 offen sc1
	s_waitcnt vmcnt(55)
	v_pk_add_f32 v[4:5], v[50:51], v[4:5]
	v_pk_add_f32 v[6:7], v[52:53], v[6:7]
	v_pk_add_f32 v[8:9], v[54:55], v[8:9]
	v_pk_add_f32 v[10:11], v[56:57], v[10:11]
	v_cvt_pk_bf16_f32 v12, v50, v51
	v_cvt_pk_bf16_f32 v13, v52, v53
	v_cvt_pk_bf16_f32 v14, v54, v55
	v_cvt_pk_bf16_f32 v15, v56, v57
	s_mov_b32 s42, 0xd000
	buffer_store_dwordx4 v[12:15], v26, s[4:7], s42 offen sc1
	s_waitcnt vmcnt(53)
	v_pk_add_f32 v[4:5], v[58:59], v[4:5]
	v_pk_add_f32 v[6:7], v[60:61], v[6:7]
	v_pk_add_f32 v[8:9], v[62:63], v[8:9]
	v_pk_add_f32 v[10:11], v[64:65], v[10:11]
	v_cvt_pk_bf16_f32 v16, v58, v59
	v_cvt_pk_bf16_f32 v17, v60, v61
	v_cvt_pk_bf16_f32 v18, v62, v63
	v_cvt_pk_bf16_f32 v19, v64, v65
	s_mov_b32 s42, 0xe000
	buffer_store_dwordx4 v[16:19], v26, s[4:7], s42 offen sc1
	s_waitcnt vmcnt(51)
	v_pk_add_f32 v[4:5], v[66:67], v[4:5]
	v_pk_add_f32 v[6:7], v[68:69], v[6:7]
	v_pk_add_f32 v[8:9], v[70:71], v[8:9]
	v_pk_add_f32 v[10:11], v[72:73], v[10:11]
	v_cvt_pk_bf16_f32 v20, v66, v67
	v_cvt_pk_bf16_f32 v21, v68, v69
	v_cvt_pk_bf16_f32 v22, v70, v71
	v_cvt_pk_bf16_f32 v23, v72, v73
	s_mov_b32 s42, 0xf000
	buffer_store_dwordx4 v[20:23], v26, s[4:7], s42 offen sc1
	v_mul_u32_u24_e32 v27, 0x210, v28
	s_mov_b32 s43, 0x20000
	v_add3_u32 v27, s43, v27, v30
	ds_write_b128 v27, v[4:7]
	ds_write_b128 v27, v[8:11] offset:16
	s_movk_i32 s0, 0x80
	v_cmp_gt_u32_e64 s[0:1], s0, v0
	s_waitcnt lgkmcnt(0)
	s_barrier
	s_and_saveexec_b64 s[38:39], s[0:1]
	s_cbranch_execz .Lpro_nopart
	v_add_u32_e32 v28, 0x20000, v38
	ds_read2_b32 v[12:13], v28 offset1:132
	v_add_u32_e32 v29, 0x400, v28
	ds_read2_b32 v[14:15], v29 offset0:8 offset1:140
	v_add_u32_e32 v29, 0x800, v28
	ds_read2_b32 v[16:17], v29 offset0:16 offset1:148
	v_add_u32_e32 v29, 0xc00, v28
	ds_read2_b32 v[18:19], v29 offset0:24 offset1:156
	v_add_u32_e32 v29, 0x1000, v28
	ds_read2_b32 v[20:21], v29 offset0:32 offset1:164
	v_add_u32_e32 v29, 0x1400, v28
	ds_read2_b32 v[22:23], v29 offset0:40 offset1:172
	v_add_u32_e32 v29, 0x1800, v28
	ds_read2_b32 v[24:25], v29 offset0:48 offset1:180
	v_add_u32_e32 v29, 0x1c00, v28
	ds_read2_b32 v[26:27], v29 offset0:56 offset1:188
	s_waitcnt lgkmcnt(0)
	v_add_f32_e32 v4, 0, v12
	v_add_f32_e32 v4, v4, v13
	v_add_f32_e32 v4, v4, v14
	v_add_f32_e32 v4, v4, v15
	v_add_f32_e32 v4, v4, v16
	v_add_f32_e32 v4, v4, v17
	v_add_f32_e32 v4, v4, v18
	v_add_f32_e32 v4, v4, v19
	v_add_f32_e32 v4, v4, v20
	v_add_f32_e32 v4, v4, v21
	v_add_f32_e32 v4, v4, v22
	v_add_f32_e32 v4, v4, v23
	v_add_f32_e32 v4, v4, v24
	v_add_f32_e32 v4, v4, v25
	v_add_f32_e32 v4, v4, v26
	v_add_f32_e32 v4, v4, v27
	global_store_dword v38, v4, s[26:27] sc1

.Lpro_noflag:
	s_or_b64 exec, exec, s[38:39]
	v_lshlrev_b32_e32 v41, 2, v204
	v_and_b32_e32 v41, 28, v41
	global_load_dword v30, v41, s[10:11] sc1
	v_lshrrev_b32_e32 v202, 4, v204
	v_and_b32_e32 v31, 15, v204
	v_xor_b32_e32 v32, v31, v202
	v_xor_b32_e32 v33, 4, v32
	v_lshlrev_b32_e32 v34, 8, v202
	v_or_b32_e32 v35, 0x10000, v40
	v_add_u32_e32 v34, v34, v35
	v_lshl_add_u32 v24, v32, 4, v34
	v_lshl_add_u32 v25, v33, 4, v34
	v_pk_mul_f32 v[74:75], v[74:75], s[44:45] op_sel_hi:[1,0]
	v_pk_mul_f32 v[76:77], v[76:77], s[44:45] op_sel_hi:[1,0]
	v_pk_mul_f32 v[78:79], v[78:79], s[44:45] op_sel_hi:[1,0]
	v_pk_mul_f32 v[80:81], v[80:81], s[44:45] op_sel_hi:[1,0]
	v_cvt_pk_bf16_f32 v12, v74, v75
	v_cvt_pk_bf16_f32 v13, v76, v77
	v_cvt_pk_bf16_f32 v14, v78, v79
	v_cvt_pk_bf16_f32 v15, v80, v81
	ds_write_b128 v24, v[12:15] offset:0
	v_pk_mul_f32 v[82:83], v[82:83], s[44:45] op_sel_hi:[1,0]
	v_pk_mul_f32 v[84:85], v[84:85], s[44:45] op_sel_hi:[1,0]
	v_pk_mul_f32 v[86:87], v[86:87], s[44:45] op_sel_hi:[1,0]
	v_pk_mul_f32 v[88:89], v[88:89], s[44:45] op_sel_hi:[1,0]
	v_cvt_pk_bf16_f32 v16, v82, v83
	v_cvt_pk_bf16_f32 v17, v84, v85
	v_cvt_pk_bf16_f32 v18, v86, v87
	v_cvt_pk_bf16_f32 v19, v88, v89
	ds_write_b128 v25, v[16:19] offset:1024
	v_pk_mul_f32 v[90:91], v[90:91], s[44:45] op_sel_hi:[1,0]
	v_pk_mul_f32 v[92:93], v[92:93], s[44:45] op_sel_hi:[1,0]
	v_pk_mul_f32 v[94:95], v[94:95], s[44:45] op_sel_hi:[1,0]
	v_pk_mul_f32 v[96:97], v[96:97], s[44:45] op_sel_hi:[1,0]
	v_cvt_pk_bf16_f32 v20, v90, v91
	v_cvt_pk_bf16_f32 v21, v92, v93
	v_cvt_pk_bf16_f32 v22, v94, v95
	v_cvt_pk_bf16_f32 v23, v96, v97
	ds_write_b128 v24, v[20:23] offset:2048
	v_pk_mul_f32 v[98:99], v[98:99], s[44:45] op_sel_hi:[1,0]
	v_pk_mul_f32 v[100:101], v[100:101], s[44:45] op_sel_hi:[1,0]
	v_pk_mul_f32 v[102:103], v[102:103], s[44:45] op_sel_hi:[1,0]
	v_pk_mul_f32 v[104:105], v[104:105], s[44:45] op_sel_hi:[1,0]
	v_cvt_pk_bf16_f32 v12, v98, v99
	v_cvt_pk_bf16_f32 v13, v100, v101
	v_cvt_pk_bf16_f32 v14, v102, v103
	v_cvt_pk_bf16_f32 v15, v104, v105
	ds_write_b128 v25, v[12:15] offset:3072
	v_pk_mul_f32 v[106:107], v[106:107], s[44:45] op_sel_hi:[1,0]
	v_pk_mul_f32 v[108:109], v[108:109], s[44:45] op_sel_hi:[1,0]
	v_pk_mul_f32 v[110:111], v[110:111], s[44:45] op_sel_hi:[1,0]
	v_pk_mul_f32 v[112:113], v[112:113], s[44:45] op_sel_hi:[1,0]
	v_cvt_pk_bf16_f32 v16, v106, v107
	v_cvt_pk_bf16_f32 v17, v108, v109
	v_cvt_pk_bf16_f32 v18, v110, v111
	v_cvt_pk_bf16_f32 v19, v112, v113
	ds_write_b128 v24, v[16:19] offset:4096
	v_pk_mul_f32 v[114:115], v[114:115], s[44:45] op_sel_hi:[1,0]
	v_pk_mul_f32 v[116:117], v[116:117], s[44:45] op_sel_hi:[1,0]
	v_pk_mul_f32 v[118:119], v[118:119], s[44:45] op_sel_hi:[1,0]
	v_pk_mul_f32 v[120:121], v[120:121], s[44:45] op_sel_hi:[1,0]
	v_cvt_pk_bf16_f32 v20, v114, v115
	v_cvt_pk_bf16_f32 v21, v116, v117
	v_cvt_pk_bf16_f32 v22, v118, v119
	v_cvt_pk_bf16_f32 v23, v120, v121
	ds_write_b128 v25, v[20:23] offset:5120
	v_pk_mul_f32 v[122:123], v[122:123], s[44:45] op_sel_hi:[1,0]
	v_pk_mul_f32 v[124:125], v[124:125], s[44:45] op_sel_hi:[1,0]
	v_pk_mul_f32 v[126:127], v[126:127], s[44:45] op_sel_hi:[1,0]
	v_pk_mul_f32 v[128:129], v[128:129], s[44:45] op_sel_hi:[1,0]
	v_cvt_pk_bf16_f32 v12, v122, v123
	v_cvt_pk_bf16_f32 v13, v124, v125
	v_cvt_pk_bf16_f32 v14, v126, v127
	v_cvt_pk_bf16_f32 v15, v128, v129
	ds_write_b128 v24, v[12:15] offset:6144
	v_pk_mul_f32 v[130:131], v[130:131], s[44:45] op_sel_hi:[1,0]
	v_pk_mul_f32 v[132:133], v[132:133], s[44:45] op_sel_hi:[1,0]
	v_pk_mul_f32 v[134:135], v[134:135], s[44:45] op_sel_hi:[1,0]
	v_pk_mul_f32 v[136:137], v[136:137], s[44:45] op_sel_hi:[1,0]
	v_cvt_pk_bf16_f32 v16, v130, v131
	v_cvt_pk_bf16_f32 v17, v132, v133
	v_cvt_pk_bf16_f32 v18, v134, v135
	v_cvt_pk_bf16_f32 v19, v136, v137
	ds_write_b128 v25, v[16:19] offset:7168
	v_pk_mul_f32 v[138:139], v[138:139], s[44:45] op_sel_hi:[1,0]
	v_pk_mul_f32 v[140:141], v[140:141], s[44:45] op_sel_hi:[1,0]
	v_pk_mul_f32 v[142:143], v[142:143], s[44:45] op_sel_hi:[1,0]
	v_pk_mul_f32 v[144:145], v[144:145], s[44:45] op_sel_hi:[1,0]
	v_cvt_pk_bf16_f32 v20, v138, v139
	v_cvt_pk_bf16_f32 v21, v140, v141
	v_cvt_pk_bf16_f32 v22, v142, v143
	v_cvt_pk_bf16_f32 v23, v144, v145
	ds_write_b128 v24, v[20:23] offset:8192
	v_pk_mul_f32 v[146:147], v[146:147], s[44:45] op_sel_hi:[1,0]
	v_pk_mul_f32 v[148:149], v[148:149], s[44:45] op_sel_hi:[1,0]
	v_pk_mul_f32 v[150:151], v[150:151], s[44:45] op_sel_hi:[1,0]
	v_pk_mul_f32 v[152:153], v[152:153], s[44:45] op_sel_hi:[1,0]
	v_cvt_pk_bf16_f32 v12, v146, v147
	v_cvt_pk_bf16_f32 v13, v148, v149
	v_cvt_pk_bf16_f32 v14, v150, v151
	v_cvt_pk_bf16_f32 v15, v152, v153
	ds_write_b128 v25, v[12:15] offset:9216
	v_pk_mul_f32 v[154:155], v[154:155], s[44:45] op_sel_hi:[1,0]
	v_pk_mul_f32 v[156:157], v[156:157], s[44:45] op_sel_hi:[1,0]
	v_pk_mul_f32 v[158:159], v[158:159], s[44:45] op_sel_hi:[1,0]
	v_pk_mul_f32 v[160:161], v[160:161], s[44:45] op_sel_hi:[1,0]
	v_cvt_pk_bf16_f32 v16, v154, v155
	v_cvt_pk_bf16_f32 v17, v156, v157
	v_cvt_pk_bf16_f32 v18, v158, v159
	v_cvt_pk_bf16_f32 v19, v160, v161
	ds_write_b128 v24, v[16:19] offset:10240
	v_pk_mul_f32 v[162:163], v[162:163], s[44:45] op_sel_hi:[1,0]
	v_pk_mul_f32 v[164:165], v[164:165], s[44:45] op_sel_hi:[1,0]
	v_pk_mul_f32 v[166:167], v[166:167], s[44:45] op_sel_hi:[1,0]
	v_pk_mul_f32 v[168:169], v[168:169], s[44:45] op_sel_hi:[1,0]
	v_cvt_pk_bf16_f32 v20, v162, v163
	v_cvt_pk_bf16_f32 v21, v164, v165
	v_cvt_pk_bf16_f32 v22, v166, v167
	v_cvt_pk_bf16_f32 v23, v168, v169
	ds_write_b128 v25, v[20:23] offset:11264
	v_pk_mul_f32 v[170:171], v[170:171], s[44:45] op_sel_hi:[1,0]
	v_pk_mul_f32 v[172:173], v[172:173], s[44:45] op_sel_hi:[1,0]
	v_pk_mul_f32 v[174:175], v[174:175], s[44:45] op_sel_hi:[1,0]
	v_pk_mul_f32 v[176:177], v[176:177], s[44:45] op_sel_hi:[1,0]
	v_cvt_pk_bf16_f32 v12, v170, v171
	v_cvt_pk_bf16_f32 v13, v172, v173
	v_cvt_pk_bf16_f32 v14, v174, v175
	v_cvt_pk_bf16_f32 v15, v176, v177
	ds_write_b128 v24, v[12:15] offset:12288
	v_pk_mul_f32 v[178:179], v[178:179], s[44:45] op_sel_hi:[1,0]
	v_pk_mul_f32 v[180:181], v[180:181], s[44:45] op_sel_hi:[1,0]
	v_pk_mul_f32 v[182:183], v[182:183], s[44:45] op_sel_hi:[1,0]
	v_pk_mul_f32 v[184:185], v[184:185], s[44:45] op_sel_hi:[1,0]
	v_cvt_pk_bf16_f32 v16, v178, v179
	v_cvt_pk_bf16_f32 v17, v180, v181
	v_cvt_pk_bf16_f32 v18, v182, v183
	v_cvt_pk_bf16_f32 v19, v184, v185
	ds_write_b128 v25, v[16:19] offset:13312
	v_pk_mul_f32 v[186:187], v[186:187], s[44:45] op_sel_hi:[1,0]
	v_pk_mul_f32 v[188:189], v[188:189], s[44:45] op_sel_hi:[1,0]
	v_pk_mul_f32 v[190:191], v[190:191], s[44:45] op_sel_hi:[1,0]
	v_pk_mul_f32 v[192:193], v[192:193], s[44:45] op_sel_hi:[1,0]
	v_cvt_pk_bf16_f32 v20, v186, v187
	v_cvt_pk_bf16_f32 v21, v188, v189
	v_cvt_pk_bf16_f32 v22, v190, v191
	v_cvt_pk_bf16_f32 v23, v192, v193
	ds_write_b128 v24, v[20:23] offset:14336
	v_pk_mul_f32 v[194:195], v[194:195], s[44:45] op_sel_hi:[1,0]
	v_pk_mul_f32 v[196:197], v[196:197], s[44:45] op_sel_hi:[1,0]
	v_pk_mul_f32 v[198:199], v[198:199], s[44:45] op_sel_hi:[1,0]
	v_pk_mul_f32 v[200:201], v[200:201], s[44:45] op_sel_hi:[1,0]
	v_cvt_pk_bf16_f32 v12, v194, v195
	v_cvt_pk_bf16_f32 v13, v196, v197
	v_cvt_pk_bf16_f32 v14, v198, v199
	v_cvt_pk_bf16_f32 v15, v200, v201
	ds_write_b128 v25, v[12:15] offset:15360
	v_mov_b32_e32 v209, v41
	v_lshrrev_b32_e32 v29, 6, v0
	s_nop 0
	v_readfirstlane_b32 s50, v29
	s_mov_b32 s51, s30
	s_add_i32 s52, s24, s31
	s_mov_b32 s54, s32
	s_mov_b32 s55, s33
	s_mov_b32 s56, 0x8000
	s_lshl_b32 s43, s30, 16
	s_add_i32 s61, s28, s43
	s_add_i32 s43, s30, 1
	s_and_b32 s43, s43, 7
	s_lshl_b32 s43, s43, 16
	s_add_i32 s62, s28, s43
	s_add_i32 s43, s30, 7
	s_and_b32 s43, s43, 7
	s_lshl_b32 s43, s43, 16
	s_add_i32 s63, s28, s43
	s_add_i32 s63, s63, 0xc000
	s_add_i32 s58, s62, 0x4000
	s_mov_b32 s57, s62
	s_mov_b32 s59, 0xc000
	s_mov_b32 s60, 0x4000
	s_mov_b32 s64, s10
	s_mov_b32 s65, s11
	s_mov_b32 s66, 0x10000
	s_mov_b32 s67, 0x4000
	s_mov_b32 s68, 0xc000
	s_mov_b32 s69, 0x14000
	s_mov_b32 s70, 0x600df1a6
	s_mov_b32 s71, 0x145440
	s_mov_b32 s72, s46
	s_mov_b32 s73, s47
	s_mov_b32 s22, 0x600df1a6
	s_mov_b32 s23, 0x10000
	s_waitcnt vmcnt(0) lgkmcnt(0)
	v_cmp_eq_u32_e32 vcc, s22, v30
	s_cmp_eq_u64 vcc, exec
	s_cbranch_scc0 .LBB0_27

.LBB0_13:
	s_or_b64 exec, exec, s[0:1]
	v_bfe_u32 v3, v0, 5, 1
	v_lshlrev_b32_e32 v4, 8, v0
	v_and_b32_e32 v4, 0x1f00, v4
	v_and_b32_e32 v5, 7, v0
	v_bitop3_b32 v6, v3, v0, 7 bitop3:0x78
	v_lshl_or_b32 v64, v6, 4, v4
	v_bitop3_b32 v6, v3, v5, 2 bitop3:0x36
	v_lshl_or_b32 v65, v6, 4, v4
	v_bitop3_b32 v6, v3, v5, 4 bitop3:0x36
	v_bitop3_b32 v5, v3, v5, 6 bitop3:0x36
	v_lshl_or_b32 v66, v6, 4, v4
	v_lshl_or_b32 v67, v5, 4, v4
	v_and_b32_e32 v4, 3, v0
	v_lshlrev_b32_e32 v6, 4, v0
	v_lshlrev_b32_e32 v5, 3, v4
	v_and_b32_e32 v6, 0xc0, v6
	v_lshlrev_b32_e32 v8, 1, v0
	v_lshlrev_b32_e32 v9, 8, v3
	v_bfe_u32 v7, v0, 4, 2
	v_and_b32_e32 v8, 32, v8
	v_or3_b32 v5, v5, v9, v6
	s_mov_b32 s0, 0x8000
	v_or3_b32 v184, v5, v8, s0
	v_lshlrev_b32_e32 v5, 8, v7
	v_xor_b32_e32 v6, v7, v1
	s_cmp_lg_u32 0, -1
	v_lshl_or_b32 v222, v6, 4, v5
	v_bitop3_b32 v1, v7, v1, 4 bitop3:0x36
	s_mov_b32 m0, s29
	s_nop 0
	buffer_load_dwordx4 v222, s[12:15], s61 offen lds
	s_cselect_b32 s17, 0, 0
	v_lshl_or_b32 v223, v1, 4, v5
	s_add_i32 s20, s29, 0x400
	s_add_i32 s0, s61, 0x400
	s_mov_b32 m0, s20
	s_nop 0
	buffer_load_dwordx4 v223, s[12:15], s0 offen lds
	v_lshlrev_b32_e32 v0, 6, v0
	s_add_i32 s21, s29, 0x800
	s_add_i32 s0, s61, 0x800
	s_mov_b32 m0, s21
	s_nop 0
	buffer_load_dwordx4 v222, s[12:15], s0 offen lds
	v_and_b32_e32 v0, 0x700, v0
	v_lshlrev_b32_e32 v1, 6, v3
	v_lshlrev_b32_e32 v3, 4, v4
	s_add_i32 s22, s29, 0xc00
	s_add_i32 s1, s61, 0xc00
	s_mov_b32 m0, s22
	s_nop 0
	buffer_load_dwordx4 v223, s[12:15], s1 offen lds
	v_or3_b32 v196, v0, v1, v3
	s_add_i32 s2, s29, 0x8000
	s_mov_b32 m0, s2
	s_nop 0
	buffer_load_dwordx4 v196, s[4:7], s61 offen lds
	s_add_i32 s1, s2, 0x400
	s_add_i32 s3, s61, 0x80
	s_mov_b32 m0, s1
	s_nop 0
	buffer_load_dwordx4 v196, s[4:7], s3 offen lds
	s_add_i32 s1, s2, 0x800
	s_mov_b32 m0, s1
	s_nop 0
	buffer_load_dwordx4 v196, s[4:7], s0 offen lds
	s_add_i32 s0, s2, 0xc00
	s_add_i32 s1, s61, 0x880
	s_mov_b32 m0, s0
	s_nop 0
	buffer_load_dwordx4 v196, s[4:7], s1 offen lds
	s_add_i32 s3, s29, 0x4000
	s_add_i32 s19, s61, 0x4000
	s_mov_b32 m0, s3
	s_nop 0
	buffer_load_dwordx4 v222, s[12:15], s19 offen lds
	v_or_b32_e32 v2, 0x10000, v40
	v_add_u32_e32 v218, s17, v64
	v_add_u32_e32 v219, s17, v65
	v_add_u32_e32 v220, s17, v66
	v_add_u32_e32 v221, s17, v67
	s_add_i32 s10, s29, 0x4400
	s_add_i32 s0, s61, 0x4400
	s_mov_b32 m0, s10
	s_nop 0
	buffer_load_dwordx4 v223, s[12:15], s0 offen lds
	s_add_i32 s11, s29, 0x4800
	s_add_i32 s18, s61, 0x4800
	s_mov_b32 m0, s11
	s_nop 0
	buffer_load_dwordx4 v222, s[12:15], s18 offen lds
	v_add_u32_e32 v32, v2, v218
	v_add_u32_e32 v33, v2, v219
	v_add_u32_e32 v34, v2, v220
	v_add_u32_e32 v35, v2, v221
	s_add_i32 s16, s29, 0x4c00
	s_add_i32 s0, s61, 0x4c00
	s_mov_b32 m0, s16
	s_nop 0
	buffer_load_dwordx4 v223, s[12:15], s0 offen lds
	v_add_u32_e32 v212, s17, v184
	ds_read_b128 v[0:3], v32 offset:0
	ds_read_b128 v[4:7], v33 offset:0
	ds_read_b128 v[8:11], v34 offset:0
	ds_read_b128 v[12:15], v35 offset:0
	ds_read_b128 v[16:19], v32 offset:128
	ds_read_b128 v[20:23], v33 offset:128
	ds_read_b128 v[24:27], v34 offset:128
	ds_read_b128 v[28:31], v35 offset:128
	s_waitcnt lgkmcnt(0)
	v_accvgpr_write_b32 a[128], v0
	v_accvgpr_write_b32 a[129], v1
	v_accvgpr_write_b32 a[130], v2
	v_accvgpr_write_b32 a[131], v3
	v_accvgpr_write_b32 a[132], v4
	v_accvgpr_write_b32 a[133], v5
	v_accvgpr_write_b32 a[134], v6
	v_accvgpr_write_b32 a[135], v7
	v_accvgpr_write_b32 a[136], v8
	v_accvgpr_write_b32 a[137], v9
	v_accvgpr_write_b32 a[138], v10
	v_accvgpr_write_b32 a[139], v11
	v_accvgpr_write_b32 a[140], v12
	v_accvgpr_write_b32 a[141], v13
	v_accvgpr_write_b32 a[142], v14
	v_accvgpr_write_b32 a[143], v15
	v_accvgpr_write_b32 a[144], v16
	v_accvgpr_write_b32 a[145], v17
	v_accvgpr_write_b32 a[146], v18
	v_accvgpr_write_b32 a[147], v19
	v_accvgpr_write_b32 a[148], v20
	v_accvgpr_write_b32 a[149], v21
	v_accvgpr_write_b32 a[150], v22
	v_accvgpr_write_b32 a[151], v23
	v_accvgpr_write_b32 a[152], v24
	v_accvgpr_write_b32 a[153], v25
	v_accvgpr_write_b32 a[154], v26
	v_accvgpr_write_b32 a[155], v27
	v_accvgpr_write_b32 a[156], v28
	v_accvgpr_write_b32 a[157], v29
	v_accvgpr_write_b32 a[158], v30
	v_accvgpr_write_b32 a[159], v31
	ds_read_b128 v[0:3], v32 offset:8192
	ds_read_b128 v[4:7], v33 offset:8192
	ds_read_b128 v[8:11], v34 offset:8192
	ds_read_b128 v[12:15], v35 offset:8192
	ds_read_b128 v[16:19], v32 offset:8320
	ds_read_b128 v[20:23], v33 offset:8320
	ds_read_b128 v[24:27], v34 offset:8320
	ds_read_b128 v[28:31], v35 offset:8320
	s_waitcnt lgkmcnt(0)
	v_accvgpr_write_b32 a[160], v0
	v_accvgpr_write_b32 a[161], v1
	v_accvgpr_write_b32 a[162], v2
	v_accvgpr_write_b32 a[163], v3
	v_accvgpr_write_b32 a[164], v4
	v_accvgpr_write_b32 a[165], v5
	v_accvgpr_write_b32 a[166], v6
	v_accvgpr_write_b32 a[167], v7
	v_accvgpr_write_b32 a[168], v8
	v_accvgpr_write_b32 a[169], v9
	v_accvgpr_write_b32 a[170], v10
	v_accvgpr_write_b32 a[171], v11
	v_accvgpr_write_b32 a[172], v12
	v_accvgpr_write_b32 a[173], v13
	v_accvgpr_write_b32 a[174], v14
	v_accvgpr_write_b32 a[175], v15
	v_accvgpr_write_b32 a[176], v16
	v_accvgpr_write_b32 a[177], v17
	v_accvgpr_write_b32 a[178], v18
	v_accvgpr_write_b32 a[179], v19
	v_accvgpr_write_b32 a[180], v20
	v_accvgpr_write_b32 a[181], v21
	v_accvgpr_write_b32 a[182], v22
	v_accvgpr_write_b32 a[183], v23
	v_accvgpr_write_b32 a[184], v24
	v_accvgpr_write_b32 a[185], v25
	v_accvgpr_write_b32 a[186], v26
	v_accvgpr_write_b32 a[187], v27
	v_accvgpr_write_b32 a[188], v28
	v_accvgpr_write_b32 a[189], v29
	v_accvgpr_write_b32 a[190], v30
	v_accvgpr_write_b32 a[191], v31
	s_waitcnt vmcnt(0) lgkmcnt(0)
	s_barrier
	s_nop 0
	ds_read_b128 a[192:195], v218 offset:0
	s_nop 0
	ds_read_b128 a[196:199], v219 offset:0
	ds_read_b128 a[200:203], v220 offset:0
	ds_read_b128 a[204:207], v221 offset:0
	ds_read_b128 a[208:211], v218 offset:128
	ds_read_b128 a[212:215], v219 offset:128
	ds_read_b128 a[216:219], v220 offset:128
	ds_read_b128 a[220:223], v221 offset:128
	ds_read_b128 a[224:227], v218 offset:8192
	ds_read_b128 a[228:231], v219 offset:8192
	ds_read_b128 a[232:235], v220 offset:8192
	ds_read_b128 a[236:239], v221 offset:8192
	ds_read_b128 a[240:243], v218 offset:8320
	ds_read_b128 a[244:247], v219 offset:8320
	ds_read_b128 a[248:251], v220 offset:8320
	ds_read_b128 a[252:255], v221 offset:8320
	s_waitcnt lgkmcnt(0)
	v_mfma_f32_32x32x16_bf16 v[48:63], a[192:195], a[128:131], 0
	v_mfma_f32_32x32x16_bf16 v[32:47], a[192:195], a[160:163], 0
	v_mfma_f32_32x32x16_bf16 v[0:15], a[224:227], a[128:131], 0
	v_mfma_f32_32x32x16_bf16 v[16:31], a[224:227], a[160:163], 0
	v_mfma_f32_32x32x16_bf16 v[48:63], a[196:199], a[132:135], v[48:63]
	v_mfma_f32_32x32x16_bf16 v[32:47], a[196:199], a[164:167], v[32:47]
	v_mfma_f32_32x32x16_bf16 v[0:15], a[228:231], a[132:135], v[0:15]
	v_mfma_f32_32x32x16_bf16 v[16:31], a[228:231], a[164:167], v[16:31]
	v_mfma_f32_32x32x16_bf16 v[48:63], a[200:203], a[136:139], v[48:63]
	v_mfma_f32_32x32x16_bf16 v[32:47], a[200:203], a[168:171], v[32:47]
	v_mfma_f32_32x32x16_bf16 v[0:15], a[232:235], a[136:139], v[0:15]
	v_mfma_f32_32x32x16_bf16 v[16:31], a[232:235], a[168:171], v[16:31]
	v_mfma_f32_32x32x16_bf16 v[48:63], a[204:207], a[140:143], v[48:63]
	v_mfma_f32_32x32x16_bf16 v[32:47], a[204:207], a[172:175], v[32:47]
	v_mfma_f32_32x32x16_bf16 v[0:15], a[236:239], a[140:143], v[0:15]
	v_mfma_f32_32x32x16_bf16 v[16:31], a[236:239], a[172:175], v[16:31]
	v_mfma_f32_32x32x16_bf16 v[48:63], a[208:211], a[144:147], v[48:63]
	s_mov_b32 s27, s29
	v_mfma_f32_32x32x16_bf16 v[32:47], a[208:211], a[176:179], v[32:47]
	s_add_i32 s0, s62, 0x0
	s_mov_b32 s30, s0
	v_mfma_f32_32x32x16_bf16 v[0:15], a[240:243], a[144:147], v[0:15]
	s_mov_b32 s31, s20
	v_mfma_f32_32x32x16_bf16 v[16:31], a[240:243], a[176:179], v[16:31]
	s_add_i32 s33, s62, 0x400
	v_mfma_f32_32x32x16_bf16 v[48:63], a[212:215], a[148:151], v[48:63]
	s_mov_b32 s34, s21
	v_mfma_f32_32x32x16_bf16 v[32:47], a[212:215], a[180:183], v[32:47]
	s_add_i32 s1, s62, 0x800
	s_mov_b32 s35, s1
	v_mfma_f32_32x32x16_bf16 v[0:15], a[244:247], a[148:151], v[0:15]
	s_mov_b32 s36, s22
	v_mfma_f32_32x32x16_bf16 v[16:31], a[244:247], a[180:183], v[16:31]
	s_add_i32 s37, s62, 0xc00
	v_mfma_f32_32x32x16_bf16 v[48:63], a[216:219], a[152:155], v[48:63]
	s_add_i32 s23, s29, 0xc000
	s_mov_b32 s38, s23
	v_mfma_f32_32x32x16_bf16 v[32:47], a[216:219], a[184:187], v[32:47]
	v_mfma_f32_32x32x16_bf16 v[0:15], a[248:251], a[152:155], v[0:15]
	s_add_i32 s24, s29, 0xc400
	s_mov_b32 s39, s24
	v_mfma_f32_32x32x16_bf16 v[16:31], a[248:251], a[184:187], v[16:31]
	s_add_i32 s40, s61, 0x4080
	v_mfma_f32_32x32x16_bf16 v[48:63], a[220:223], a[156:159], v[48:63]
	s_add_i32 s25, s29, 0xc800
	s_mov_b32 s41, s25
	v_mfma_f32_32x32x16_bf16 v[32:47], a[220:223], a[188:191], v[32:47]
	v_mfma_f32_32x32x16_bf16 v[0:15], a[252:255], a[156:159], v[0:15]
	s_add_i32 s26, s29, 0xcc00
	s_mov_b32 s42, s26
	v_mfma_f32_32x32x16_bf16 v[16:31], a[252:255], a[188:191], v[16:31]
	s_add_i32 s43, s61, 0x4880
	s_nop 0
	s_nop 4
	s_waitcnt vmcnt(0) lgkmcnt(0)
	s_barrier
	s_nop 0
	s_mov_b32 m0, s27
	s_nop 0
	buffer_load_dwordx4 v222, s[12:15], s30 offen lds
	s_mov_b32 m0, s31
	s_nop 0
	buffer_load_dwordx4 v223, s[12:15], s33 offen lds
	s_addk_i32 s17, 0x4000
	v_add_u32_e32 v217, s17, v64
	ds_read_b128 a[192:195], v217 offset:0
	s_mov_b32 m0, s34
	s_nop 0
	buffer_load_dwordx4 v222, s[12:15], s35 offen lds
	v_add_u32_e32 v199, s17, v65
	ds_read_b128 a[196:199], v199 offset:0
	s_mov_b32 m0, s36
	s_nop 0
	buffer_load_dwordx4 v223, s[12:15], s37 offen lds
	v_add_u32_e32 v198, s17, v66
	ds_read_b128 a[200:203], v198 offset:0
	s_mov_b32 m0, s38
	s_nop 0
	buffer_load_dwordx4 v196, s[4:7], s19 offen lds
	v_add_u32_e32 v197, s17, v67
	ds_read_b128 a[204:207], v197 offset:0
	s_mov_b32 m0, s39
	s_nop 0
	buffer_load_dwordx4 v196, s[4:7], s40 offen lds
	ds_read_b128 a[208:211], v217 offset:128
	s_mov_b32 m0, s41
	s_nop 0
	buffer_load_dwordx4 v196, s[4:7], s18 offen lds
	ds_read_b128 a[212:215], v199 offset:128
	s_mov_b32 m0, s42
	s_nop 0
	buffer_load_dwordx4 v196, s[4:7], s43 offen lds
	ds_read_b128 a[216:219], v198 offset:128
	ds_read_b128 a[220:223], v197 offset:128
	v_cvt_pk_bf16_f32 v248, v248, v249
	v_cvt_pk_bf16_f32 v249, v250, v251
	v_cvt_pk_bf16_f32 v250, v252, v253
	v_cvt_pk_bf16_f32 v251, v254, v255
	buffer_store_dwordx4 v[248:251], v208, s[12:15], s56 offen sc1
	s_add_i32 s56, s56, 0x1000
	v_max3_f32 v64, v48, v49, v0
	v_max3_f32 v65, v50, v51, v1
	v_max3_f32 v64, v64, v2, v3
	ds_read_b128 a[224:227], v217 offset:8192
	v_max3_f32 v64, v64, v52, v53
	v_max3_f32 v65, v65, v54, v55
	v_max3_f32 v64, v64, v4, v5
	v_max3_f32 v65, v65, v6, v7
	ds_read_b128 a[228:231], v199 offset:8192
	v_max3_f32 v64, v64, v56, v57
	v_max3_f32 v65, v65, v58, v59
	v_max3_f32 v64, v64, v8, v9
	v_max3_f32 v65, v65, v10, v11
	ds_read_b128 a[232:235], v198 offset:8192
	v_max3_f32 v64, v64, v60, v61
	v_max3_f32 v65, v65, v62, v63
	v_max3_f32 v64, v64, v12, v13
	v_max3_f32 v65, v65, v14, v15
	ds_read_b128 a[236:239], v197 offset:8192
	v_max3_f32 v66, v32, v33, v16
	v_max3_f32 v67, v34, v35, v17
	v_max3_f32 v66, v66, v18, v19
	ds_read_b128 a[240:243], v217 offset:8320
	v_max3_f32 v66, v66, v36, v37
	v_max3_f32 v67, v67, v38, v39
	v_max3_f32 v66, v66, v20, v21
	v_max3_f32 v67, v67, v22, v23
	ds_read_b128 a[244:247], v199 offset:8320
	v_max3_f32 v66, v66, v40, v41
	v_max3_f32 v67, v67, v42, v43
	v_max3_f32 v66, v66, v24, v25
	v_max3_f32 v67, v67, v26, v27
	ds_read_b128 a[248:251], v198 offset:8320
	v_max3_f32 v66, v66, v44, v45
	v_max3_f32 v67, v67, v46, v47
	v_max3_f32 v66, v66, v28, v29
	v_max3_f32 v67, v67, v30, v31
	ds_read_b128 a[252:255], v197 offset:8320
	v_max_f32_e32 v64, v64, v65
	v_mov_b32_e32 v65, v64
	s_nop 1
	v_permlane32_swap_b32_e32 v64, v65
	v_max_f32_e32 v214, v64, v65
	v_max_f32_e32 v64, v66, v67
	v_mov_b32_e32 v65, v64
	s_nop 1
	v_permlane32_swap_b32_e32 v64, v65
	v_max_f32_e32 v213, v64, v65
	v_sub_f32_e32 v64, v0, v214
	v_mbcnt_lo_u32_b32 v0, -1, 0
	v_mbcnt_hi_u32_b32 v0, -1, v0
	v_sub_f32_e32 v65, v1, v214
	v_xor_b32_e32 v1, 0x80000000, v214
	v_cmp_gt_u32_e32 vcc, 32, v0
	v_sub_f32_e32 v128, v2, v214
	v_sub_f32_e32 v129, v3, v214
	v_sub_f32_e32 v130, v4, v214
	v_sub_f32_e32 v131, v5, v214
	v_sub_f32_e32 v132, v6, v214
	v_sub_f32_e32 v133, v7, v214
	v_sub_f32_e32 v134, v8, v214
	v_sub_f32_e32 v135, v9, v214
	v_sub_f32_e32 v136, v10, v214
	v_sub_f32_e32 v137, v11, v214
	v_sub_f32_e32 v138, v12, v214
	v_sub_f32_e32 v139, v13, v214
	v_sub_f32_e32 v140, v14, v214
	v_sub_f32_e32 v141, v15, v214
	v_sub_f32_e32 v142, v16, v213
	v_mov_b32_e32 v211, 1.0
	v_sub_f32_e32 v143, v17, v213
	v_xor_b32_e32 v17, 0x80000000, v213
	v_cndmask_b32_e64 v0, 0, 1.0, vcc
	s_nop 1
	v_mfma_f32_32x32x2_f32 v[0:15], v0, v1, 0
	v_mbcnt_lo_u32_b32 v16, -1, 0
	v_mbcnt_hi_u32_b32 v16, -1, v16
	v_sub_f32_e32 v48, v48, v214
	v_sub_f32_e32 v49, v49, v214
	v_sub_f32_e32 v50, v50, v214
	v_sub_f32_e32 v51, v51, v214
	v_sub_f32_e32 v52, v52, v214
	v_sub_f32_e32 v53, v53, v214
	v_sub_f32_e32 v54, v54, v214
	v_sub_f32_e32 v55, v55, v214
	v_sub_f32_e32 v56, v56, v214
	v_sub_f32_e32 v57, v57, v214
	v_sub_f32_e32 v58, v58, v214
	v_sub_f32_e32 v59, v59, v214
	v_sub_f32_e32 v60, v60, v214
	v_sub_f32_e32 v61, v61, v214
	v_sub_f32_e32 v62, v62, v214
	v_sub_f32_e32 v63, v63, v214
	v_sub_f32_e32 v32, v32, v213
	v_sub_f32_e32 v33, v33, v213
	v_sub_f32_e32 v34, v34, v213
	v_cmp_gt_u32_e32 vcc, 32, v16
	v_sub_f32_e32 v35, v35, v213
	v_sub_f32_e32 v36, v36, v213
	v_sub_f32_e32 v37, v37, v213
	v_sub_f32_e32 v38, v38, v213
	v_sub_f32_e32 v39, v39, v213
	v_sub_f32_e32 v40, v40, v213
	v_sub_f32_e32 v41, v41, v213
	v_sub_f32_e32 v42, v42, v213
	v_sub_f32_e32 v43, v43, v213
	v_sub_f32_e32 v44, v44, v213
	v_sub_f32_e32 v45, v45, v213
	v_sub_f32_e32 v46, v46, v213
	v_sub_f32_e32 v47, v47, v213
	v_sub_f32_e32 v144, v18, v213
	v_sub_f32_e32 v145, v19, v213
	v_sub_f32_e32 v146, v20, v213
	v_sub_f32_e32 v147, v21, v213
	v_sub_f32_e32 v183, v22, v213
	v_sub_f32_e32 v194, v23, v213
	v_cndmask_b32_e64 v16, 0, 1.0, vcc
	v_sub_f32_e32 v195, v24, v213
	v_sub_f32_e32 v215, v25, v213
	v_sub_f32_e32 v216, v26, v213
	v_sub_f32_e32 v224, v27, v213
	v_sub_f32_e32 v225, v28, v213
	v_sub_f32_e32 v226, v29, v213
	v_sub_f32_e32 v229, v30, v213
	v_sub_f32_e32 v230, v31, v213
	v_mfma_f32_32x32x2_f32 v[16:31], v16, v17, 0
	v_exp_f32_e32 v112, v48
	v_exp_f32_e32 v113, v49
	v_exp_f32_e32 v114, v50
	v_exp_f32_e32 v115, v51
	v_mov_b32_e32 v193, 0
	v_add_f32_e32 v48, v193, v112
	v_add_f32_e32 v49, v193, v113
	v_exp_f32_e32 v116, v52
	v_exp_f32_e32 v117, v53
	v_exp_f32_e32 v118, v54
	v_add_f32_e32 v48, v48, v114
	v_add_f32_e32 v49, v49, v115
	v_exp_f32_e32 v119, v55
	v_exp_f32_e32 v120, v56
	v_add_f32_e32 v48, v48, v116
	v_add_f32_e32 v49, v49, v117
	v_add_f32_e32 v48, v48, v118
	v_exp_f32_e32 v121, v57
	v_exp_f32_e32 v122, v58
	v_exp_f32_e32 v123, v59
	v_add_f32_e32 v49, v49, v119
	v_add_f32_e32 v48, v48, v120
	v_exp_f32_e32 v124, v60
	v_exp_f32_e32 v125, v61
	v_add_f32_e32 v49, v49, v121
	v_add_f32_e32 v48, v48, v122
	v_add_f32_e32 v49, v49, v123
	v_exp_f32_e32 v126, v62
	v_exp_f32_e32 v127, v63
	v_exp_f32_e32 v96, v32
	v_add_f32_e32 v32, v48, v124
	v_add_f32_e32 v48, v49, v125
	v_exp_f32_e32 v97, v33
	v_exp_f32_e32 v98, v34
	v_add_f32_e32 v231, v32, v126
	v_add_f32_e32 v232, v48, v127
	v_add_f32_e32 v32, v193, v96
	v_exp_f32_e32 v99, v35
	v_exp_f32_e32 v100, v36
	v_exp_f32_e32 v101, v37
	v_add_f32_e32 v33, v193, v97
	v_add_f32_e32 v32, v32, v98
	v_exp_f32_e32 v102, v38
	v_exp_f32_e32 v103, v39
	v_add_f32_e32 v33, v33, v99
	v_add_f32_e32 v32, v32, v100
	v_add_f32_e32 v33, v33, v101
	v_exp_f32_e32 v104, v40
	v_exp_f32_e32 v105, v41
	v_exp_f32_e32 v106, v42
	v_add_f32_e32 v32, v32, v102
	v_add_f32_e32 v33, v33, v103
	v_exp_f32_e32 v107, v43
	v_exp_f32_e32 v108, v44
	v_add_f32_e32 v32, v32, v104
	v_add_f32_e32 v33, v33, v105
	v_add_f32_e32 v32, v32, v106
	v_exp_f32_e32 v109, v45
	v_exp_f32_e32 v110, v46
	v_exp_f32_e32 v111, v47
	v_add_f32_e32 v33, v33, v107
	v_add_f32_e32 v32, v32, v108
	s_waitcnt lgkmcnt(0)
	v_add_f32_e32 v33, v33, v109
	v_add_f32_e32 v233, v32, v110
	v_add_f32_e32 v234, v33, v111
	v_mfma_f32_32x32x16_bf16 v[80:95], a[192:195], a[128:131], v[0:15]
	ds_read_b64_tr_b16 v[160:161], v212 offset:0
	v_exp_f32_e32 v235, v64
	v_exp_f32_e32 v236, v65
	v_cvt_pk_bf16_f32 v152, v112, v113
	v_mfma_f32_32x32x16_bf16 v[64:79], a[192:195], a[160:163], v[16:31]
	ds_read_b64_tr_b16 v[162:163], v212 offset:0x800
	v_exp_f32_e32 v237, v128
	v_exp_f32_e32 v238, v129
	v_cvt_pk_bf16_f32 v153, v114, v115
	v_exp_f32_e32 v115, v130
	v_mfma_f32_32x32x16_bf16 v[48:63], a[224:227], a[128:131], v[0:15]
	ds_read_b64_tr_b16 v[172:173], v212 offset:0x200
	v_exp_f32_e32 v239, v131
	v_cvt_pk_bf16_f32 v154, v116, v117
	v_mfma_f32_32x32x16_bf16 v[32:47], a[224:227], a[160:163], v[16:31]
	ds_read_b64_tr_b16 v[174:175], v212 offset:0xa00
	ds_read_b64_tr_b16 v[168:169], v212 offset:0x400
	v_exp_f32_e32 v240, v132
	v_exp_f32_e32 v241, v133
	v_cvt_pk_bf16_f32 v155, v118, v119
	v_exp_f32_e32 v185, v134
	v_exp_f32_e32 v186, v135
	v_mfma_f32_32x32x16_bf16 v[80:95], a[196:199], a[132:135], v[80:95]
	ds_read_b64_tr_b16 v[170:171], v212 offset:0xc00
	v_cvt_pk_bf16_f32 v128, v120, v121
	v_exp_f32_e32 v187, v136
	v_exp_f32_e32 v188, v137
	v_mfma_f32_32x32x16_bf16 v[64:79], a[196:199], a[164:167], v[64:79]
	ds_read_b64_tr_b16 v[176:177], v212 offset:0x600
	v_cvt_pk_bf16_f32 v129, v122, v123
	v_exp_f32_e32 v189, v138
	v_exp_f32_e32 v190, v139
	v_mfma_f32_32x32x16_bf16 v[48:63], a[228:231], a[132:135], v[48:63]
	ds_read_b64_tr_b16 v[178:179], v212 offset:0xe00
	v_cvt_pk_bf16_f32 v130, v124, v125
	v_mfma_f32_32x32x16_bf16 v[32:47], a[228:231], a[164:167], v[32:47]
	ds_read_b64_tr_b16 v[164:165], v212 offset:0x1000
	v_exp_f32_e32 v191, v140
	v_exp_f32_e32 v192, v141
	ds_read_b64_tr_b16 v[166:167], v212 offset:0x1800
	v_cvt_pk_bf16_f32 v131, v126, v127
	v_exp_f32_e32 v141, v142
	v_exp_f32_e32 v142, v143
	v_mfma_f32_32x32x16_bf16 v[80:95], a[200:203], a[136:139], v[80:95]
	ds_read_b64_tr_b16 v[156:157], v212 offset:0x1200
	v_cvt_pk_bf16_f32 v180, v96, v97
	v_exp_f32_e32 v143, v144
	v_mfma_f32_32x32x16_bf16 v[64:79], a[200:203], a[168:171], v[64:79]
	ds_read_b64_tr_b16 v[158:159], v212 offset:0x1a00
	v_exp_f32_e32 v242, v145
	v_cvt_pk_bf16_f32 v181, v98, v99
	v_mfma_f32_32x32x16_bf16 v[48:63], a[232:235], a[136:139], v[48:63]
	ds_read_b64_tr_b16 v[148:149], v212 offset:0x1400
	v_exp_f32_e32 v243, v146
	v_exp_f32_e32 v244, v147
	v_cvt_pk_bf16_f32 v182, v100, v101
	v_mfma_f32_32x32x16_bf16 v[32:47], a[232:235], a[168:171], v[32:47]
	ds_read_b64_tr_b16 v[150:151], v212 offset:0x1c00
	ds_read_b64_tr_b16 v[136:137], v212 offset:0x1600
	v_exp_f32_e32 v245, v183
	v_exp_f32_e32 v246, v194
	v_cvt_pk_bf16_f32 v183, v102, v103
	v_exp_f32_e32 v194, v195
	v_exp_f32_e32 v195, v215
	v_mfma_f32_32x32x16_bf16 v[80:95], a[204:207], a[140:143], v[80:95]
	ds_read_b64_tr_b16 v[138:139], v212 offset:0x1e00
	v_cvt_pk_bf16_f32 v144, v104, v105
	v_exp_f32_e32 v215, v216
	v_exp_f32_e32 v224, v224
	v_mfma_f32_32x32x16_bf16 v[64:79], a[204:207], a[172:175], v[64:79]
	ds_read_b64_tr_b16 v[132:133], v212 offset:0x2000
	v_cvt_pk_bf16_f32 v145, v106, v107
	v_exp_f32_e32 v227, v225
	v_exp_f32_e32 v228, v226
	v_mfma_f32_32x32x16_bf16 v[48:63], a[236:239], a[140:143], v[48:63]
	ds_read_b64_tr_b16 v[134:135], v212 offset:0x2800
	v_cvt_pk_bf16_f32 v146, v108, v109
	v_mfma_f32_32x32x16_bf16 v[32:47], a[236:239], a[172:175], v[32:47]
	ds_read_b64_tr_b16 v[124:125], v212 offset:0x2200
	v_exp_f32_e32 v229, v229
	v_exp_f32_e32 v230, v230
	ds_read_b64_tr_b16 v[126:127], v212 offset:0x2a00
	v_cvt_pk_bf16_f32 v147, v110, v111
	s_mov_b32 s27, s3
	v_mfma_f32_32x32x16_bf16 v[80:95], a[208:211], a[144:147], v[80:95]
	ds_read_b64_tr_b16 v[120:121], v212 offset:0x2400
	v_cvt_pk_bf16_f32 v112, v235, v236
	v_add_f32_e32 v96, v231, v235
	v_add_f32_e32 v97, v232, v236
	s_add_i32 s30, s62, 0x4000
	v_mfma_f32_32x32x16_bf16 v[64:79], a[208:211], a[176:179], v[64:79]
	ds_read_b64_tr_b16 v[122:123], v212 offset:0x2c00
	v_cvt_pk_bf16_f32 v113, v237, v238
	v_add_f32_e32 v96, v96, v237
	v_add_f32_e32 v97, v97, v238
	s_mov_b32 s31, s10
	v_mfma_f32_32x32x16_bf16 v[48:63], a[240:243], a[144:147], v[48:63]
	ds_read_b64_tr_b16 v[116:117], v212 offset:0x2600
	v_cvt_pk_bf16_f32 v114, v115, v239
	v_add_f32_e32 v96, v96, v115
	v_add_f32_e32 v97, v97, v239
	s_add_i32 s33, s62, 0x4400
	v_mfma_f32_32x32x16_bf16 v[32:47], a[240:243], a[176:179], v[32:47]
	ds_read_b64_tr_b16 v[118:119], v212 offset:0x2e00
	ds_read_b64_tr_b16 v[104:105], v212 offset:0x3000
	v_cvt_pk_bf16_f32 v115, v240, v241
	v_add_f32_e32 v96, v96, v240
	v_add_f32_e32 v97, v97, v241
	s_mov_b32 s34, s11
	v_mfma_f32_32x32x16_bf16 v[80:95], a[212:215], a[148:151], v[80:95]
	ds_read_b64_tr_b16 v[106:107], v212 offset:0x3800
	v_add_f32_e32 v96, v96, v185
	v_add_f32_e32 v97, v97, v186
	s_add_i32 s35, s62, 0x4800
	v_mfma_f32_32x32x16_bf16 v[64:79], a[212:215], a[180:183], v[64:79]
	ds_read_b64_tr_b16 v[108:109], v212 offset:0x3200
	v_add_f32_e32 v96, v96, v187
	v_add_f32_e32 v97, v97, v188
	s_mov_b32 s36, s16
	v_mfma_f32_32x32x16_bf16 v[48:63], a[244:247], a[148:151], v[48:63]
	ds_read_b64_tr_b16 v[110:111], v212 offset:0x3a00
	v_add_f32_e32 v96, v96, v189
	v_add_f32_e32 v97, v97, v190
	s_add_i32 s37, s62, 0x4c00
	v_mfma_f32_32x32x16_bf16 v[32:47], a[244:247], a[180:183], v[32:47]
	ds_read_b64_tr_b16 v[100:101], v212 offset:0x3400
	ds_read_b64_tr_b16 v[102:103], v212 offset:0x3c00
	v_add_f32_e32 v216, v96, v191
	v_add_f32_e32 v225, v97, v192
	s_mov_b32 s38, s2
	v_mfma_f32_32x32x16_bf16 v[80:95], a[216:219], a[152:155], v[80:95]
	ds_read_b64_tr_b16 v[96:97], v212 offset:0x3600
	v_cvt_pk_bf16_f32 v140, v141, v142
	v_add_f32_e32 v226, v233, v141
	v_add_f32_e32 v142, v234, v142
	v_mfma_f32_32x32x16_bf16 v[64:79], a[216:219], a[184:187], v[64:79]
	ds_read_b64_tr_b16 v[98:99], v212 offset:0x3e00
	v_cvt_pk_bf16_f32 v141, v143, v242
	v_add_f32_e32 v143, v226, v143
	v_add_f32_e32 v226, v142, v242
	v_mfma_f32_32x32x16_bf16 v[48:63], a[248:251], a[152:155], v[48:63]
	s_add_i32 s17, s29, 0x8400
	s_mov_b32 s39, s17
	v_cvt_pk_bf16_f32 v142, v243, v244
	v_add_f32_e32 v231, v143, v243
	v_add_f32_e32 v226, v226, v244
	v_mfma_f32_32x32x16_bf16 v[32:47], a[248:251], a[184:187], v[32:47]
	s_add_i32 s40, s62, 0x80
	v_cvt_pk_bf16_f32 v143, v245, v246
	v_add_f32_e32 v231, v231, v245
	v_add_f32_e32 v226, v226, v246
	v_mfma_f32_32x32x16_bf16 v[80:95], a[220:223], a[156:159], v[80:95]
	s_add_i32 s18, s29, 0x8800
	s_mov_b32 s41, s18
	v_add_f32_e32 v231, v231, v194
	v_add_f32_e32 v226, v226, v195
	v_mfma_f32_32x32x16_bf16 v[64:79], a[220:223], a[188:191], v[64:79]
	v_add_f32_e32 v231, v231, v215
	v_add_f32_e32 v226, v226, v224
	v_mfma_f32_32x32x16_bf16 v[48:63], a[252:255], a[156:159], v[48:63]
	s_add_i32 s19, s29, 0x8c00
	s_mov_b32 s42, s19
	v_add_f32_e32 v231, v231, v227
	v_add_f32_e32 v226, v226, v228
	v_mfma_f32_32x32x16_bf16 v[32:47], a[252:255], a[188:191], v[32:47]
	s_add_i32 s43, s62, 0x880
	v_add_f32_e32 v231, v231, v229
	v_add_f32_e32 v226, v226, v230
	s_nop 0
	s_nop 4
	v_add_f32_e32 v216, v216, v225
	s_waitcnt vmcnt(0) lgkmcnt(0)
	s_barrier
	s_nop 0
	v_mov_b32_e32 v225, v216
	s_nop 1
	v_permlane32_swap_b32_e32 v216, v225
	v_add_f32_e32 v216, v216, v225
	v_add_f32_e32 v225, v193, v216
	v_add_f32_e32 v216, v231, v226
	v_mov_b32_e32 v226, v216
	s_nop 1
	v_permlane32_swap_b32_e32 v216, v226
	v_add_f32_e32 v216, v216, v226
	v_add_f32_e32 v226, v193, v216
	v_mfma_f32_32x32x16_bf16 a[0:15], v[160:163], v[152:155], 0
	s_mov_b32 m0, s27
	s_nop 0
	buffer_load_dwordx4 v222, s[12:15], s30 offen lds
	v_mfma_f32_32x32x16_bf16 a[16:31], v[160:163], v[180:183], 0
	s_mov_b32 m0, s31
	s_nop 0
	buffer_load_dwordx4 v223, s[12:15], s33 offen lds
	ds_read_b128 a[192:195], v218 offset:0
	v_mfma_f32_32x32x16_bf16 a[32:47], v[172:175], v[152:155], 0
	s_mov_b32 m0, s34
	s_nop 0
	buffer_load_dwordx4 v222, s[12:15], s35 offen lds
	ds_read_b128 a[196:199], v219 offset:0
	v_mfma_f32_32x32x16_bf16 a[48:63], v[172:175], v[180:183], 0
	s_mov_b32 m0, s36
	s_nop 0
	buffer_load_dwordx4 v223, s[12:15], s37 offen lds
	ds_read_b128 a[200:203], v220 offset:0
	v_mfma_f32_32x32x16_bf16 a[64:79], v[168:171], v[152:155], 0
	s_mov_b32 m0, s38
	s_nop 0
	buffer_load_dwordx4 v196, s[4:7], s0 offen lds
	ds_read_b128 a[204:207], v221 offset:0
	v_mfma_f32_32x32x16_bf16 a[80:95], v[168:171], v[180:183], 0
	s_mov_b32 m0, s39
	s_nop 0
	buffer_load_dwordx4 v196, s[4:7], s40 offen lds
	ds_read_b128 a[208:211], v218 offset:128
	v_mfma_f32_32x32x16_bf16 a[96:111], v[176:179], v[152:155], 0
	s_mov_b32 m0, s41
	s_nop 0
	buffer_load_dwordx4 v196, s[4:7], s1 offen lds
	ds_read_b128 a[212:215], v219 offset:128
	v_mfma_f32_32x32x16_bf16 a[112:127], v[176:179], v[180:183], 0
	s_mov_b32 m0, s42
	s_nop 0
	buffer_load_dwordx4 v196, s[4:7], s43 offen lds
	ds_read_b128 a[216:219], v220 offset:128
	v_mfma_f32_32x32x16_bf16 a[0:15], v[164:167], v[128:131], a[0:15]
	ds_read_b128 a[220:223], v221 offset:128
	global_load_dwordx4 v[248:251], v207, s[54:55] nt
	global_load_dwordx4 v[252:255], v207, s[54:55] offset:16 nt
	s_add_u32 s54, s54, 0x2000
	s_addc_u32 s55, s55, 0
	v_max3_f32 v152, v80, v81, v48
	v_max3_f32 v153, v82, v83, v49
	v_max3_f32 v152, v152, v50, v51
	v_mfma_f32_32x32x16_bf16 a[16:31], v[164:167], v[144:147], a[16:31]
	ds_read_b128 a[224:227], v218 offset:8192
	v_max3_f32 v152, v152, v84, v85
	v_max3_f32 v153, v153, v86, v87
	v_max3_f32 v152, v152, v52, v53
	v_max3_f32 v153, v153, v54, v55
	v_mfma_f32_32x32x16_bf16 a[32:47], v[156:159], v[128:131], a[32:47]
	ds_read_b128 a[228:231], v219 offset:8192
	v_max3_f32 v152, v152, v88, v89
	v_max3_f32 v153, v153, v90, v91
	v_max3_f32 v152, v152, v56, v57
	v_max3_f32 v153, v153, v58, v59
	v_mfma_f32_32x32x16_bf16 a[48:63], v[156:159], v[144:147], a[48:63]
	ds_read_b128 a[232:235], v220 offset:8192
	v_max3_f32 v152, v152, v92, v93
	v_max3_f32 v153, v153, v94, v95
	v_max3_f32 v152, v152, v60, v61
	v_max3_f32 v153, v153, v62, v63
	v_mfma_f32_32x32x16_bf16 a[64:79], v[148:151], v[128:131], a[64:79]
	ds_read_b128 a[236:239], v221 offset:8192
	v_max3_f32 v154, v64, v65, v32
	v_max3_f32 v155, v66, v67, v33
	v_max3_f32 v154, v154, v34, v35
	v_mfma_f32_32x32x16_bf16 a[80:95], v[148:151], v[144:147], a[80:95]
	ds_read_b128 a[240:243], v218 offset:8320
	v_max3_f32 v148, v154, v68, v69
	v_max3_f32 v149, v155, v70, v71
	v_max3_f32 v148, v148, v36, v37
	v_max3_f32 v149, v149, v38, v39
	v_mfma_f32_32x32x16_bf16 a[96:111], v[136:139], v[128:131], a[96:111]
	ds_read_b128 a[244:247], v219 offset:8320
	v_max3_f32 v128, v148, v72, v73
	v_max3_f32 v129, v149, v74, v75
	v_max3_f32 v128, v128, v40, v41
	v_max3_f32 v129, v129, v42, v43
	v_mfma_f32_32x32x16_bf16 a[112:127], v[136:139], v[144:147], a[112:127]
	ds_read_b128 a[248:251], v220 offset:8320
	v_max3_f32 v128, v128, v76, v77
	v_max3_f32 v129, v129, v78, v79
	v_max3_f32 v128, v128, v44, v45
	v_max3_f32 v130, v129, v46, v47
	v_mfma_f32_32x32x16_bf16 a[0:15], v[132:135], v[112:115], a[0:15]
	ds_read_b128 a[252:255], v221 offset:8320
	v_max_f32_e32 v129, v152, v153
	v_mov_b32_e32 v131, v129
	s_nop 1
	v_permlane32_swap_b32_e32 v129, v131
	v_max_f32_e32 v129, v129, v131
	v_mfma_f32_32x32x16_bf16 a[16:31], v[132:135], v[140:143], a[16:31]
	v_max_f32_e32 v128, v128, v130
	v_mov_b32_e32 v130, v128
	s_nop 1
	v_permlane32_swap_b32_e32 v128, v130
	v_max_f32_e32 v128, v128, v130
	v_max_f32_e32 v130, v129, v129
	v_max_f32_e32 v131, v128, v128
	v_max_f32_e32 v130, v130, v131
	s_mov_b32 s0, 0x41000000
	v_mfma_f32_32x32x16_bf16 a[32:47], v[124:127], v[112:115], a[32:47]
	v_cmp_lt_f32_e32 vcc, s0, v130
	s_cmp_lg_u64 vcc, 0
	s_cselect_b64 s[0:1], -1, 0
	s_cbranch_vccnz .LBB0_41
	v_mov_b32_e32 v216, 1.0
.LBB0_15:
	v_cvt_pk_bf16_f32 v156, v185, v186
	v_cvt_pk_bf16_f32 v157, v187, v188
	v_cvt_pk_bf16_f32 v158, v189, v190
	v_cvt_pk_bf16_f32 v159, v191, v192
	v_cvt_pk_bf16_f32 v160, v194, v195
	v_cvt_pk_bf16_f32 v161, v215, v224
	v_cvt_pk_bf16_f32 v162, v227, v228
	v_cvt_pk_bf16_f32 v163, v229, v230
	v_exp_f32_e32 v128, v80
	v_exp_f32_e32 v129, v81
	v_mfma_f32_32x32x16_bf16 a[48:63], v[124:127], v[140:143], a[48:63]
	v_exp_f32_e32 v130, v82
	v_exp_f32_e32 v131, v83
	v_mfma_f32_32x32x16_bf16 a[64:79], v[120:123], v[112:115], a[64:79]
	v_mov_b32_e32 v224, 0
	v_add_f32_e32 v80, v224, v128
	v_add_f32_e32 v81, v224, v129
	v_exp_f32_e32 v132, v84
	v_exp_f32_e32 v133, v85
	v_exp_f32_e32 v134, v86
	v_mfma_f32_32x32x16_bf16 a[80:95], v[120:123], v[140:143], a[80:95]
	v_add_f32_e32 v80, v80, v130
	v_add_f32_e32 v81, v81, v131
	v_exp_f32_e32 v135, v87
	v_exp_f32_e32 v136, v88
	v_mfma_f32_32x32x16_bf16 a[96:111], v[116:119], v[112:115], a[96:111]
	v_add_f32_e32 v80, v80, v132
	v_add_f32_e32 v81, v81, v133
	v_add_f32_e32 v80, v80, v134
	v_exp_f32_e32 v137, v89
	v_exp_f32_e32 v138, v90
	v_exp_f32_e32 v139, v91
	v_mfma_f32_32x32x16_bf16 a[112:127], v[116:119], v[140:143], a[112:127]
	v_add_f32_e32 v81, v81, v135
	v_add_f32_e32 v80, v80, v136
	v_exp_f32_e32 v140, v92
	v_exp_f32_e32 v141, v93
	v_mfma_f32_32x32x16_bf16 a[0:15], v[104:107], v[156:159], a[0:15]
	v_add_f32_e32 v81, v81, v137
	v_add_f32_e32 v80, v80, v138
	v_add_f32_e32 v81, v81, v139
	v_exp_f32_e32 v142, v94
	v_exp_f32_e32 v143, v95
	v_exp_f32_e32 v144, v64
	v_mfma_f32_32x32x16_bf16 a[16:31], v[104:107], v[160:163], a[16:31]
	v_add_f32_e32 v64, v80, v140
	v_add_f32_e32 v80, v81, v141
	v_exp_f32_e32 v145, v65
	v_exp_f32_e32 v146, v66
	v_mfma_f32_32x32x16_bf16 a[32:47], v[108:111], v[156:159], a[32:47]
	v_add_f32_e32 v236, v64, v142
	v_add_f32_e32 v235, v80, v143
	v_add_f32_e32 v64, v224, v144
	v_exp_f32_e32 v147, v67
	v_exp_f32_e32 v148, v68
	v_exp_f32_e32 v149, v69
	v_mfma_f32_32x32x16_bf16 a[48:63], v[108:111], v[160:163], a[48:63]
	v_add_f32_e32 v65, v224, v145
	v_add_f32_e32 v64, v64, v146
	v_exp_f32_e32 v150, v70
	v_exp_f32_e32 v151, v71
	v_mfma_f32_32x32x16_bf16 a[64:79], v[100:103], v[156:159], a[64:79]
	v_add_f32_e32 v65, v65, v147
	v_add_f32_e32 v64, v64, v148
	v_add_f32_e32 v65, v65, v149
	v_exp_f32_e32 v152, v72
	v_exp_f32_e32 v153, v73
	v_exp_f32_e32 v154, v74
	v_mfma_f32_32x32x16_bf16 a[80:95], v[100:103], v[160:163], a[80:95]
	v_add_f32_e32 v64, v64, v150
	v_add_f32_e32 v65, v65, v151
	v_mfma_f32_32x32x16_bf16 a[96:111], v[96:99], v[156:159], a[96:111]
	v_exp_f32_e32 v155, v75
	v_exp_f32_e32 v156, v76
	v_add_f32_e32 v64, v64, v152
	v_add_f32_e32 v65, v65, v153
	v_add_f32_e32 v64, v64, v154
	v_exp_f32_e32 v157, v77
	v_exp_f32_e32 v158, v78
	v_exp_f32_e32 v159, v79
	v_mfma_f32_32x32x16_bf16 a[112:127], v[96:99], v[160:163], a[112:127]
	v_add_f32_e32 v65, v65, v155
	v_add_f32_e32 v64, v64, v156
	s_andn2_b64 vcc, exec, s[0:1]
	v_add_f32_e32 v65, v65, v157
	v_add_f32_e32 v237, v64, v158
	s_nop 0
	v_add_f32_e32 v238, v65, v159
	s_cbranch_vccz .LBB0_42

.LBB0_17:
	v_exp_f32_e32 v48, v48
	v_exp_f32_e32 v49, v49
	v_mfma_f32_32x32x16_bf16 v[112:127], a[192:195], a[128:131], v[0:15]
	ds_read_b64_tr_b16 v[172:173], v215 offset:0
	v_cvt_pk_bf16_f32 v164, v128, v129
	v_exp_f32_e32 v50, v50
	v_exp_f32_e32 v51, v51
	v_mfma_f32_32x32x16_bf16 v[96:111], a[192:195], a[160:163], v[16:31]
	ds_read_b64_tr_b16 v[174:175], v215 offset:0x800
	v_cvt_pk_bf16_f32 v165, v130, v131
	v_mfma_f32_32x32x16_bf16 v[80:95], a[224:227], a[128:131], v[0:15]
	ds_read_b64_tr_b16 v[184:185], v215 offset:0x200
	v_exp_f32_e32 v239, v52
	v_exp_f32_e32 v240, v53
	v_cvt_pk_bf16_f32 v166, v132, v133
	v_mfma_f32_32x32x16_bf16 v[64:79], a[224:227], a[160:163], v[16:31]
	ds_read_b64_tr_b16 v[186:187], v215 offset:0xa00
	ds_read_b64_tr_b16 v[180:181], v215 offset:0x400
	v_exp_f32_e32 v241, v54
	v_exp_f32_e32 v242, v55
	v_cvt_pk_bf16_f32 v167, v134, v135
	v_exp_f32_e32 v227, v56
	v_exp_f32_e32 v228, v57
	v_mfma_f32_32x32x16_bf16 v[112:127], a[196:199], a[132:135], v[112:127]
	ds_read_b64_tr_b16 v[182:183], v215 offset:0xc00
	v_cvt_pk_bf16_f32 v128, v136, v137
	v_exp_f32_e32 v229, v58
	v_exp_f32_e32 v230, v59
	v_mfma_f32_32x32x16_bf16 v[96:111], a[196:199], a[164:167], v[96:111]
	ds_read_b64_tr_b16 v[188:189], v215 offset:0x600
	v_cvt_pk_bf16_f32 v129, v138, v139
	v_exp_f32_e32 v231, v60
	v_exp_f32_e32 v232, v61
	v_mfma_f32_32x32x16_bf16 v[80:95], a[228:231], a[132:135], v[80:95]
	ds_read_b64_tr_b16 v[190:191], v215 offset:0xe00
	v_cvt_pk_bf16_f32 v130, v140, v141
	v_mfma_f32_32x32x16_bf16 v[64:79], a[228:231], a[164:167], v[64:79]
	ds_read_b64_tr_b16 v[176:177], v215 offset:0x1000
	v_exp_f32_e32 v233, v62
	v_exp_f32_e32 v234, v63
	ds_read_b64_tr_b16 v[178:179], v215 offset:0x1800
	v_cvt_pk_bf16_f32 v131, v142, v143
	v_exp_f32_e32 v141, v32
	v_exp_f32_e32 v142, v33
	v_mfma_f32_32x32x16_bf16 v[112:127], a[200:203], a[136:139], v[112:127]
	ds_read_b64_tr_b16 v[168:169], v215 offset:0x1200
	v_cvt_pk_bf16_f32 v192, v144, v145
	v_exp_f32_e32 v143, v34
	v_mfma_f32_32x32x16_bf16 v[96:111], a[200:203], a[168:171], v[96:111]
	ds_read_b64_tr_b16 v[170:171], v215 offset:0x1a00
	v_exp_f32_e32 v243, v35
	v_cvt_pk_bf16_f32 v193, v146, v147
	v_mfma_f32_32x32x16_bf16 v[80:95], a[232:235], a[136:139], v[80:95]
	ds_read_b64_tr_b16 v[160:161], v215 offset:0x1400
	v_exp_f32_e32 v244, v36
	v_exp_f32_e32 v245, v37
	v_cvt_pk_bf16_f32 v194, v148, v149
	v_mfma_f32_32x32x16_bf16 v[64:79], a[232:235], a[168:171], v[64:79]
	ds_read_b64_tr_b16 v[162:163], v215 offset:0x1c00
	ds_read_b64_tr_b16 v[136:137], v215 offset:0x1600
	v_exp_f32_e32 v246, v38
	v_exp_f32_e32 v247, v39
	v_cvt_pk_bf16_f32 v195, v150, v151
	v_exp_f32_e32 v148, v40
	v_exp_f32_e32 v149, v41
	v_mfma_f32_32x32x16_bf16 v[112:127], a[204:207], a[140:143], v[112:127]
	ds_read_b64_tr_b16 v[138:139], v215 offset:0x1e00
	v_cvt_pk_bf16_f32 v144, v152, v153
	v_exp_f32_e32 v150, v42
	v_exp_f32_e32 v151, v43
	v_mfma_f32_32x32x16_bf16 v[96:111], a[204:207], a[172:175], v[96:111]
	ds_read_b64_tr_b16 v[132:133], v215 offset:0x2000
	v_cvt_pk_bf16_f32 v145, v154, v155
	v_exp_f32_e32 v152, v44
	v_exp_f32_e32 v153, v45
	v_mfma_f32_32x32x16_bf16 v[80:95], a[236:239], a[140:143], v[80:95]
	ds_read_b64_tr_b16 v[134:135], v215 offset:0x2800
	v_cvt_pk_bf16_f32 v146, v156, v157
	v_mfma_f32_32x32x16_bf16 v[64:79], a[236:239], a[172:175], v[64:79]
	ds_read_b64_tr_b16 v[60:61], v215 offset:0x2200
	v_exp_f32_e32 v154, v46
	v_exp_f32_e32 v155, v47
	ds_read_b64_tr_b16 v[62:63], v215 offset:0x2a00
	v_cvt_pk_bf16_f32 v147, v158, v159
	s_mov_b32 s0, s29
	v_mfma_f32_32x32x16_bf16 v[112:127], a[208:211], a[144:147], v[112:127]
	ds_read_b64_tr_b16 v[56:57], v215 offset:0x2400
	v_cvt_pk_bf16_f32 v52, v48, v49
	v_add_f32_e32 v32, v236, v48
	v_add_f32_e32 v33, v235, v49
	s_add_i32 s57, s58, s59
	s_and_b32 s57, s57, 0x7ffff
	s_mov_b32 s33, s57
	s_mov_b32 s1, s33
	v_mfma_f32_32x32x16_bf16 v[96:111], a[208:211], a[176:179], v[96:111]
	ds_read_b64_tr_b16 v[58:59], v215 offset:0x2c00
	v_cvt_pk_bf16_f32 v53, v50, v51
	v_add_f32_e32 v32, v32, v50
	v_add_f32_e32 v33, v33, v51
	s_mov_b32 s35, s20
	v_mfma_f32_32x32x16_bf16 v[80:95], a[240:243], a[144:147], v[80:95]
	ds_read_b64_tr_b16 v[48:49], v215 offset:0x2600
	v_cvt_pk_bf16_f32 v54, v239, v240
	v_add_f32_e32 v32, v32, v239
	v_add_f32_e32 v33, v33, v240
	s_add_i32 s36, s57, 0x400
	v_mfma_f32_32x32x16_bf16 v[64:79], a[240:243], a[176:179], v[64:79]
	ds_read_b64_tr_b16 v[50:51], v215 offset:0x2e00
	ds_read_b64_tr_b16 v[44:45], v215 offset:0x3000
	v_cvt_pk_bf16_f32 v55, v241, v242
	v_add_f32_e32 v32, v32, v241
	v_add_f32_e32 v33, v33, v242
	s_mov_b32 s37, s21
	v_mfma_f32_32x32x16_bf16 v[112:127], a[212:215], a[148:151], v[112:127]
	ds_read_b64_tr_b16 v[46:47], v215 offset:0x3800
	v_add_f32_e32 v32, v32, v227
	v_add_f32_e32 v33, v33, v228
	s_add_i32 s34, s57, 0x800
	s_mov_b32 s38, s34
	v_mfma_f32_32x32x16_bf16 v[96:111], a[212:215], a[180:183], v[96:111]
	ds_read_b64_tr_b16 v[40:41], v215 offset:0x3200
	v_add_f32_e32 v32, v32, v229
	v_add_f32_e32 v33, v33, v230
	s_mov_b32 s39, s22
	v_mfma_f32_32x32x16_bf16 v[80:95], a[244:247], a[148:151], v[80:95]
	ds_read_b64_tr_b16 v[42:43], v215 offset:0x3a00
	v_add_f32_e32 v32, v32, v231
	v_add_f32_e32 v33, v33, v232
	s_add_i32 s40, s57, 0xc00
	v_mfma_f32_32x32x16_bf16 v[64:79], a[244:247], a[180:183], v[64:79]
	ds_read_b64_tr_b16 v[36:37], v215 offset:0x3400
	ds_read_b64_tr_b16 v[38:39], v215 offset:0x3c00
	v_add_f32_e32 v156, v32, v233
	v_add_f32_e32 v157, v33, v234
	s_mov_b32 s41, s23
	v_mfma_f32_32x32x16_bf16 v[112:127], a[216:219], a[152:155], v[112:127]
	ds_read_b64_tr_b16 v[32:33], v215 offset:0x3600
	v_cvt_pk_bf16_f32 v140, v141, v142
	v_add_f32_e32 v158, v237, v141
	v_add_f32_e32 v142, v238, v142
	s_mov_b32 s42, s58
	v_mfma_f32_32x32x16_bf16 v[96:111], a[216:219], a[184:187], v[96:111]
	ds_read_b64_tr_b16 v[34:35], v215 offset:0x3e00
	v_cvt_pk_bf16_f32 v141, v143, v243
	v_add_f32_e32 v143, v158, v143
	v_add_f32_e32 v158, v142, v243
	v_mfma_f32_32x32x16_bf16 v[80:95], a[248:251], a[152:155], v[80:95]
	s_mov_b32 s43, s24
	v_cvt_pk_bf16_f32 v142, v244, v245
	v_add_f32_e32 v159, v143, v244
	v_add_f32_e32 v158, v158, v245
	v_mfma_f32_32x32x16_bf16 v[64:79], a[248:251], a[184:187], v[64:79]
	s_add_i32 s44, s58, 0x80
	v_cvt_pk_bf16_f32 v143, v246, v247
	v_add_f32_e32 v159, v159, v246
	v_add_f32_e32 v158, v158, v247
	v_mfma_f32_32x32x16_bf16 v[112:127], a[220:223], a[156:159], v[112:127]
	s_mov_b32 s45, s25
	v_add_f32_e32 v159, v159, v148
	v_add_f32_e32 v158, v158, v149
	v_mfma_f32_32x32x16_bf16 v[96:111], a[220:223], a[188:191], v[96:111]
	s_add_i32 s46, s58, 0x800
	v_add_f32_e32 v159, v159, v150
	v_add_f32_e32 v158, v158, v151
	v_mfma_f32_32x32x16_bf16 v[80:95], a[252:255], a[156:159], v[80:95]
	s_mov_b32 s47, s26
	v_add_f32_e32 v159, v159, v152
	v_add_f32_e32 v158, v158, v153
	v_mfma_f32_32x32x16_bf16 v[64:79], a[252:255], a[188:191], v[64:79]
	s_add_i32 s48, s58, 0x880
	v_add_f32_e32 v159, v159, v154
	v_add_f32_e32 v158, v158, v155
	s_nop 0
	s_nop 4
	v_add_f32_e32 v156, v156, v157
	s_waitcnt vmcnt(0) lgkmcnt(0)
	s_barrier
	s_nop 0
	v_mov_b32_e32 v157, v156
	s_nop 1
	v_permlane32_swap_b32_e32 v156, v157
	v_add_f32_e32 v156, v156, v157
	v_add_f32_e32 v225, v225, v156
	v_add_f32_e32 v156, v159, v158
	v_mov_b32_e32 v157, v156
	s_nop 1
	v_permlane32_swap_b32_e32 v156, v157
	v_add_f32_e32 v156, v156, v157
	v_add_f32_e32 v226, v226, v156
	v_mfma_f32_32x32x16_bf16 a[0:15], v[172:175], v[164:167], a[0:15]
	s_mov_b32 m0, s0
	s_nop 0
	buffer_load_dwordx4 v222, s[12:15], s1 offen lds
	v_mfma_f32_32x32x16_bf16 a[16:31], v[172:175], v[192:195], a[16:31]
	s_mov_b32 m0, s35
	s_nop 0
	buffer_load_dwordx4 v223, s[12:15], s36 offen lds
	ds_read_b128 a[192:195], v217 offset:0
	v_mfma_f32_32x32x16_bf16 a[32:47], v[184:187], v[164:167], a[32:47]
	s_mov_b32 m0, s37
	s_nop 0
	buffer_load_dwordx4 v222, s[12:15], s38 offen lds
	ds_read_b128 a[196:199], v199 offset:0
	v_mfma_f32_32x32x16_bf16 a[48:63], v[184:187], v[192:195], a[48:63]
	s_mov_b32 m0, s39
	s_nop 0
	buffer_load_dwordx4 v223, s[12:15], s40 offen lds
	ds_read_b128 a[200:203], v198 offset:0
	v_mfma_f32_32x32x16_bf16 a[64:79], v[180:183], v[164:167], a[64:79]
	s_mov_b32 m0, s41
	s_nop 0
	buffer_load_dwordx4 v196, s[4:7], s42 offen lds
	ds_read_b128 a[204:207], v197 offset:0
	v_mfma_f32_32x32x16_bf16 a[80:95], v[180:183], v[192:195], a[80:95]
	s_mov_b32 m0, s43
	s_nop 0
	buffer_load_dwordx4 v196, s[4:7], s44 offen lds
	ds_read_b128 a[208:211], v217 offset:128
	v_mfma_f32_32x32x16_bf16 a[96:111], v[188:191], v[164:167], a[96:111]
	s_mov_b32 m0, s45
	s_nop 0
	buffer_load_dwordx4 v196, s[4:7], s46 offen lds
	ds_read_b128 a[212:215], v199 offset:128
	v_mfma_f32_32x32x16_bf16 a[112:127], v[188:191], v[192:195], a[112:127]
	s_mov_b32 m0, s47
	s_nop 0
	buffer_load_dwordx4 v196, s[4:7], s48 offen lds
	ds_read_b128 a[216:219], v198 offset:128
	s_nop 0
	v_mfma_f32_32x32x16_bf16 a[0:15], v[176:179], v[128:131], a[0:15]
	ds_read_b128 a[220:223], v197 offset:128
	s_cmp_gt_u32 s27, 12
	s_cbranch_scc1 .Lkc_skip_a
	v_cvt_pk_bf16_f32 v248, v248, v249
	v_cvt_pk_bf16_f32 v249, v250, v251
	v_cvt_pk_bf16_f32 v250, v252, v253
	v_cvt_pk_bf16_f32 v251, v254, v255
	buffer_store_dwordx4 v[248:251], v208, s[12:15], s56 offen sc1
	s_add_i32 s56, s56, 0x1000
.Lkc_skip_a:
	v_max3_f32 v156, v112, v113, v80
	v_max3_f32 v157, v114, v115, v81
	s_nop 0
	v_max3_f32 v156, v156, v82, v83
	v_mfma_f32_32x32x16_bf16 a[16:31], v[176:179], v[144:147], a[16:31]
	ds_read_b128 a[224:227], v217 offset:8192
	v_max3_f32 v156, v156, v116, v117
	v_max3_f32 v157, v157, v118, v119
	v_max3_f32 v156, v156, v84, v85
	v_max3_f32 v157, v157, v86, v87
	v_mfma_f32_32x32x16_bf16 a[32:47], v[168:171], v[128:131], a[32:47]
	ds_read_b128 a[228:231], v199 offset:8192
	v_max3_f32 v156, v156, v120, v121
	v_max3_f32 v157, v157, v122, v123
	v_max3_f32 v156, v156, v88, v89
	v_max3_f32 v157, v157, v90, v91
	v_mfma_f32_32x32x16_bf16 a[48:63], v[168:171], v[144:147], a[48:63]
	ds_read_b128 a[232:235], v198 offset:8192
	v_max3_f32 v156, v156, v124, v125
	v_max3_f32 v157, v157, v126, v127
	v_max3_f32 v156, v156, v92, v93
	v_max3_f32 v157, v157, v94, v95
	v_mfma_f32_32x32x16_bf16 a[64:79], v[160:163], v[128:131], a[64:79]
	ds_read_b128 a[236:239], v197 offset:8192
	v_max3_f32 v158, v96, v97, v64
	v_max3_f32 v159, v98, v99, v65
	v_max3_f32 v158, v158, v66, v67
	v_mfma_f32_32x32x16_bf16 a[80:95], v[160:163], v[144:147], a[80:95]
	ds_read_b128 a[240:243], v217 offset:8320
	v_max3_f32 v158, v158, v100, v101
	v_max3_f32 v159, v159, v102, v103
	v_max3_f32 v158, v158, v68, v69
	v_max3_f32 v159, v159, v70, v71
	v_mfma_f32_32x32x16_bf16 a[96:111], v[136:139], v[128:131], a[96:111]
	ds_read_b128 a[244:247], v199 offset:8320
	v_max3_f32 v128, v158, v104, v105
	v_max3_f32 v129, v159, v106, v107
	v_max3_f32 v128, v128, v72, v73
	v_max3_f32 v129, v129, v74, v75
	v_mfma_f32_32x32x16_bf16 a[112:127], v[136:139], v[144:147], a[112:127]
	ds_read_b128 a[248:251], v198 offset:8320
	v_max3_f32 v128, v128, v108, v109
	v_max3_f32 v129, v129, v110, v111
	v_max3_f32 v128, v128, v76, v77
	v_max3_f32 v130, v129, v78, v79
	v_mfma_f32_32x32x16_bf16 a[0:15], v[132:135], v[52:55], a[0:15]
	ds_read_b128 a[252:255], v197 offset:8320
	v_max_f32_e32 v129, v156, v157
	v_mov_b32_e32 v131, v129
	s_nop 1
	v_permlane32_swap_b32_e32 v129, v131
	v_max_f32_e32 v129, v129, v131
	v_mfma_f32_32x32x16_bf16 a[16:31], v[132:135], v[140:143], a[16:31]
	v_max_f32_e32 v128, v128, v130
	v_mov_b32_e32 v130, v128
	s_nop 1
	v_permlane32_swap_b32_e32 v128, v130
	v_max_f32_e32 v128, v128, v130
	v_max_f32_e32 v130, v129, v129
	v_max_f32_e32 v131, v128, v128
	v_max_f32_e32 v130, v130, v131
	v_mfma_f32_32x32x16_bf16 a[32:47], v[60:63], v[52:55], a[32:47]
	v_cmp_lt_f32_e32 vcc, s31, v130
	s_cmp_lg_u64 vcc, 0
	s_cselect_b64 s[0:1], -1, 0
	s_cbranch_vccnz .LBB0_22
.LBB0_18:
	v_cvt_pk_bf16_f32 v156, v227, v228
	v_cvt_pk_bf16_f32 v157, v229, v230
	v_cvt_pk_bf16_f32 v158, v231, v232
	v_cvt_pk_bf16_f32 v159, v233, v234
	v_cvt_pk_bf16_f32 v160, v148, v149
	v_cvt_pk_bf16_f32 v161, v150, v151
	v_cvt_pk_bf16_f32 v162, v152, v153
	v_cvt_pk_bf16_f32 v163, v154, v155
	v_exp_f32_e32 v128, v112
	v_exp_f32_e32 v129, v113
	v_mfma_f32_32x32x16_bf16 a[48:63], v[60:63], v[140:143], a[48:63]
	v_exp_f32_e32 v130, v114
	v_exp_f32_e32 v131, v115
	v_mfma_f32_32x32x16_bf16 a[64:79], v[56:59], v[52:55], a[64:79]
	v_add_f32_e32 v60, v224, v128
	v_add_f32_e32 v61, v224, v129
	v_exp_f32_e32 v132, v116
	v_exp_f32_e32 v133, v117
	v_exp_f32_e32 v134, v118
	v_mfma_f32_32x32x16_bf16 a[80:95], v[56:59], v[140:143], a[80:95]
	v_add_f32_e32 v56, v60, v130
	v_add_f32_e32 v57, v61, v131
	v_exp_f32_e32 v135, v119
	v_exp_f32_e32 v136, v120
	v_mfma_f32_32x32x16_bf16 a[96:111], v[48:51], v[52:55], a[96:111]
	v_add_f32_e32 v52, v56, v132
	v_add_f32_e32 v53, v57, v133
	v_add_f32_e32 v52, v52, v134
	v_exp_f32_e32 v137, v121
	v_exp_f32_e32 v138, v122
	v_exp_f32_e32 v139, v123
	v_mfma_f32_32x32x16_bf16 a[112:127], v[48:51], v[140:143], a[112:127]
	v_add_f32_e32 v48, v53, v135
	v_add_f32_e32 v49, v52, v136
	v_exp_f32_e32 v140, v124
	v_exp_f32_e32 v141, v125
	v_mfma_f32_32x32x16_bf16 a[0:15], v[44:47], v[156:159], a[0:15]
	v_add_f32_e32 v48, v48, v137
	v_add_f32_e32 v49, v49, v138
	v_add_f32_e32 v48, v48, v139
	v_exp_f32_e32 v142, v126
	v_exp_f32_e32 v143, v127
	v_exp_f32_e32 v144, v96
	v_mfma_f32_32x32x16_bf16 a[16:31], v[44:47], v[160:163], a[16:31]
	v_add_f32_e32 v44, v49, v140
	v_add_f32_e32 v45, v48, v141
	v_exp_f32_e32 v145, v97
	v_exp_f32_e32 v146, v98
	v_mfma_f32_32x32x16_bf16 a[32:47], v[40:43], v[156:159], a[32:47]
	v_add_f32_e32 v236, v44, v142
	v_add_f32_e32 v235, v45, v143
	v_add_f32_e32 v44, v224, v144
	v_exp_f32_e32 v147, v99
	v_exp_f32_e32 v148, v100
	v_exp_f32_e32 v149, v101
	v_mfma_f32_32x32x16_bf16 a[48:63], v[40:43], v[160:163], a[48:63]
	v_add_f32_e32 v40, v224, v145
	v_add_f32_e32 v41, v44, v146
	v_exp_f32_e32 v150, v102
	v_exp_f32_e32 v151, v103
	v_mfma_f32_32x32x16_bf16 a[64:79], v[36:39], v[156:159], a[64:79]
	v_add_f32_e32 v40, v40, v147
	v_add_f32_e32 v41, v41, v148
	v_add_f32_e32 v40, v40, v149
	v_exp_f32_e32 v152, v104
	v_exp_f32_e32 v153, v105
	v_exp_f32_e32 v154, v106
	v_mfma_f32_32x32x16_bf16 a[80:95], v[36:39], v[160:163], a[80:95]
	v_add_f32_e32 v36, v41, v150
	v_add_f32_e32 v37, v40, v151
	v_mfma_f32_32x32x16_bf16 a[96:111], v[32:35], v[156:159], a[96:111]
	v_exp_f32_e32 v155, v107
	v_exp_f32_e32 v156, v108
	v_add_f32_e32 v36, v36, v152
	v_add_f32_e32 v37, v37, v153
	v_add_f32_e32 v36, v36, v154
	v_exp_f32_e32 v157, v109
	v_exp_f32_e32 v158, v110
	v_exp_f32_e32 v159, v111
	v_mfma_f32_32x32x16_bf16 a[112:127], v[32:35], v[160:163], a[112:127]
	v_add_f32_e32 v32, v37, v155
	v_add_f32_e32 v33, v36, v156
	s_andn2_b64 vcc, exec, s[0:1]
	v_add_f32_e32 v32, v32, v157
	v_add_f32_e32 v237, v33, v158
	s_nop 0
	v_add_f32_e32 v238, v32, v159
	s_cbranch_vccz .LBB0_23
.LBB0_19:
	s_waitcnt lgkmcnt(0)
	v_exp_f32_e32 v80, v80
	v_exp_f32_e32 v81, v81
	v_mfma_f32_32x32x16_bf16 v[112:127], a[192:195], a[128:131], v[0:15]
	ds_read_b64_tr_b16 v[180:181], v212 offset:0
	v_cvt_pk_bf16_f32 v168, v128, v129
	v_exp_f32_e32 v82, v82
	v_exp_f32_e32 v83, v83
	v_mfma_f32_32x32x16_bf16 v[96:111], a[192:195], a[160:163], v[16:31]
	ds_read_b64_tr_b16 v[182:183], v212 offset:0x800
	v_cvt_pk_bf16_f32 v169, v130, v131
	v_mfma_f32_32x32x16_bf16 v[48:63], a[224:227], a[128:131], v[0:15]
	ds_read_b64_tr_b16 v[184:185], v212 offset:0x200
	v_exp_f32_e32 v239, v84
	v_exp_f32_e32 v240, v85
	v_cvt_pk_bf16_f32 v170, v132, v133
	v_mfma_f32_32x32x16_bf16 v[32:47], a[224:227], a[160:163], v[16:31]
	ds_read_b64_tr_b16 v[186:187], v212 offset:0xa00
	ds_read_b64_tr_b16 v[176:177], v212 offset:0x400
	v_exp_f32_e32 v241, v86
	v_exp_f32_e32 v242, v87
	v_cvt_pk_bf16_f32 v171, v134, v135
	v_exp_f32_e32 v227, v88
	v_exp_f32_e32 v228, v89
	v_mfma_f32_32x32x16_bf16 v[112:127], a[196:199], a[132:135], v[112:127]
	ds_read_b64_tr_b16 v[178:179], v212 offset:0xc00
	v_cvt_pk_bf16_f32 v128, v136, v137
	v_exp_f32_e32 v229, v90
	v_exp_f32_e32 v230, v91
	v_mfma_f32_32x32x16_bf16 v[96:111], a[196:199], a[164:167], v[96:111]
	ds_read_b64_tr_b16 v[188:189], v212 offset:0x600
	v_cvt_pk_bf16_f32 v129, v138, v139
	v_exp_f32_e32 v231, v92
	v_exp_f32_e32 v232, v93
	v_mfma_f32_32x32x16_bf16 v[48:63], a[228:231], a[132:135], v[48:63]
	ds_read_b64_tr_b16 v[190:191], v212 offset:0xe00
	v_cvt_pk_bf16_f32 v130, v140, v141
	v_mfma_f32_32x32x16_bf16 v[32:47], a[228:231], a[164:167], v[32:47]
	ds_read_b64_tr_b16 v[172:173], v212 offset:0x1000
	v_exp_f32_e32 v233, v94
	v_exp_f32_e32 v234, v95
	ds_read_b64_tr_b16 v[174:175], v212 offset:0x1800
	v_cvt_pk_bf16_f32 v131, v142, v143
	v_exp_f32_e32 v141, v64
	v_exp_f32_e32 v142, v65
	v_mfma_f32_32x32x16_bf16 v[112:127], a[200:203], a[136:139], v[112:127]
	ds_read_b64_tr_b16 v[164:165], v212 offset:0x1200
	v_cvt_pk_bf16_f32 v192, v144, v145
	v_exp_f32_e32 v143, v66
	v_mfma_f32_32x32x16_bf16 v[96:111], a[200:203], a[168:171], v[96:111]
	ds_read_b64_tr_b16 v[166:167], v212 offset:0x1a00
	v_exp_f32_e32 v243, v67
	v_cvt_pk_bf16_f32 v193, v146, v147
	v_mfma_f32_32x32x16_bf16 v[48:63], a[232:235], a[136:139], v[48:63]
	ds_read_b64_tr_b16 v[160:161], v212 offset:0x1400
	v_exp_f32_e32 v244, v68
	v_exp_f32_e32 v245, v69
	v_cvt_pk_bf16_f32 v194, v148, v149
	v_mfma_f32_32x32x16_bf16 v[32:47], a[232:235], a[168:171], v[32:47]
	ds_read_b64_tr_b16 v[162:163], v212 offset:0x1c00
	ds_read_b64_tr_b16 v[136:137], v212 offset:0x1600
	v_exp_f32_e32 v246, v70
	v_exp_f32_e32 v247, v71
	v_cvt_pk_bf16_f32 v195, v150, v151
	v_exp_f32_e32 v148, v72
	v_exp_f32_e32 v149, v73
	v_mfma_f32_32x32x16_bf16 v[112:127], a[204:207], a[140:143], v[112:127]
	ds_read_b64_tr_b16 v[138:139], v212 offset:0x1e00
	v_cvt_pk_bf16_f32 v144, v152, v153
	v_exp_f32_e32 v150, v74
	v_exp_f32_e32 v151, v75
	v_mfma_f32_32x32x16_bf16 v[96:111], a[204:207], a[172:175], v[96:111]
	ds_read_b64_tr_b16 v[132:133], v212 offset:0x2000
	v_cvt_pk_bf16_f32 v145, v154, v155
	v_exp_f32_e32 v152, v76
	v_exp_f32_e32 v153, v77
	v_mfma_f32_32x32x16_bf16 v[48:63], a[236:239], a[140:143], v[48:63]
	ds_read_b64_tr_b16 v[134:135], v212 offset:0x2800
	v_cvt_pk_bf16_f32 v146, v156, v157
	v_mfma_f32_32x32x16_bf16 v[32:47], a[236:239], a[172:175], v[32:47]
	ds_read_b64_tr_b16 v[92:93], v212 offset:0x2200
	v_exp_f32_e32 v154, v78
	v_exp_f32_e32 v155, v79
	ds_read_b64_tr_b16 v[94:95], v212 offset:0x2a00
	v_cvt_pk_bf16_f32 v147, v158, v159
	s_mov_b32 s0, s3
	v_mfma_f32_32x32x16_bf16 v[112:127], a[208:211], a[144:147], v[112:127]
	ds_read_b64_tr_b16 v[88:89], v212 offset:0x2400
	v_cvt_pk_bf16_f32 v84, v80, v81
	v_add_f32_e32 v64, v236, v80
	v_add_f32_e32 v65, v235, v81
	s_add_i32 s58, s57, s60
	s_and_b32 s58, s58, 0x7ffff
	s_mov_b32 s1, s58
	v_mfma_f32_32x32x16_bf16 v[96:111], a[208:211], a[176:179], v[96:111]
	ds_read_b64_tr_b16 v[90:91], v212 offset:0x2c00
	v_cvt_pk_bf16_f32 v85, v82, v83
	v_add_f32_e32 v64, v64, v82
	v_add_f32_e32 v65, v65, v83
	s_mov_b32 s35, s10
	v_mfma_f32_32x32x16_bf16 v[48:63], a[240:243], a[144:147], v[48:63]
	ds_read_b64_tr_b16 v[80:81], v212 offset:0x2600
	v_cvt_pk_bf16_f32 v86, v239, v240
	v_add_f32_e32 v64, v64, v239
	v_add_f32_e32 v65, v65, v240
	s_add_i32 s36, s58, 0x400
	v_mfma_f32_32x32x16_bf16 v[32:47], a[240:243], a[176:179], v[32:47]
	ds_read_b64_tr_b16 v[82:83], v212 offset:0x2e00
	ds_read_b64_tr_b16 v[76:77], v212 offset:0x3000
	v_cvt_pk_bf16_f32 v87, v241, v242
	v_add_f32_e32 v64, v64, v241
	v_add_f32_e32 v65, v65, v242
	s_mov_b32 s37, s11
	v_mfma_f32_32x32x16_bf16 v[112:127], a[212:215], a[148:151], v[112:127]
	ds_read_b64_tr_b16 v[78:79], v212 offset:0x3800
	v_add_f32_e32 v64, v64, v227
	v_add_f32_e32 v65, v65, v228
	s_add_i32 s38, s58, 0x800
	v_mfma_f32_32x32x16_bf16 v[96:111], a[212:215], a[180:183], v[96:111]
	ds_read_b64_tr_b16 v[72:73], v212 offset:0x3200
	v_add_f32_e32 v64, v64, v229
	v_add_f32_e32 v65, v65, v230
	s_mov_b32 s39, s16
	v_mfma_f32_32x32x16_bf16 v[48:63], a[244:247], a[148:151], v[48:63]
	ds_read_b64_tr_b16 v[74:75], v212 offset:0x3a00
	v_add_f32_e32 v64, v64, v231
	v_add_f32_e32 v65, v65, v232
	s_add_i32 s40, s58, 0xc00
	v_mfma_f32_32x32x16_bf16 v[32:47], a[244:247], a[180:183], v[32:47]
	ds_read_b64_tr_b16 v[68:69], v212 offset:0x3400
	ds_read_b64_tr_b16 v[70:71], v212 offset:0x3c00
	v_add_f32_e32 v156, v64, v233
	v_add_f32_e32 v157, v65, v234
	s_mov_b32 s41, s2
	v_mfma_f32_32x32x16_bf16 v[112:127], a[216:219], a[152:155], v[112:127]
	ds_read_b64_tr_b16 v[64:65], v212 offset:0x3600
	v_cvt_pk_bf16_f32 v140, v141, v142
	v_add_f32_e32 v158, v237, v141
	v_add_f32_e32 v142, v238, v142
	v_mfma_f32_32x32x16_bf16 v[96:111], a[216:219], a[184:187], v[96:111]
	ds_read_b64_tr_b16 v[66:67], v212 offset:0x3e00
	v_cvt_pk_bf16_f32 v141, v143, v243
	v_add_f32_e32 v143, v158, v143
	v_add_f32_e32 v158, v142, v243
	v_mfma_f32_32x32x16_bf16 v[48:63], a[248:251], a[152:155], v[48:63]
	s_mov_b32 s42, s17
	v_cvt_pk_bf16_f32 v142, v244, v245
	v_add_f32_e32 v159, v143, v244
	v_add_f32_e32 v158, v158, v245
	v_mfma_f32_32x32x16_bf16 v[32:47], a[248:251], a[184:187], v[32:47]
	s_add_i32 s43, s57, 0x80
	v_cvt_pk_bf16_f32 v143, v246, v247
	v_add_f32_e32 v159, v159, v246
	v_add_f32_e32 v158, v158, v247
	v_mfma_f32_32x32x16_bf16 v[112:127], a[220:223], a[156:159], v[112:127]
	s_mov_b32 s44, s18
	v_add_f32_e32 v159, v159, v148
	v_add_f32_e32 v158, v158, v149
	v_mfma_f32_32x32x16_bf16 v[96:111], a[220:223], a[188:191], v[96:111]
	v_add_f32_e32 v159, v159, v150
	v_add_f32_e32 v158, v158, v151
	v_mfma_f32_32x32x16_bf16 v[48:63], a[252:255], a[156:159], v[48:63]
	s_mov_b32 s45, s19
	v_add_f32_e32 v159, v159, v152
	v_add_f32_e32 v158, v158, v153
	v_mfma_f32_32x32x16_bf16 v[32:47], a[252:255], a[188:191], v[32:47]
	s_add_i32 s46, s57, 0x880
	v_add_f32_e32 v159, v159, v154
	v_add_f32_e32 v158, v158, v155
	s_nop 0
	s_nop 4
	v_add_f32_e32 v156, v156, v157
	s_waitcnt vmcnt(0) lgkmcnt(0)
	s_barrier
	s_nop 0
	v_mov_b32_e32 v157, v156
	s_nop 1
	v_permlane32_swap_b32_e32 v156, v157
	v_add_f32_e32 v156, v156, v157
	v_add_f32_e32 v225, v225, v156
	v_add_f32_e32 v156, v159, v158
	v_mov_b32_e32 v157, v156
	s_nop 1
	v_permlane32_swap_b32_e32 v156, v157
	v_add_f32_e32 v156, v156, v157
	v_add_f32_e32 v226, v226, v156
	v_mfma_f32_32x32x16_bf16 a[0:15], v[180:183], v[168:171], a[0:15]
	s_mov_b32 m0, s0
	s_nop 0
	buffer_load_dwordx4 v222, s[12:15], s1 offen lds
	v_mfma_f32_32x32x16_bf16 a[16:31], v[180:183], v[192:195], a[16:31]
	s_mov_b32 m0, s35
	s_nop 0
	buffer_load_dwordx4 v223, s[12:15], s36 offen lds
	ds_read_b128 a[192:195], v218 offset:0
	v_mfma_f32_32x32x16_bf16 a[32:47], v[184:187], v[168:171], a[32:47]
	s_mov_b32 m0, s37
	s_nop 0
	buffer_load_dwordx4 v222, s[12:15], s38 offen lds
	ds_read_b128 a[196:199], v219 offset:0
	v_mfma_f32_32x32x16_bf16 a[48:63], v[184:187], v[192:195], a[48:63]
	s_mov_b32 m0, s39
	s_nop 0
	buffer_load_dwordx4 v223, s[12:15], s40 offen lds
	ds_read_b128 a[200:203], v220 offset:0
	v_mfma_f32_32x32x16_bf16 a[64:79], v[176:179], v[168:171], a[64:79]
	s_mov_b32 m0, s41
	s_nop 0
	buffer_load_dwordx4 v196, s[4:7], s33 offen lds
	ds_read_b128 a[204:207], v221 offset:0
	v_mfma_f32_32x32x16_bf16 a[80:95], v[176:179], v[192:195], a[80:95]
	s_mov_b32 m0, s42
	s_nop 0
	buffer_load_dwordx4 v196, s[4:7], s43 offen lds
	ds_read_b128 a[208:211], v218 offset:128
	v_mfma_f32_32x32x16_bf16 a[96:111], v[188:191], v[168:171], a[96:111]
	s_mov_b32 m0, s44
	s_nop 0
	buffer_load_dwordx4 v196, s[4:7], s34 offen lds
	ds_read_b128 a[212:215], v219 offset:128
	v_mfma_f32_32x32x16_bf16 a[112:127], v[188:191], v[192:195], a[112:127]
	s_mov_b32 m0, s45
	s_nop 0
	buffer_load_dwordx4 v196, s[4:7], s46 offen lds
	ds_read_b128 a[216:219], v220 offset:128
	s_nop 0
	v_mfma_f32_32x32x16_bf16 a[0:15], v[172:175], v[128:131], a[0:15]
	ds_read_b128 a[220:223], v221 offset:128
	s_cmp_gt_u32 s27, 10
	s_cbranch_scc1 .Lkc_skip_b
	global_load_dwordx4 v[248:251], v207, s[54:55] nt
	global_load_dwordx4 v[252:255], v207, s[54:55] offset:16 nt
	s_add_u32 s54, s54, 0x2000
	s_addc_u32 s55, s55, 0
.Lkc_skip_b:
	v_max3_f32 v156, v112, v113, v48
	v_max3_f32 v157, v114, v115, v49
	s_nop 0
	v_max3_f32 v156, v156, v50, v51
	v_mfma_f32_32x32x16_bf16 a[16:31], v[172:175], v[144:147], a[16:31]
	ds_read_b128 a[224:227], v218 offset:8192
	v_max3_f32 v156, v156, v116, v117
	v_max3_f32 v157, v157, v118, v119
	v_max3_f32 v156, v156, v52, v53
	v_max3_f32 v157, v157, v54, v55
	v_mfma_f32_32x32x16_bf16 a[32:47], v[164:167], v[128:131], a[32:47]
	ds_read_b128 a[228:231], v219 offset:8192
	v_max3_f32 v156, v156, v120, v121
	v_max3_f32 v157, v157, v122, v123
	v_max3_f32 v156, v156, v56, v57
	v_max3_f32 v157, v157, v58, v59
	v_mfma_f32_32x32x16_bf16 a[48:63], v[164:167], v[144:147], a[48:63]
	ds_read_b128 a[232:235], v220 offset:8192
	v_max3_f32 v156, v156, v124, v125
	v_max3_f32 v157, v157, v126, v127
	v_max3_f32 v156, v156, v60, v61
	v_max3_f32 v157, v157, v62, v63
	v_mfma_f32_32x32x16_bf16 a[64:79], v[160:163], v[128:131], a[64:79]
	ds_read_b128 a[236:239], v221 offset:8192
	v_max3_f32 v158, v96, v97, v32
	v_max3_f32 v159, v98, v99, v33
	v_max3_f32 v158, v158, v34, v35
	v_mfma_f32_32x32x16_bf16 a[80:95], v[160:163], v[144:147], a[80:95]
	ds_read_b128 a[240:243], v218 offset:8320
	v_max3_f32 v158, v158, v100, v101
	v_max3_f32 v159, v159, v102, v103
	v_max3_f32 v158, v158, v36, v37
	v_max3_f32 v159, v159, v38, v39
	v_mfma_f32_32x32x16_bf16 a[96:111], v[136:139], v[128:131], a[96:111]
	ds_read_b128 a[244:247], v219 offset:8320
	v_max3_f32 v128, v158, v104, v105
	v_max3_f32 v129, v159, v106, v107
	v_max3_f32 v128, v128, v40, v41
	v_max3_f32 v129, v129, v42, v43
	v_mfma_f32_32x32x16_bf16 a[112:127], v[136:139], v[144:147], a[112:127]
	ds_read_b128 a[248:251], v220 offset:8320
	v_max3_f32 v128, v128, v108, v109
	v_max3_f32 v129, v129, v110, v111
	v_max3_f32 v128, v128, v44, v45
	v_max3_f32 v130, v129, v46, v47
	v_mfma_f32_32x32x16_bf16 a[0:15], v[132:135], v[84:87], a[0:15]
	ds_read_b128 a[252:255], v221 offset:8320
	v_max_f32_e32 v129, v156, v157
	v_mov_b32_e32 v131, v129
	s_nop 1
	v_permlane32_swap_b32_e32 v129, v131
	v_max_f32_e32 v129, v129, v131
	v_mfma_f32_32x32x16_bf16 a[16:31], v[132:135], v[140:143], a[16:31]
	v_max_f32_e32 v128, v128, v130
	v_mov_b32_e32 v130, v128
	s_nop 1
	v_permlane32_swap_b32_e32 v128, v130
	v_max_f32_e32 v128, v128, v130
	v_max_f32_e32 v130, v129, v129
	v_max_f32_e32 v131, v128, v128
	v_max_f32_e32 v130, v130, v131
	v_mfma_f32_32x32x16_bf16 a[32:47], v[92:95], v[84:87], a[32:47]
	v_cmp_lt_f32_e32 vcc, s31, v130
	s_cmp_lg_u64 vcc, 0
	s_cselect_b64 s[0:1], -1, 0
	s_cbranch_vccnz .LBB0_24
.LBB0_20:
	v_cvt_pk_bf16_f32 v156, v227, v228
	v_cvt_pk_bf16_f32 v157, v229, v230
	v_cvt_pk_bf16_f32 v158, v231, v232
	v_cvt_pk_bf16_f32 v159, v233, v234
	v_cvt_pk_bf16_f32 v160, v148, v149
	v_cvt_pk_bf16_f32 v161, v150, v151
	v_cvt_pk_bf16_f32 v162, v152, v153
	v_cvt_pk_bf16_f32 v163, v154, v155
	v_exp_f32_e32 v128, v112
	v_exp_f32_e32 v129, v113
	v_mfma_f32_32x32x16_bf16 a[48:63], v[92:95], v[140:143], a[48:63]
	v_exp_f32_e32 v130, v114
	v_exp_f32_e32 v131, v115
	v_mfma_f32_32x32x16_bf16 a[64:79], v[88:91], v[84:87], a[64:79]
	v_add_f32_e32 v92, v224, v128
	v_add_f32_e32 v93, v224, v129
	v_exp_f32_e32 v132, v116
	v_exp_f32_e32 v133, v117
	v_exp_f32_e32 v134, v118
	v_mfma_f32_32x32x16_bf16 a[80:95], v[88:91], v[140:143], a[80:95]
	v_add_f32_e32 v88, v92, v130
	v_add_f32_e32 v89, v93, v131
	v_exp_f32_e32 v135, v119
	v_exp_f32_e32 v136, v120
	v_mfma_f32_32x32x16_bf16 a[96:111], v[80:83], v[84:87], a[96:111]
	v_add_f32_e32 v84, v88, v132
	v_add_f32_e32 v85, v89, v133
	v_add_f32_e32 v84, v84, v134
	v_exp_f32_e32 v137, v121
	v_exp_f32_e32 v138, v122
	v_exp_f32_e32 v139, v123
	v_mfma_f32_32x32x16_bf16 a[112:127], v[80:83], v[140:143], a[112:127]
	v_add_f32_e32 v80, v85, v135
	v_add_f32_e32 v81, v84, v136
	v_exp_f32_e32 v140, v124
	v_exp_f32_e32 v141, v125
	v_mfma_f32_32x32x16_bf16 a[0:15], v[76:79], v[156:159], a[0:15]
	v_add_f32_e32 v80, v80, v137
	v_add_f32_e32 v81, v81, v138
	v_add_f32_e32 v80, v80, v139
	v_exp_f32_e32 v142, v126
	v_exp_f32_e32 v143, v127
	v_exp_f32_e32 v144, v96
	v_mfma_f32_32x32x16_bf16 a[16:31], v[76:79], v[160:163], a[16:31]
	v_add_f32_e32 v76, v81, v140
	v_add_f32_e32 v77, v80, v141
	v_exp_f32_e32 v145, v97
	v_exp_f32_e32 v146, v98
	v_mfma_f32_32x32x16_bf16 a[32:47], v[72:75], v[156:159], a[32:47]
	v_add_f32_e32 v236, v76, v142
	v_add_f32_e32 v235, v77, v143
	v_add_f32_e32 v76, v224, v144
	v_exp_f32_e32 v147, v99
	v_exp_f32_e32 v148, v100
	v_exp_f32_e32 v149, v101
	v_mfma_f32_32x32x16_bf16 a[48:63], v[72:75], v[160:163], a[48:63]
	v_add_f32_e32 v72, v224, v145
	v_add_f32_e32 v73, v76, v146
	v_exp_f32_e32 v150, v102
	v_exp_f32_e32 v151, v103
	v_mfma_f32_32x32x16_bf16 a[64:79], v[68:71], v[156:159], a[64:79]
	v_add_f32_e32 v72, v72, v147
	v_add_f32_e32 v73, v73, v148
	v_add_f32_e32 v72, v72, v149
	v_exp_f32_e32 v152, v104
	v_exp_f32_e32 v153, v105
	v_exp_f32_e32 v154, v106
	v_mfma_f32_32x32x16_bf16 a[80:95], v[68:71], v[160:163], a[80:95]
	v_add_f32_e32 v68, v73, v150
	v_add_f32_e32 v69, v72, v151
	v_mfma_f32_32x32x16_bf16 a[96:111], v[64:67], v[156:159], a[96:111]
	v_exp_f32_e32 v155, v107
	v_exp_f32_e32 v156, v108
	v_add_f32_e32 v68, v68, v152
	v_add_f32_e32 v69, v69, v153
	v_add_f32_e32 v68, v68, v154
	v_exp_f32_e32 v157, v109
	v_exp_f32_e32 v158, v110
	v_exp_f32_e32 v159, v111
	v_mfma_f32_32x32x16_bf16 a[112:127], v[64:67], v[160:163], a[112:127]
	v_add_f32_e32 v64, v69, v155
	v_add_f32_e32 v65, v68, v156
	s_andn2_b64 vcc, exec, s[0:1]
	v_add_f32_e32 v64, v64, v157
	v_add_f32_e32 v237, v65, v158
	s_nop 0
	v_add_f32_e32 v238, v64, v159
	s_cbranch_vccz .LBB0_25
.LBB0_21:
	s_waitcnt lgkmcnt(0)
	s_add_i32 s27, s27, 2
	s_cmp_gt_u32 s27, 10
	s_cselect_b32 s60, s66, s67
	s_cselect_b32 s59, s66, s68
	s_bitcmp1_b32 s71, s27
	s_cbranch_scc1 .Ltail_events
.Ltail_resume:
	s_cmp_gt_u32 s27, 27
	s_cbranch_scc0 .LBB0_17
	s_branch .LBB0_36
.Ltail_events:
	s_cmp_eq_u32 s27, 6
	s_cbranch_scc1 .Ltail_pub2
	s_cmp_eq_u32 s27, 14
	s_cbranch_scc1 .Ltail_pub3
	s_cmp_eq_u32 s27, 10
	s_cbranch_scc1 .Ltail_smp2
	s_cmp_eq_u32 s27, 18
	s_cbranch_scc1 .Ltail_smp3
	s_mov_b32 s59, s69
	s_mov_b32 s53, 0x10000
	s_cmp_eq_u32 s27, 12
	s_cbranch_scc0 .Ltail_chk3
.Ltail_chk2:
	v_cmp_ne_u32_e32 vcc, s70, v210
	s_cmp_lg_u64 vcc, 0
	s_cbranch_scc0 .Ltail_resume
	s_sleep 8
	global_load_dword v210, v209, s[64:65] offset:1024 sc1
	s_waitcnt vmcnt(0)
	s_add_i32 s53, s53, -1
	s_cmp_eq_u32 s53, 0
	s_cbranch_scc0 .Ltail_chk2
	s_branch .Ltail_resume
.Ltail_chk3:
	v_cmp_ne_u32_e32 vcc, s70, v210
	s_cmp_lg_u64 vcc, 0
	s_cbranch_scc0 .Ltail_resume
	s_sleep 8
	global_load_dword v210, v209, s[64:65] offset:2048 sc1
	s_waitcnt vmcnt(0)
	s_add_i32 s53, s53, -1
	s_cmp_eq_u32 s53, 0
	s_cbranch_scc0 .Ltail_chk3
	s_branch .Ltail_resume
.Ltail_smp2:
	global_load_dword v210, v209, s[64:65] offset:1024 sc1
	s_branch .Ltail_resume
.Ltail_smp3:
	global_load_dword v210, v209, s[64:65] offset:2048 sc1
	s_branch .Ltail_resume
.Ltail_pub2:
	s_cmp_eq_u32 s50, 0
	s_cbranch_scc0 .Ltail_resume
	v_mov_b32_e32 v210, s70
	s_mov_b64 exec, 1
	global_store_dword v209, v210, s[72:73] offset:1024 sc1
	s_mov_b64 exec, -1
	s_branch .Ltail_resume
.Ltail_pub3:
	s_cmp_eq_u32 s50, 0
	s_cbranch_scc0 .Ltail_resume
	v_mov_b32_e32 v210, s70
	s_mov_b64 exec, 1
	global_store_dword v209, v210, s[72:73] offset:2048 sc1
	s_mov_b64 exec, -1
	s_branch .Ltail_resume

.LBB0_36:
	s_lshl_b32 s53, s50, 6
	s_add_i32 s53, s53, s52
	v_mov_b32_e32 v200, s53
	s_lshl_b32 s53, s50, 14
	s_add_i32 s53, s53, 0x10000
	v_mov_b32_e32 v201, s53
	v_mbcnt_lo_u32_b32 v204, -1, 0
	v_mbcnt_hi_u32_b32 v204, -1, v204
	v_lshrrev_b32_e32 v202, 4, v204
	v_add_u32_e32 v203, 4, v202
	v_add_u32_e32 v205, 8, v202
	v_add_u32_e32 v206, 12, v202
	v_add_u32_e32 v207, 16, v202
	v_add_u32_e32 v208, 20, v202
	v_add_u32_e32 v209, 24, v202
	v_add_u32_e32 v210, 28, v202
	v_exp_f32_e32 v48, v48
	v_exp_f32_e32 v49, v49
	v_mfma_f32_32x32x16_bf16 v[112:127], a[192:195], a[128:131], v[0:15]
	ds_read_b64_tr_b16 v[180:181], v215 offset:0
	v_cvt_pk_bf16_f32 v164, v128, v129
	v_exp_f32_e32 v50, v50
	v_exp_f32_e32 v51, v51
	v_mfma_f32_32x32x16_bf16 v[96:111], a[192:195], a[160:163], v[16:31]
	ds_read_b64_tr_b16 v[182:183], v215 offset:0x800
	v_cvt_pk_bf16_f32 v165, v130, v131
	v_exp_f32_e32 v218, v52
	v_exp_f32_e32 v219, v53
	v_mfma_f32_32x32x16_bf16 v[80:95], a[224:227], a[128:131], v[0:15]
	ds_read_b64_tr_b16 v[188:189], v215 offset:0x200
	v_cvt_pk_bf16_f32 v166, v132, v133
	v_mfma_f32_32x32x16_bf16 v[64:79], a[224:227], a[160:163], v[16:31]
	ds_read_b64_tr_b16 v[190:191], v215 offset:0xa00
	ds_read_b64_tr_b16 v[176:177], v215 offset:0x400
	v_exp_f32_e32 v230, v54
	v_exp_f32_e32 v231, v55
	v_cvt_pk_bf16_f32 v167, v134, v135
	v_exp_f32_e32 v220, v56
	v_exp_f32_e32 v221, v57
	v_mfma_f32_32x32x16_bf16 v[112:127], a[196:199], a[132:135], v[112:127]
	ds_read_b64_tr_b16 v[178:179], v215 offset:0xc00
	v_cvt_pk_bf16_f32 v128, v136, v137
	v_exp_f32_e32 v222, v58
	v_exp_f32_e32 v223, v59
	v_mfma_f32_32x32x16_bf16 v[96:111], a[196:199], a[164:167], v[96:111]
	ds_read_b64_tr_b16 v[184:185], v215 offset:0x600
	v_cvt_pk_bf16_f32 v129, v138, v139
	v_exp_f32_e32 v224, v60
	v_exp_f32_e32 v227, v61
	v_mfma_f32_32x32x16_bf16 v[80:95], a[228:231], a[132:135], v[80:95]
	ds_read_b64_tr_b16 v[186:187], v215 offset:0xe00
	v_cvt_pk_bf16_f32 v130, v140, v141
	v_mfma_f32_32x32x16_bf16 v[64:79], a[228:231], a[164:167], v[64:79]
	ds_read_b64_tr_b16 v[172:173], v215 offset:0x1000
	v_exp_f32_e32 v228, v62
	v_exp_f32_e32 v229, v63
	ds_read_b64_tr_b16 v[174:175], v215 offset:0x1800
	v_cvt_pk_bf16_f32 v131, v142, v143
	v_exp_f32_e32 v141, v32
	v_exp_f32_e32 v142, v33
	v_mfma_f32_32x32x16_bf16 v[112:127], a[200:203], a[136:139], v[112:127]
	ds_read_b64_tr_b16 v[168:169], v215 offset:0x1200
	v_cvt_pk_bf16_f32 v192, v144, v145
	v_exp_f32_e32 v143, v34
	v_mfma_f32_32x32x16_bf16 v[96:111], a[200:203], a[168:171], v[96:111]
	ds_read_b64_tr_b16 v[170:171], v215 offset:0x1a00
	v_exp_f32_e32 v232, v35
	v_cvt_pk_bf16_f32 v193, v146, v147
	v_mfma_f32_32x32x16_bf16 v[80:95], a[232:235], a[136:139], v[80:95]
	ds_read_b64_tr_b16 v[160:161], v215 offset:0x1400
	v_exp_f32_e32 v233, v36
	v_exp_f32_e32 v234, v37
	v_cvt_pk_bf16_f32 v194, v148, v149
	v_mfma_f32_32x32x16_bf16 v[64:79], a[232:235], a[168:171], v[64:79]
	ds_read_b64_tr_b16 v[162:163], v215 offset:0x1c00
	ds_read_b64_tr_b16 v[136:137], v215 offset:0x1600
	v_exp_f32_e32 v239, v38
	v_exp_f32_e32 v240, v39
	v_cvt_pk_bf16_f32 v195, v150, v151
	v_exp_f32_e32 v148, v40
	v_exp_f32_e32 v149, v41
	v_mfma_f32_32x32x16_bf16 v[112:127], a[204:207], a[140:143], v[112:127]
	ds_read_b64_tr_b16 v[138:139], v215 offset:0x1e00
	v_cvt_pk_bf16_f32 v144, v152, v153
	v_exp_f32_e32 v150, v42
	v_exp_f32_e32 v151, v43
	v_mfma_f32_32x32x16_bf16 v[96:111], a[204:207], a[172:175], v[96:111]
	ds_read_b64_tr_b16 v[132:133], v215 offset:0x2000
	v_cvt_pk_bf16_f32 v145, v154, v155
	v_exp_f32_e32 v152, v44
	v_exp_f32_e32 v153, v45
	v_mfma_f32_32x32x16_bf16 v[80:95], a[236:239], a[140:143], v[80:95]
	ds_read_b64_tr_b16 v[134:135], v215 offset:0x2800
	v_cvt_pk_bf16_f32 v146, v156, v157
	v_mfma_f32_32x32x16_bf16 v[64:79], a[236:239], a[172:175], v[64:79]
	ds_read_b64_tr_b16 v[60:61], v215 offset:0x2200
	v_exp_f32_e32 v154, v46
	v_exp_f32_e32 v155, v47
	ds_read_b64_tr_b16 v[62:63], v215 offset:0x2a00
	v_cvt_pk_bf16_f32 v147, v158, v159
	v_mfma_f32_32x32x16_bf16 v[112:127], a[208:211], a[144:147], v[112:127]
	ds_read_b64_tr_b16 v[56:57], v215 offset:0x2400
	v_cvt_pk_bf16_f32 v52, v48, v49
	v_add_f32_e32 v32, v236, v48
	v_add_f32_e32 v33, v235, v49
	s_add_i32 s12, s28, 0x80000
	s_mov_b32 s0, s12
	v_mfma_f32_32x32x16_bf16 v[96:111], a[208:211], a[176:179], v[96:111]
	ds_read_b64_tr_b16 v[58:59], v215 offset:0x2c00
	v_cvt_pk_bf16_f32 v53, v50, v51
	v_add_f32_e32 v32, v32, v50
	v_add_f32_e32 v33, v33, v51
	v_mfma_f32_32x32x16_bf16 v[80:95], a[240:243], a[144:147], v[80:95]
	ds_read_b64_tr_b16 v[48:49], v215 offset:0x2600
	v_cvt_pk_bf16_f32 v54, v218, v219
	v_add_f32_e32 v32, v32, v218
	v_add_f32_e32 v33, v33, v219
	s_add_i32 s1, s28, 0x80400
	v_mfma_f32_32x32x16_bf16 v[64:79], a[240:243], a[176:179], v[64:79]
	ds_read_b64_tr_b16 v[50:51], v215 offset:0x2e00
	ds_read_b64_tr_b16 v[44:45], v215 offset:0x3000
	v_cvt_pk_bf16_f32 v55, v230, v231
	v_add_f32_e32 v32, v32, v230
	v_add_f32_e32 v33, v33, v231
	v_mfma_f32_32x32x16_bf16 v[112:127], a[212:215], a[148:151], v[112:127]
	ds_read_b64_tr_b16 v[46:47], v215 offset:0x3800
	v_add_f32_e32 v32, v32, v220
	v_add_f32_e32 v33, v33, v221
	s_add_i32 s13, s28, 0x80800
	s_mov_b32 s14, s13
	v_mfma_f32_32x32x16_bf16 v[96:111], a[212:215], a[180:183], v[96:111]
	ds_read_b64_tr_b16 v[40:41], v215 offset:0x3200
	v_add_f32_e32 v32, v32, v222
	v_add_f32_e32 v33, v33, v223
	v_mfma_f32_32x32x16_bf16 v[80:95], a[244:247], a[148:151], v[80:95]
	ds_read_b64_tr_b16 v[42:43], v215 offset:0x3a00
	v_add_f32_e32 v32, v32, v224
	v_add_f32_e32 v33, v33, v227
	s_add_i32 s15, s28, 0x80c00
	v_mfma_f32_32x32x16_bf16 v[64:79], a[244:247], a[180:183], v[64:79]
	ds_read_b64_tr_b16 v[36:37], v215 offset:0x3400
	ds_read_b64_tr_b16 v[38:39], v215 offset:0x3c00
	v_add_f32_e32 v156, v32, v228
	v_add_f32_e32 v157, v33, v229
	v_mfma_f32_32x32x16_bf16 v[112:127], a[216:219], a[152:155], v[112:127]
	ds_read_b64_tr_b16 v[32:33], v215 offset:0x3600
	v_cvt_pk_bf16_f32 v140, v141, v142
	v_add_f32_e32 v158, v237, v141
	v_add_f32_e32 v142, v238, v142
	s_add_i32 s27, s63, 0x0
	v_mfma_f32_32x32x16_bf16 v[96:111], a[216:219], a[184:187], v[96:111]
	ds_read_b64_tr_b16 v[34:35], v215 offset:0x3e00
	v_cvt_pk_bf16_f32 v141, v143, v232
	v_add_f32_e32 v143, v158, v143
	v_add_f32_e32 v158, v142, v232
	v_mfma_f32_32x32x16_bf16 v[80:95], a[248:251], a[152:155], v[80:95]
	v_cvt_pk_bf16_f32 v142, v233, v234
	v_add_f32_e32 v159, v143, v233
	v_add_f32_e32 v158, v158, v234
	v_mfma_f32_32x32x16_bf16 v[64:79], a[248:251], a[184:187], v[64:79]
	s_add_i32 s30, s63, 0x80
	v_cvt_pk_bf16_f32 v143, v239, v240
	v_add_f32_e32 v159, v159, v239
	v_add_f32_e32 v158, v158, v240
	v_mfma_f32_32x32x16_bf16 v[112:127], a[220:223], a[156:159], v[112:127]
	v_add_f32_e32 v159, v159, v148
	v_add_f32_e32 v158, v158, v149
	v_mfma_f32_32x32x16_bf16 v[96:111], a[220:223], a[188:191], v[96:111]
	s_add_i32 s31, s63, 0x800
	v_add_f32_e32 v159, v159, v150
	v_add_f32_e32 v158, v158, v151
	v_mfma_f32_32x32x16_bf16 v[80:95], a[252:255], a[156:159], v[80:95]
	v_add_f32_e32 v159, v159, v152
	v_add_f32_e32 v158, v158, v153
	v_mfma_f32_32x32x16_bf16 v[64:79], a[252:255], a[188:191], v[64:79]
	s_add_i32 s33, s63, 0x880
	v_add_f32_e32 v159, v159, v154
	v_add_f32_e32 v158, v158, v155
	s_nop 0
	s_nop 4
	v_add_f32_e32 v156, v156, v157
	s_waitcnt vmcnt(0) lgkmcnt(0)
	s_barrier
	s_nop 0
	v_mov_b32_e32 v157, v156
	s_nop 1
	v_permlane32_swap_b32_e32 v156, v157
	v_add_f32_e32 v156, v156, v157
	v_add_f32_e32 v219, v225, v156
	v_add_f32_e32 v156, v159, v158
	v_mov_b32_e32 v157, v156
	s_nop 1
	v_permlane32_swap_b32_e32 v156, v157
	v_add_f32_e32 v156, v156, v157
	v_add_f32_e32 v218, v226, v156
	v_mfma_f32_32x32x16_bf16 a[0:15], v[180:183], v[164:167], a[0:15]
	v_mfma_f32_32x32x16_bf16 a[16:31], v[180:183], v[192:195], a[16:31]
	ds_read_b128 a[192:195], v217 offset:0
	v_mfma_f32_32x32x16_bf16 a[32:47], v[188:191], v[164:167], a[32:47]
	ds_read_b128 a[196:199], v199 offset:0
	v_mfma_f32_32x32x16_bf16 a[48:63], v[188:191], v[192:195], a[48:63]
	ds_read_b128 a[200:203], v198 offset:0
	v_mfma_f32_32x32x16_bf16 a[64:79], v[176:179], v[164:167], a[64:79]
	s_mov_b32 m0, s23
	s_nop 0
	buffer_load_dwordx4 v196, s[4:7], s27 offen lds
	ds_read_b128 a[204:207], v197 offset:0
	v_mfma_f32_32x32x16_bf16 a[80:95], v[176:179], v[192:195], a[80:95]
	s_mov_b32 m0, s24
	s_nop 0
	buffer_load_dwordx4 v196, s[4:7], s30 offen lds
	ds_read_b128 a[208:211], v217 offset:128
	v_mfma_f32_32x32x16_bf16 a[96:111], v[184:187], v[164:167], a[96:111]
	s_mov_b32 m0, s25
	s_nop 0
	buffer_load_dwordx4 v196, s[4:7], s31 offen lds
	ds_read_b128 a[212:215], v199 offset:128
	v_mfma_f32_32x32x16_bf16 a[112:127], v[184:187], v[192:195], a[112:127]
	s_mov_b32 m0, s26
	s_nop 0
	buffer_load_dwordx4 v196, s[4:7], s33 offen lds
	ds_read_b128 a[216:219], v198 offset:128
	v_mfma_f32_32x32x16_bf16 a[0:15], v[172:175], v[128:131], a[0:15]
	ds_read_b128 a[220:223], v197 offset:128
	v_max3_f32 v156, v112, v113, v80
	v_max3_f32 v157, v114, v115, v81
	v_max3_f32 v156, v156, v82, v83
	v_mfma_f32_32x32x16_bf16 a[16:31], v[172:175], v[144:147], a[16:31]
	ds_read_b128 a[224:227], v217 offset:8192
	v_max3_f32 v156, v156, v116, v117
	v_max3_f32 v157, v157, v118, v119
	v_max3_f32 v156, v156, v84, v85
	v_max3_f32 v157, v157, v86, v87
	v_mfma_f32_32x32x16_bf16 a[32:47], v[168:171], v[128:131], a[32:47]
	ds_read_b128 a[228:231], v199 offset:8192
	v_max3_f32 v156, v156, v120, v121
	v_max3_f32 v157, v157, v122, v123
	v_max3_f32 v156, v156, v88, v89
	v_max3_f32 v157, v157, v90, v91
	v_mfma_f32_32x32x16_bf16 a[48:63], v[168:171], v[144:147], a[48:63]
	ds_read_b128 a[232:235], v198 offset:8192
	v_max3_f32 v156, v156, v124, v125
	v_max3_f32 v157, v157, v126, v127
	v_max3_f32 v156, v156, v92, v93
	v_max3_f32 v157, v157, v94, v95
	v_mfma_f32_32x32x16_bf16 a[64:79], v[160:163], v[128:131], a[64:79]
	ds_read_b128 a[236:239], v197 offset:8192
	v_max3_f32 v158, v96, v97, v64
	v_max3_f32 v159, v98, v99, v65
	v_max3_f32 v158, v158, v66, v67
	v_mfma_f32_32x32x16_bf16 a[80:95], v[160:163], v[144:147], a[80:95]
	ds_read_b128 a[240:243], v217 offset:8320
	v_max3_f32 v158, v158, v100, v101
	v_max3_f32 v159, v159, v102, v103
	v_max3_f32 v158, v158, v68, v69
	v_max3_f32 v159, v159, v70, v71
	v_mfma_f32_32x32x16_bf16 a[96:111], v[136:139], v[128:131], a[96:111]
	ds_read_b128 a[244:247], v199 offset:8320
	v_max3_f32 v128, v158, v104, v105
	v_max3_f32 v129, v159, v106, v107
	v_max3_f32 v128, v128, v72, v73
	v_max3_f32 v129, v129, v74, v75
	v_mfma_f32_32x32x16_bf16 a[112:127], v[136:139], v[144:147], a[112:127]
	ds_read_b128 a[248:251], v198 offset:8320
	v_max3_f32 v128, v128, v108, v109
	v_max3_f32 v129, v129, v110, v111
	v_max3_f32 v128, v128, v76, v77
	v_max3_f32 v130, v129, v78, v79
	v_mfma_f32_32x32x16_bf16 a[0:15], v[132:135], v[52:55], a[0:15]
	ds_read_b128 a[252:255], v197 offset:8320
	v_max_f32_e32 v129, v156, v157
	v_mov_b32_e32 v131, v129
	s_nop 1
	v_permlane32_swap_b32_e32 v129, v131
	v_max_f32_e32 v129, v129, v131
	v_mfma_f32_32x32x16_bf16 a[16:31], v[132:135], v[140:143], a[16:31]
	v_max_f32_e32 v128, v128, v130
	v_mov_b32_e32 v130, v128
	s_nop 1
	v_permlane32_swap_b32_e32 v128, v130
	v_max_f32_e32 v128, v128, v130
	v_max_f32_e32 v130, v129, v129
	v_max_f32_e32 v131, v128, v128
	v_max_f32_e32 v130, v130, v131
	s_mov_b32 s0, 0x41000000
	v_mfma_f32_32x32x16_bf16 a[32:47], v[60:63], v[52:55], a[32:47]
	v_cmp_lt_f32_e32 vcc, s0, v130
	s_cmp_lg_u64 vcc, 0
	s_cselect_b64 s[0:1], -1, 0
	s_cbranch_vccnz .LBB0_43
.LBB0_37:
	v_cvt_pk_bf16_f32 v156, v220, v221
	v_cvt_pk_bf16_f32 v157, v222, v223
	v_cvt_pk_bf16_f32 v158, v224, v227
	v_cvt_pk_bf16_f32 v159, v228, v229
	v_cvt_pk_bf16_f32 v160, v148, v149
	v_cvt_pk_bf16_f32 v161, v150, v151
	v_cvt_pk_bf16_f32 v162, v152, v153
	v_cvt_pk_bf16_f32 v163, v154, v155
	v_exp_f32_e32 v128, v112
	v_exp_f32_e32 v129, v113
	v_mfma_f32_32x32x16_bf16 a[48:63], v[60:63], v[140:143], a[48:63]
	v_exp_f32_e32 v130, v114
	v_exp_f32_e32 v131, v115
	v_mfma_f32_32x32x16_bf16 a[64:79], v[56:59], v[52:55], a[64:79]
	v_mov_b32_e32 v60, 0
	v_add_f32_e32 v61, v60, v128
	v_add_f32_e32 v62, v60, v129
	v_exp_f32_e32 v132, v116
	v_exp_f32_e32 v133, v117
	v_exp_f32_e32 v134, v118
	v_mfma_f32_32x32x16_bf16 a[80:95], v[56:59], v[140:143], a[80:95]
	v_add_f32_e32 v56, v61, v130
	v_add_f32_e32 v57, v62, v131
	v_exp_f32_e32 v135, v119
	v_exp_f32_e32 v136, v120
	v_mfma_f32_32x32x16_bf16 a[96:111], v[48:51], v[52:55], a[96:111]
	v_add_f32_e32 v52, v56, v132
	v_add_f32_e32 v53, v57, v133
	v_add_f32_e32 v52, v52, v134
	v_exp_f32_e32 v137, v121
	v_exp_f32_e32 v138, v122
	v_exp_f32_e32 v139, v123
	v_mfma_f32_32x32x16_bf16 a[112:127], v[48:51], v[140:143], a[112:127]
	v_add_f32_e32 v48, v53, v135
	v_add_f32_e32 v49, v52, v136
	v_exp_f32_e32 v140, v124
	v_exp_f32_e32 v141, v125
	v_mfma_f32_32x32x16_bf16 a[0:15], v[44:47], v[156:159], a[0:15]
	v_add_f32_e32 v48, v48, v137
	v_add_f32_e32 v49, v49, v138
	v_add_f32_e32 v48, v48, v139
	v_exp_f32_e32 v142, v126
	v_exp_f32_e32 v143, v127
	v_exp_f32_e32 v144, v96
	v_mfma_f32_32x32x16_bf16 a[16:31], v[44:47], v[160:163], a[16:31]
	v_add_f32_e32 v44, v49, v140
	v_add_f32_e32 v45, v48, v141
	v_exp_f32_e32 v145, v97
	v_exp_f32_e32 v146, v98
	v_mfma_f32_32x32x16_bf16 a[32:47], v[40:43], v[156:159], a[32:47]
	v_add_f32_e32 v226, v44, v142
	v_add_f32_e32 v224, v45, v143
	v_add_f32_e32 v44, v60, v144
	v_exp_f32_e32 v147, v99
	v_exp_f32_e32 v148, v100
	v_exp_f32_e32 v149, v101
	v_mfma_f32_32x32x16_bf16 a[48:63], v[40:43], v[160:163], a[48:63]
	v_add_f32_e32 v40, v60, v145
	v_add_f32_e32 v41, v44, v146
	v_exp_f32_e32 v150, v102
	v_exp_f32_e32 v151, v103
	v_mfma_f32_32x32x16_bf16 a[64:79], v[36:39], v[156:159], a[64:79]
	v_add_f32_e32 v40, v40, v147
	v_add_f32_e32 v41, v41, v148
	v_add_f32_e32 v40, v40, v149
	v_exp_f32_e32 v152, v104
	v_exp_f32_e32 v153, v105
	v_exp_f32_e32 v154, v106
	v_mfma_f32_32x32x16_bf16 a[80:95], v[36:39], v[160:163], a[80:95]
	v_add_f32_e32 v36, v41, v150
	v_add_f32_e32 v37, v40, v151
	v_mfma_f32_32x32x16_bf16 a[96:111], v[32:35], v[156:159], a[96:111]
	v_exp_f32_e32 v155, v107
	v_exp_f32_e32 v156, v108
	v_add_f32_e32 v36, v36, v152
	v_add_f32_e32 v37, v37, v153
	v_add_f32_e32 v36, v36, v154
	v_exp_f32_e32 v157, v109
	v_exp_f32_e32 v158, v110
	v_exp_f32_e32 v159, v111
	v_mfma_f32_32x32x16_bf16 a[112:127], v[32:35], v[160:163], a[112:127]
	v_add_f32_e32 v32, v37, v155
	v_add_f32_e32 v33, v36, v156
	s_andn2_b64 vcc, exec, s[0:1]
	v_add_f32_e32 v32, v32, v157
	v_add_f32_e32 v223, v33, v158
	s_nop 0
	v_add_f32_e32 v225, v32, v159
	s_cbranch_vccz .LBB0_44
.LBB0_38:
	s_waitcnt lgkmcnt(0)
	v_mfma_f32_32x32x16_bf16 v[112:127], a[192:195], a[128:131], v[0:15]
	ds_read_b64_tr_b16 v[172:173], v212 offset:0
	v_exp_f32_e32 v227, v80
	v_exp_f32_e32 v228, v81
	v_cvt_pk_bf16_f32 v164, v128, v129
	v_exp_f32_e32 v82, v82
	v_exp_f32_e32 v83, v83
	v_mfma_f32_32x32x16_bf16 v[96:111], a[192:195], a[160:163], v[16:31]
	ds_read_b64_tr_b16 v[174:175], v212 offset:0x800
	v_cvt_pk_bf16_f32 v165, v130, v131
	v_exp_f32_e32 v84, v84
	v_exp_f32_e32 v85, v85
	v_mfma_f32_32x32x16_bf16 v[48:63], a[224:227], a[128:131], v[0:15]
	ds_read_b64_tr_b16 v[180:181], v212 offset:0x200
	v_cvt_pk_bf16_f32 v166, v132, v133
	v_mfma_f32_32x32x16_bf16 v[32:47], a[224:227], a[160:163], v[16:31]
	ds_read_b64_tr_b16 v[182:183], v212 offset:0xa00
	v_exp_f32_e32 v86, v86
	v_exp_f32_e32 v87, v87
	ds_read_b64_tr_b16 v[184:185], v212 offset:0x400
	v_cvt_pk_bf16_f32 v167, v134, v135
	v_exp_f32_e32 v80, v88
	v_exp_f32_e32 v81, v89
	v_mfma_f32_32x32x16_bf16 v[112:127], a[196:199], a[132:135], v[112:127]
	ds_read_b64_tr_b16 v[186:187], v212 offset:0xc00
	v_cvt_pk_bf16_f32 v160, v136, v137
	v_exp_f32_e32 v90, v90
	v_exp_f32_e32 v91, v91
	v_mfma_f32_32x32x16_bf16 v[96:111], a[196:199], a[164:167], v[96:111]
	ds_read_b64_tr_b16 v[192:193], v212 offset:0x600
	v_cvt_pk_bf16_f32 v161, v138, v139
	v_exp_f32_e32 v217, v92
	v_exp_f32_e32 v220, v93
	v_mfma_f32_32x32x16_bf16 v[48:63], a[228:231], a[132:135], v[48:63]
	ds_read_b64_tr_b16 v[194:195], v212 offset:0xe00
	v_cvt_pk_bf16_f32 v162, v140, v141
	v_mfma_f32_32x32x16_bf16 v[32:47], a[228:231], a[164:167], v[32:47]
	ds_read_b64_tr_b16 v[188:189], v212 offset:0x1000
	v_exp_f32_e32 v221, v94
	v_exp_f32_e32 v222, v95
	ds_read_b64_tr_b16 v[190:191], v212 offset:0x1800
	v_cvt_pk_bf16_f32 v163, v142, v143
	v_exp_f32_e32 v130, v64
	v_exp_f32_e32 v131, v65
	v_mfma_f32_32x32x16_bf16 v[112:127], a[200:203], a[136:139], v[112:127]
	ds_read_b64_tr_b16 v[176:177], v212 offset:0x1200
	v_cvt_pk_bf16_f32 v196, v144, v145
	v_exp_f32_e32 v138, v66
	v_exp_f32_e32 v139, v67
	v_mfma_f32_32x32x16_bf16 v[96:111], a[200:203], a[168:171], v[96:111]
	ds_read_b64_tr_b16 v[178:179], v212 offset:0x1a00
	v_cvt_pk_bf16_f32 v197, v146, v147
	v_mfma_f32_32x32x16_bf16 v[48:63], a[232:235], a[136:139], v[48:63]
	ds_read_b64_tr_b16 v[168:169], v212 offset:0x1400
	v_exp_f32_e32 v229, v68
	v_exp_f32_e32 v230, v69
	v_cvt_pk_bf16_f32 v198, v148, v149
	v_mfma_f32_32x32x16_bf16 v[32:47], a[232:235], a[168:171], v[32:47]
	ds_read_b64_tr_b16 v[170:171], v212 offset:0x1c00
	ds_read_b64_tr_b16 v[144:145], v212 offset:0x1600
	v_exp_f32_e32 v231, v70
	v_exp_f32_e32 v232, v71
	v_cvt_pk_bf16_f32 v199, v150, v151
	v_exp_f32_e32 v64, v72
	v_exp_f32_e32 v65, v73
	v_mfma_f32_32x32x16_bf16 v[112:127], a[204:207], a[140:143], v[112:127]
	ds_read_b64_tr_b16 v[146:147], v212 offset:0x1e00
	v_cvt_pk_bf16_f32 v148, v152, v153
	v_exp_f32_e32 v70, v74
	v_exp_f32_e32 v71, v75
	v_mfma_f32_32x32x16_bf16 v[96:111], a[204:207], a[172:175], v[96:111]
	ds_read_b64_tr_b16 v[140:141], v212 offset:0x2000
	v_cvt_pk_bf16_f32 v149, v154, v155
	v_exp_f32_e32 v154, v76
	v_exp_f32_e32 v155, v77
	v_mfma_f32_32x32x16_bf16 v[48:63], a[236:239], a[140:143], v[48:63]
	ds_read_b64_tr_b16 v[142:143], v212 offset:0x2800
	v_cvt_pk_bf16_f32 v150, v156, v157
	v_mfma_f32_32x32x16_bf16 v[32:47], a[236:239], a[172:175], v[32:47]
	ds_read_b64_tr_b16 v[66:67], v212 offset:0x2200
	v_exp_f32_e32 v156, v78
	v_exp_f32_e32 v157, v79
	ds_read_b64_tr_b16 v[68:69], v212 offset:0x2a00
	v_cvt_pk_bf16_f32 v151, v158, v159
	v_mfma_f32_32x32x16_bf16 v[112:127], a[208:211], a[144:147], v[112:127]
	ds_read_b64_tr_b16 v[132:133], v212 offset:0x2400
	v_cvt_pk_bf16_f32 v72, v227, v228
	v_add_f32_e32 v74, v226, v227
	v_add_f32_e32 v75, v224, v228
	s_add_i32 s0, s28, 0x84000
	v_mfma_f32_32x32x16_bf16 v[96:111], a[208:211], a[176:179], v[96:111]
	ds_read_b64_tr_b16 v[134:135], v212 offset:0x2c00
	v_cvt_pk_bf16_f32 v73, v82, v83
	v_add_f32_e32 v78, v74, v82
	v_add_f32_e32 v75, v75, v83
	v_mfma_f32_32x32x16_bf16 v[48:63], a[240:243], a[144:147], v[48:63]
	ds_read_b64_tr_b16 v[76:77], v212 offset:0x2600
	v_cvt_pk_bf16_f32 v74, v84, v85
	v_add_f32_e32 v84, v78, v84
	v_add_f32_e32 v85, v75, v85
	s_add_i32 s1, s28, 0x84400
	v_mfma_f32_32x32x16_bf16 v[32:47], a[240:243], a[176:179], v[32:47]
	ds_read_b64_tr_b16 v[78:79], v212 offset:0x2e00
	ds_read_b64_tr_b16 v[82:83], v212 offset:0x3000
	v_cvt_pk_bf16_f32 v75, v86, v87
	v_add_f32_e32 v86, v84, v86
	v_add_f32_e32 v87, v85, v87
	v_mfma_f32_32x32x16_bf16 v[112:127], a[212:215], a[148:151], v[112:127]
	ds_read_b64_tr_b16 v[84:85], v212 offset:0x3800
	v_add_f32_e32 v88, v86, v80
	v_add_f32_e32 v89, v87, v81
	s_add_i32 s4, s28, 0x84800
	v_mfma_f32_32x32x16_bf16 v[96:111], a[212:215], a[180:183], v[96:111]
	ds_read_b64_tr_b16 v[86:87], v212 offset:0x3200
	v_add_f32_e32 v92, v88, v90
	v_add_f32_e32 v93, v89, v91
	v_mfma_f32_32x32x16_bf16 v[48:63], a[244:247], a[148:151], v[48:63]
	ds_read_b64_tr_b16 v[88:89], v212 offset:0x3a00
	v_add_f32_e32 v128, v92, v217
	v_add_f32_e32 v129, v93, v220
	s_add_i32 s5, s28, 0x84c00
	v_mfma_f32_32x32x16_bf16 v[32:47], a[244:247], a[180:183], v[32:47]
	ds_read_b64_tr_b16 v[92:93], v212 offset:0x3400
	ds_read_b64_tr_b16 v[94:95], v212 offset:0x3c00
	v_add_f32_e32 v152, v128, v221
	v_add_f32_e32 v153, v129, v222
	v_mfma_f32_32x32x16_bf16 v[112:127], a[216:219], a[152:155], v[112:127]
	ds_read_b64_tr_b16 v[128:129], v212 offset:0x3600
	v_cvt_pk_bf16_f32 v136, v130, v131
	v_add_f32_e32 v158, v223, v130
	v_add_f32_e32 v159, v225, v131
	v_mfma_f32_32x32x16_bf16 v[96:111], a[216:219], a[184:187], v[96:111]
	ds_read_b64_tr_b16 v[130:131], v212 offset:0x3e00
	v_cvt_pk_bf16_f32 v137, v138, v139
	v_add_f32_e32 v158, v158, v138
	v_add_f32_e32 v139, v159, v139
	v_mfma_f32_32x32x16_bf16 v[48:63], a[248:251], a[152:155], v[48:63]
	v_cvt_pk_bf16_f32 v138, v229, v230
	v_add_f32_e32 v158, v158, v229
	v_add_f32_e32 v159, v139, v230
	v_mfma_f32_32x32x16_bf16 v[32:47], a[248:251], a[184:187], v[32:47]
	s_add_i32 s6, s28, 0x80080
	v_cvt_pk_bf16_f32 v139, v231, v232
	v_add_f32_e32 v158, v158, v231
	v_add_f32_e32 v159, v159, v232
	v_mfma_f32_32x32x16_bf16 v[112:127], a[220:223], a[156:159], v[112:127]
	v_add_f32_e32 v158, v158, v64
	v_add_f32_e32 v159, v159, v65
	v_mfma_f32_32x32x16_bf16 v[96:111], a[220:223], a[188:191], v[96:111]
	v_add_f32_e32 v158, v158, v70
	v_add_f32_e32 v159, v159, v71
	v_mfma_f32_32x32x16_bf16 v[48:63], a[252:255], a[156:159], v[48:63]
	v_add_f32_e32 v158, v158, v154
	v_add_f32_e32 v159, v159, v155
	v_mfma_f32_32x32x16_bf16 v[32:47], a[252:255], a[188:191], v[32:47]
	s_add_i32 s7, s28, 0x80880
	v_add_f32_e32 v158, v158, v156
	v_add_f32_e32 v159, v159, v157
	s_nop 0
	s_nop 4
	v_add_f32_e32 v152, v152, v153
	s_waitcnt vmcnt(0) lgkmcnt(0)
	s_barrier
	s_nop 0
	v_mov_b32_e32 v153, v152
	s_nop 1
	v_permlane32_swap_b32_e32 v152, v153
	v_add_f32_e32 v152, v152, v153
	v_add_f32_e32 v153, v219, v152
	v_add_f32_e32 v152, v158, v159
	v_mov_b32_e32 v158, v152
	s_nop 1
	v_permlane32_swap_b32_e32 v152, v158
	v_add_f32_e32 v152, v152, v158
	v_add_f32_e32 v152, v218, v152
	v_mfma_f32_32x32x16_bf16 a[0:15], v[172:175], v[164:167], a[0:15]
	v_mfma_f32_32x32x16_bf16 a[16:31], v[172:175], v[196:199], a[16:31]
	v_mfma_f32_32x32x16_bf16 a[32:47], v[180:183], v[164:167], a[32:47]
	v_mfma_f32_32x32x16_bf16 a[48:63], v[180:183], v[196:199], a[48:63]
	v_mfma_f32_32x32x16_bf16 a[64:79], v[184:187], v[164:167], a[64:79]
	v_mfma_f32_32x32x16_bf16 a[80:95], v[184:187], v[196:199], a[80:95]
	v_mfma_f32_32x32x16_bf16 a[96:111], v[192:195], v[164:167], a[96:111]
	v_mfma_f32_32x32x16_bf16 a[112:127], v[192:195], v[196:199], a[112:127]
	v_mfma_f32_32x32x16_bf16 a[0:15], v[188:191], v[160:163], a[0:15]
	v_max3_f32 v158, v112, v113, v48
	v_max3_f32 v159, v114, v115, v49
	v_max3_f32 v158, v158, v50, v51
	v_mfma_f32_32x32x16_bf16 a[16:31], v[188:191], v[148:151], a[16:31]
	v_max3_f32 v158, v158, v116, v117
	v_max3_f32 v159, v159, v118, v119
	v_max3_f32 v158, v158, v52, v53
	v_max3_f32 v159, v159, v54, v55
	v_mfma_f32_32x32x16_bf16 a[32:47], v[176:179], v[160:163], a[32:47]
	v_max3_f32 v158, v158, v120, v121
	v_max3_f32 v159, v159, v122, v123
	v_max3_f32 v158, v158, v56, v57
	v_max3_f32 v159, v159, v58, v59
	v_mfma_f32_32x32x16_bf16 a[48:63], v[176:179], v[148:151], a[48:63]
	v_max3_f32 v158, v158, v124, v125
	v_max3_f32 v159, v159, v126, v127
	v_max3_f32 v158, v158, v60, v61
	v_max3_f32 v159, v159, v62, v63
	v_mfma_f32_32x32x16_bf16 a[64:79], v[168:171], v[160:163], a[64:79]
	v_max3_f32 v164, v96, v97, v32
	v_max3_f32 v165, v98, v99, v33
	v_max3_f32 v164, v164, v34, v35
	v_mfma_f32_32x32x16_bf16 a[80:95], v[168:171], v[148:151], a[80:95]
	v_max3_f32 v164, v164, v100, v101
	v_max3_f32 v165, v165, v102, v103
	v_max3_f32 v164, v164, v36, v37
	v_max3_f32 v165, v165, v38, v39
	v_mfma_f32_32x32x16_bf16 a[96:111], v[144:147], v[160:163], a[96:111]
	v_max3_f32 v160, v164, v104, v105
	v_max3_f32 v161, v165, v106, v107
	v_max3_f32 v160, v160, v40, v41
	v_max3_f32 v161, v161, v42, v43
	v_mfma_f32_32x32x16_bf16 a[112:127], v[144:147], v[148:151], a[112:127]
	v_max3_f32 v145, v161, v110, v111
	v_max3_f32 v144, v160, v108, v109
	v_max3_f32 v146, v144, v44, v45
	v_max3_f32 v145, v145, v46, v47
	v_mfma_f32_32x32x16_bf16 a[0:15], v[140:143], v[72:75], a[0:15]
	v_max_f32_e32 v144, v158, v159
	v_mov_b32_e32 v147, v144
	s_nop 1
	v_permlane32_swap_b32_e32 v144, v147
	v_max_f32_e32 v144, v144, v147
	v_mfma_f32_32x32x16_bf16 a[16:31], v[140:143], v[136:139], a[16:31]
	v_max_f32_e32 v140, v146, v145
	v_mov_b32_e32 v141, v140
	s_nop 1
	v_permlane32_swap_b32_e32 v140, v141
	v_max_f32_e32 v140, v140, v141
	v_max_f32_e32 v141, v144, v144
	v_max_f32_e32 v142, v140, v140
	v_max_f32_e32 v141, v141, v142
	s_mov_b32 s0, 0x41000000
	v_mfma_f32_32x32x16_bf16 a[32:47], v[66:69], v[72:75], a[32:47]
	v_cmp_lt_f32_e32 vcc, s0, v141
	s_cmp_lg_u64 vcc, 0
	s_cselect_b64 s[0:1], -1, 0
	s_cbranch_vccnz .LBB0_45
.LBB0_39:
	v_cvt_pk_bf16_f32 v140, v80, v81
	v_cvt_pk_bf16_f32 v141, v90, v91
	v_cvt_pk_bf16_f32 v142, v217, v220
	v_cvt_pk_bf16_f32 v143, v221, v222
	v_cvt_pk_bf16_f32 v144, v64, v65
	v_cvt_pk_bf16_f32 v145, v70, v71
	v_cvt_pk_bf16_f32 v146, v154, v155
	v_cvt_pk_bf16_f32 v147, v156, v157
	v_exp_f32_e32 v64, v112
	v_exp_f32_e32 v65, v113
	v_mfma_f32_32x32x16_bf16 a[48:63], v[66:69], v[136:139], a[48:63]
	v_exp_f32_e32 v66, v114
	v_exp_f32_e32 v67, v115
	v_mfma_f32_32x32x16_bf16 a[64:79], v[132:135], v[72:75], a[64:79]
	v_mov_b32_e32 v90, 0
	v_add_f32_e32 v71, v90, v64
	v_add_f32_e32 v80, v90, v65
	v_exp_f32_e32 v68, v116
	v_exp_f32_e32 v69, v117
	v_exp_f32_e32 v70, v118
	v_mfma_f32_32x32x16_bf16 a[80:95], v[132:135], v[136:139], a[80:95]
	v_add_f32_e32 v81, v71, v66
	v_add_f32_e32 v80, v80, v67
	v_mfma_f32_32x32x16_bf16 a[96:111], v[76:79], v[72:75], a[96:111]
	v_exp_f32_e32 v71, v119
	v_exp_f32_e32 v72, v120
	v_add_f32_e32 v73, v81, v68
	v_add_f32_e32 v80, v80, v69
	v_add_f32_e32 v81, v73, v70
	v_exp_f32_e32 v73, v121
	v_exp_f32_e32 v74, v122
	v_exp_f32_e32 v75, v123
	v_mfma_f32_32x32x16_bf16 a[112:127], v[76:79], v[136:139], a[112:127]
	v_add_f32_e32 v78, v80, v71
	v_add_f32_e32 v79, v81, v72
	v_exp_f32_e32 v76, v124
	v_exp_f32_e32 v77, v125
	v_mfma_f32_32x32x16_bf16 a[0:15], v[82:85], v[140:143], a[0:15]
	v_add_f32_e32 v78, v78, v73
	v_add_f32_e32 v81, v79, v74
	v_add_f32_e32 v91, v78, v75
	v_exp_f32_e32 v78, v126
	v_exp_f32_e32 v79, v127
	v_exp_f32_e32 v80, v96
	v_mfma_f32_32x32x16_bf16 a[16:31], v[82:85], v[144:147], a[16:31]
	v_add_f32_e32 v83, v81, v76
	v_add_f32_e32 v84, v91, v77
	v_exp_f32_e32 v81, v97
	v_exp_f32_e32 v82, v98
	v_mfma_f32_32x32x16_bf16 a[32:47], v[86:89], v[140:143], a[32:47]
	v_add_f32_e32 v133, v83, v78
	v_add_f32_e32 v132, v84, v79
	v_add_f32_e32 v91, v90, v80
	v_exp_f32_e32 v83, v99
	v_exp_f32_e32 v84, v100
	v_exp_f32_e32 v85, v101
	v_mfma_f32_32x32x16_bf16 a[48:63], v[86:89], v[144:147], a[48:63]
	v_add_f32_e32 v88, v90, v81
	v_add_f32_e32 v89, v91, v82
	v_exp_f32_e32 v86, v102
	v_exp_f32_e32 v87, v103
	v_mfma_f32_32x32x16_bf16 a[64:79], v[92:95], v[140:143], a[64:79]
	v_add_f32_e32 v88, v88, v83
	v_add_f32_e32 v91, v89, v84
	v_add_f32_e32 v96, v88, v85
	v_exp_f32_e32 v88, v104
	v_exp_f32_e32 v89, v105
	v_exp_f32_e32 v90, v106
	v_mfma_f32_32x32x16_bf16 a[80:95], v[92:95], v[144:147], a[80:95]
	v_add_f32_e32 v93, v91, v86
	v_add_f32_e32 v94, v96, v87
	v_exp_f32_e32 v91, v107
	v_exp_f32_e32 v92, v108
	v_mfma_f32_32x32x16_bf16 a[96:111], v[128:131], v[140:143], a[96:111]
	v_add_f32_e32 v93, v93, v88
	v_add_f32_e32 v96, v94, v89
	v_add_f32_e32 v97, v93, v90
	v_exp_f32_e32 v93, v109
	v_exp_f32_e32 v94, v110
	v_exp_f32_e32 v95, v111
	v_mfma_f32_32x32x16_bf16 a[112:127], v[128:131], v[144:147], a[112:127]
	v_add_f32_e32 v96, v96, v91
	v_add_f32_e32 v97, v97, v92
	s_andn2_b64 vcc, exec, s[0:1]
	v_add_f32_e32 v0, v96, v93
	v_add_f32_e32 v129, v97, v94
	s_nop 0
	v_add_f32_e32 v130, v0, v95
	s_cbranch_vccz .LBB0_46
.LBB0_40:
	s_waitcnt lgkmcnt(0)
	v_lshrrev_b32_e32 v128, 5, v204
	ds_read_b64_tr_b16 v[124:125], v215 offset:0
	ds_read_b64_tr_b16 v[126:127], v215 offset:0x800
	ds_read_b64_tr_b16 v[120:121], v215 offset:0x200
	ds_read_b64_tr_b16 v[122:123], v215 offset:0xa00
	ds_read_b64_tr_b16 v[116:117], v215 offset:0x400
	ds_read_b64_tr_b16 v[118:119], v215 offset:0xc00
	ds_read_b64_tr_b16 v[112:113], v215 offset:0x600
	ds_read_b64_tr_b16 v[114:115], v215 offset:0xe00
	ds_read_b64_tr_b16 v[108:109], v215 offset:0x1000
	ds_read_b64_tr_b16 v[110:111], v215 offset:0x1800
	ds_read_b64_tr_b16 v[104:105], v215 offset:0x1200
	ds_read_b64_tr_b16 v[106:107], v215 offset:0x1a00
	ds_read_b64_tr_b16 v[100:101], v215 offset:0x1400
	ds_read_b64_tr_b16 v[102:103], v215 offset:0x1c00
	ds_read_b64_tr_b16 v[96:97], v215 offset:0x1600
	ds_read_b64_tr_b16 v[98:99], v215 offset:0x1e00
	ds_read_b64_tr_b16 v[28:29], v215 offset:0x2000
	ds_read_b64_tr_b16 v[30:31], v215 offset:0x2800
	ds_read_b64_tr_b16 v[24:25], v215 offset:0x2200
	ds_read_b64_tr_b16 v[26:27], v215 offset:0x2a00
	ds_read_b64_tr_b16 v[20:21], v215 offset:0x2400
	ds_read_b64_tr_b16 v[22:23], v215 offset:0x2c00
	v_exp_f32_e32 v131, v48
	v_exp_f32_e32 v134, v49
	v_exp_f32_e32 v159, v40
	v_cvt_pk_bf16_f32 v40, v64, v65
	v_add_f32_e32 v64, v133, v131
	v_add_f32_e32 v65, v132, v134
	ds_read_b64_tr_b16 v[16:17], v215 offset:0x2600
	v_exp_f32_e32 v135, v50
	v_exp_f32_e32 v136, v51
	v_add_f32_e32 v64, v64, v135
	v_add_f32_e32 v65, v65, v136
	ds_read_b64_tr_b16 v[18:19], v215 offset:0x2e00
	v_exp_f32_e32 v137, v52
	v_exp_f32_e32 v138, v53
	v_add_f32_e32 v64, v64, v137
	v_add_f32_e32 v65, v65, v138
	ds_read_b64_tr_b16 v[12:13], v215 offset:0x3000
	v_exp_f32_e32 v139, v54
	v_exp_f32_e32 v140, v55
	v_exp_f32_e32 v149, v32
	v_exp_f32_e32 v160, v41
	v_cvt_pk_bf16_f32 v41, v66, v67
	v_add_f32_e32 v64, v64, v139
	v_add_f32_e32 v65, v65, v140
	v_add_f32_e32 v66, v129, v149
	ds_read_b64_tr_b16 v[14:15], v215 offset:0x3800
	v_exp_f32_e32 v141, v56
	v_exp_f32_e32 v142, v57
	v_exp_f32_e32 v150, v33
	v_exp_f32_e32 v151, v34
	v_add_f32_e32 v64, v64, v141
	v_add_f32_e32 v65, v65, v142
	v_add_f32_e32 v67, v130, v150
	v_add_f32_e32 v66, v66, v151
	ds_read_b64_tr_b16 v[8:9], v215 offset:0x3200
	v_exp_f32_e32 v143, v58
	v_exp_f32_e32 v144, v59
	v_exp_f32_e32 v154, v35
	v_exp_f32_e32 v155, v36
	v_add_f32_e32 v64, v64, v143
	v_add_f32_e32 v65, v65, v144
	v_add_f32_e32 v67, v67, v154
	v_add_f32_e32 v66, v66, v155
	ds_read_b64_tr_b16 v[10:11], v215 offset:0x3a00
	v_exp_f32_e32 v145, v60
	v_exp_f32_e32 v146, v61
	v_exp_f32_e32 v156, v37
	v_exp_f32_e32 v157, v38
	v_add_f32_e32 v64, v64, v145
	v_add_f32_e32 v65, v65, v146
	v_add_f32_e32 v67, v67, v156
	v_add_f32_e32 v66, v66, v157
	ds_read_b64_tr_b16 v[4:5], v215 offset:0x3400
	v_exp_f32_e32 v147, v62
	v_exp_f32_e32 v148, v63
	v_exp_f32_e32 v158, v39
	v_add_f32_e32 v64, v64, v147
	v_add_f32_e32 v65, v65, v148
	v_add_f32_e32 v67, v67, v158
	v_add_f32_e32 v66, v66, v159
	ds_read_b64_tr_b16 v[6:7], v215 offset:0x3c00
	v_exp_f32_e32 v161, v42
	v_add_f32_e32 v67, v67, v160
	v_add_f32_e32 v66, v66, v161
	v_add_f32_e32 v64, v64, v65
	ds_read_b64_tr_b16 v[0:1], v215 offset:0x3600
	v_exp_f32_e32 v162, v43
	v_mov_b32_e32 v65, v64
	v_exp_f32_e32 v163, v44
	v_add_f32_e32 v67, v67, v162
	v_add_f32_e32 v66, v66, v163
	v_permlane32_swap_b32_e32 v64, v65
	ds_read_b64_tr_b16 v[2:3], v215 offset:0x3e00
	v_exp_f32_e32 v164, v45
	v_exp_f32_e32 v165, v46
	v_exp_f32_e32 v166, v47
	v_add_f32_e32 v67, v67, v164
	v_add_f32_e32 v66, v66, v165
	v_add_f32_e32 v64, v64, v65
	s_waitcnt lgkmcnt(0)
	v_cvt_pk_bf16_f32 v42, v68, v69
	v_add_f32_e32 v67, v67, v166
	v_add_f32_e32 v65, v153, v64
	v_cvt_pk_bf16_f32 v43, v70, v71
	v_add_f32_e32 v64, v66, v67
	v_cvt_pk_bf16_f32 v32, v72, v73
	v_mov_b32_e32 v66, v64
	s_nop 1
	v_permlane32_swap_b32_e32 v64, v66
	v_add_f32_e32 v64, v64, v66
	v_cvt_pk_bf16_f32 v33, v74, v75
	v_cvt_pk_bf16_f32 v34, v76, v77
	v_cvt_pk_bf16_f32 v35, v78, v79
	v_cvt_pk_bf16_f32 v56, v80, v81
	v_cvt_pk_bf16_f32 v57, v82, v83
	v_cvt_pk_bf16_f32 v58, v84, v85
	v_cvt_pk_bf16_f32 v59, v86, v87
	v_cvt_pk_bf16_f32 v48, v88, v89
	v_cvt_pk_bf16_f32 v49, v90, v91
	v_cvt_pk_bf16_f32 v50, v92, v93
	v_cvt_pk_bf16_f32 v51, v94, v95
	v_cvt_pk_bf16_f32 v44, v131, v134
	v_cvt_pk_bf16_f32 v45, v135, v136
	v_cvt_pk_bf16_f32 v46, v137, v138
	v_cvt_pk_bf16_f32 v47, v139, v140
	v_cvt_pk_bf16_f32 v36, v141, v142
	v_cvt_pk_bf16_f32 v37, v143, v144
	v_cvt_pk_bf16_f32 v38, v145, v146
	v_cvt_pk_bf16_f32 v39, v147, v148
	v_cvt_pk_bf16_f32 v60, v149, v150
	v_cvt_pk_bf16_f32 v61, v151, v154
	v_cvt_pk_bf16_f32 v62, v155, v156
	v_cvt_pk_bf16_f32 v63, v157, v158
	v_cvt_pk_bf16_f32 v52, v159, v160
	v_cvt_pk_bf16_f32 v53, v161, v162
	v_cvt_pk_bf16_f32 v54, v163, v164
	v_cvt_pk_bf16_f32 v55, v165, v166
	v_add_f32_e32 v64, v152, v64
	v_mfma_f32_32x32x16_bf16 a[0:15], v[124:127], v[40:43], a[0:15]
	v_cmp_lt_f32_e32 vcc, 0, v65
	v_mfma_f32_32x32x16_bf16 a[16:31], v[124:127], v[56:59], a[16:31]
	v_readfirstlane_b32 s0, v200
	v_mfma_f32_32x32x16_bf16 a[32:47], v[120:123], v[40:43], a[32:47]
	s_and_b32 s9, s9, 0xffff
	v_mfma_f32_32x32x16_bf16 a[48:63], v[120:123], v[56:59], a[48:63]
	s_mov_b32 s11, 0x20000
	v_mfma_f32_32x32x16_bf16 a[64:79], v[116:119], v[40:43], a[64:79]
	s_mov_b32 s10, 0x1000000
	v_mfma_f32_32x32x16_bf16 a[80:95], v[116:119], v[56:59], a[80:95]
	s_lshl_b32 s0, s0, 8
	v_mfma_f32_32x32x16_bf16 a[96:111], v[112:115], v[40:43], a[96:111]
	v_xor_b32_e32 v43, v208, v204
	v_mfma_f32_32x32x16_bf16 a[112:127], v[112:115], v[56:59], a[112:127]
	v_lshlrev_b32_e32 v43, 5, v43
	v_mfma_f32_32x32x16_bf16 a[0:15], v[108:111], v[32:35], a[0:15]
	v_xor_b32_e32 v59, v210, v204
	v_mfma_f32_32x32x16_bf16 a[16:31], v[108:111], v[48:51], a[16:31]
	v_lshlrev_b32_e32 v42, 9, v208
	v_mfma_f32_32x32x16_bf16 a[32:47], v[104:107], v[32:35], a[32:47]
	v_and_b32_e32 v43, 0x1e0, v43
	v_mfma_f32_32x32x16_bf16 a[48:63], v[104:107], v[48:51], a[48:63]
	v_lshlrev_b32_e32 v59, 5, v59
	v_mfma_f32_32x32x16_bf16 a[64:79], v[100:103], v[32:35], a[64:79]
	v_add3_u32 v87, v201, v42, v43
	v_mfma_f32_32x32x16_bf16 a[80:95], v[100:103], v[48:51], a[80:95]
	v_lshlrev_b32_e32 v58, 9, v210
	v_mfma_f32_32x32x16_bf16 a[96:111], v[96:99], v[32:35], a[96:111]
	v_lshlrev_b32_e32 v35, 9, v207
	v_mfma_f32_32x32x16_bf16 a[112:127], v[96:99], v[48:51], a[112:127]
	v_xor_b32_e32 v51, v209, v204
	v_mfma_f32_32x32x16_bf16 a[0:15], v[28:31], v[44:47], a[0:15]
	v_lshlrev_b32_e32 v51, 5, v51
	v_mfma_f32_32x32x16_bf16 a[16:31], v[28:31], v[60:63], a[16:31]
	v_lshlrev_b32_e32 v50, 9, v209
	v_mfma_f32_32x32x16_bf16 a[32:47], v[24:27], v[44:47], a[32:47]
	v_and_b32_e32 v51, 0x1e0, v51
	v_mfma_f32_32x32x16_bf16 a[48:63], v[24:27], v[60:63], a[48:63]
	v_xor_b32_e32 v27, v206, v204
	v_mfma_f32_32x32x16_bf16 a[64:79], v[20:23], v[44:47], a[64:79]
	v_lshlrev_b32_e32 v27, 5, v27
	v_mfma_f32_32x32x16_bf16 a[80:95], v[20:23], v[60:63], a[80:95]
	v_lshlrev_b32_e32 v26, 9, v206
	v_mfma_f32_32x32x16_bf16 a[96:111], v[16:19], v[44:47], a[96:111]
	v_and_b32_e32 v27, 0x1e0, v27
	v_mfma_f32_32x32x16_bf16 a[112:127], v[16:19], v[60:63], a[112:127]
	v_add3_u32 v85, v201, v26, v27
	v_mfma_f32_32x32x16_bf16 a[0:15], v[12:15], v[36:39], a[0:15]
	v_and_b32_e32 v59, 0x1e0, v59
	v_mfma_f32_32x32x16_bf16 a[16:31], v[12:15], v[52:55], a[16:31]
	v_add3_u32 v88, v201, v50, v51
	v_mfma_f32_32x32x16_bf16 a[32:47], v[8:11], v[36:39], a[32:47]
	v_add3_u32 v89, v201, v58, v59
	v_mfma_f32_32x32x16_bf16 a[48:63], v[8:11], v[52:55], a[48:63]
	s_or_b32 s1, s0, 0x400
	v_mfma_f32_32x32x16_bf16 a[64:79], v[4:7], v[36:39], a[64:79]
	v_mfma_f32_32x32x16_bf16 a[80:95], v[4:7], v[52:55], a[80:95]
	v_lshlrev_b32_e32 v6, 1, v204
	v_mfma_f32_32x32x16_bf16 a[96:111], v[0:3], v[36:39], a[96:111]
	v_bitop3_b32 v20, v128, v6, 30 bitop3:0x78
	v_mfma_f32_32x32x16_bf16 a[112:127], v[0:3], v[52:55], a[112:127]
	v_rcp_f32_e32 v2, v65
	v_lshlrev_b32_e32 v0, 9, v204
	v_and_b32_e32 v0, 0x3e00, v0
	v_add_u32_e32 v1, v201, v0
	v_cndmask_b32_e32 v7, 0, v2, vcc
	v_accvgpr_read_b32 v2, a0
	v_accvgpr_read_b32 v3, a1
	v_accvgpr_read_b32 v4, a2
	v_accvgpr_read_b32 v5, a3
	v_accvgpr_read_b32 v8, a4
	v_accvgpr_read_b32 v9, a5
	v_accvgpr_read_b32 v10, a6
	v_accvgpr_read_b32 v11, a7
	v_accvgpr_read_b32 v12, a8
	v_accvgpr_read_b32 v13, a9
	v_accvgpr_read_b32 v14, a10
	v_accvgpr_read_b32 v15, a11
	v_accvgpr_read_b32 v16, a12
	v_accvgpr_read_b32 v17, a13
	v_accvgpr_read_b32 v18, a14
	v_accvgpr_read_b32 v19, a15

	v_lshl_add_u32 v62, v20, 4, v1
	v_mul_f32_e32 v2, v2, v7
	v_mul_f32_e32 v3, v3, v7
	v_mul_f32_e32 v4, v4, v7
	v_mul_f32_e32 v5, v5, v7
	ds_write_b128 v62, v[2:5]
	v_mul_f32_e32 v2, v8, v7
	v_add_u32_e32 v8, 2, v128
	v_bitop3_b32 v8, v8, v6, 30 bitop3:0x78
	v_lshl_add_u32 v63, v8, 4, v1
	v_add_u32_e32 v8, 4, v128
	v_bitop3_b32 v8, v8, v6, 30 bitop3:0x78
	v_mul_f32_e32 v3, v9, v7
	v_mul_f32_e32 v4, v10, v7
	v_mul_f32_e32 v5, v11, v7
	v_lshl_add_u32 v65, v8, 4, v1
	v_add_u32_e32 v8, 6, v128
	ds_write_b128 v63, v[2:5]
	v_mul_f32_e32 v2, v12, v7
	v_mul_f32_e32 v3, v13, v7
	v_mul_f32_e32 v4, v14, v7
	v_mul_f32_e32 v5, v15, v7
	v_bitop3_b32 v8, v8, v6, 30 bitop3:0x78
	ds_write_b128 v65, v[2:5]
	v_mul_f32_e32 v2, v16, v7
	v_mul_f32_e32 v3, v17, v7
	v_mul_f32_e32 v4, v18, v7
	v_mul_f32_e32 v5, v19, v7
	v_lshl_add_u32 v70, v8, 4, v1
	v_add_u32_e32 v20, 8, v128
	ds_write_b128 v70, v[2:5]
	v_accvgpr_read_b32 v2, a32
	v_accvgpr_read_b32 v3, a33
	v_accvgpr_read_b32 v4, a34
	v_accvgpr_read_b32 v5, a35
	v_accvgpr_read_b32 v8, a36
	v_accvgpr_read_b32 v9, a37
	v_accvgpr_read_b32 v10, a38
	v_accvgpr_read_b32 v11, a39
	v_accvgpr_read_b32 v12, a40
	v_accvgpr_read_b32 v13, a41
	v_accvgpr_read_b32 v14, a42
	v_accvgpr_read_b32 v15, a43
	v_accvgpr_read_b32 v16, a44
	v_accvgpr_read_b32 v17, a45
	v_accvgpr_read_b32 v18, a46
	v_accvgpr_read_b32 v19, a47

	v_bitop3_b32 v20, v20, v6, 30 bitop3:0x78
	v_mul_f32_e32 v2, v2, v7
	v_lshl_add_u32 v71, v20, 4, v1
	v_mul_f32_e32 v3, v3, v7
	v_mul_f32_e32 v4, v4, v7
	v_mul_f32_e32 v5, v5, v7
	ds_write_b128 v71, v[2:5]
	v_mul_f32_e32 v2, v8, v7
	v_add_u32_e32 v8, 10, v128
	v_bitop3_b32 v8, v8, v6, 30 bitop3:0x78
	v_lshl_add_u32 v72, v8, 4, v1
	v_add_u32_e32 v8, 12, v128
	v_bitop3_b32 v8, v8, v6, 30 bitop3:0x78
	v_mul_f32_e32 v3, v9, v7
	v_mul_f32_e32 v4, v10, v7
	v_mul_f32_e32 v5, v11, v7
	v_lshl_add_u32 v73, v8, 4, v1
	v_add_u32_e32 v8, 14, v128
	ds_write_b128 v72, v[2:5]
	v_mul_f32_e32 v2, v12, v7
	v_mul_f32_e32 v3, v13, v7
	v_mul_f32_e32 v4, v14, v7
	v_mul_f32_e32 v5, v15, v7
	v_bitop3_b32 v8, v8, v6, 30 bitop3:0x78
	ds_write_b128 v73, v[2:5]
	v_mul_f32_e32 v2, v16, v7
	v_mul_f32_e32 v3, v17, v7
	v_mul_f32_e32 v4, v18, v7
	v_mul_f32_e32 v5, v19, v7
	v_lshl_add_u32 v74, v8, 4, v1
	v_add_u32_e32 v20, 16, v128
	ds_write_b128 v74, v[2:5]
	v_accvgpr_read_b32 v2, a64
	v_accvgpr_read_b32 v3, a65
	v_accvgpr_read_b32 v4, a66
	v_accvgpr_read_b32 v5, a67
	v_accvgpr_read_b32 v8, a68
	v_accvgpr_read_b32 v9, a69
	v_accvgpr_read_b32 v10, a70
	v_accvgpr_read_b32 v11, a71
	v_accvgpr_read_b32 v12, a72
	v_accvgpr_read_b32 v13, a73
	v_accvgpr_read_b32 v14, a74
	v_accvgpr_read_b32 v15, a75
	v_accvgpr_read_b32 v16, a76
	v_accvgpr_read_b32 v17, a77
	v_accvgpr_read_b32 v18, a78
	v_accvgpr_read_b32 v19, a79

	v_bitop3_b32 v20, v20, v6, 30 bitop3:0x78
	v_mul_f32_e32 v2, v2, v7
	v_lshl_add_u32 v75, v20, 4, v1
	v_mul_f32_e32 v3, v3, v7
	v_mul_f32_e32 v4, v4, v7
	v_mul_f32_e32 v5, v5, v7
	ds_write_b128 v75, v[2:5]
	v_mul_f32_e32 v2, v8, v7
	v_add_u32_e32 v8, 18, v128
	v_bitop3_b32 v8, v8, v6, 30 bitop3:0x78
	v_lshl_add_u32 v76, v8, 4, v1
	v_add_u32_e32 v8, 20, v128
	v_bitop3_b32 v8, v8, v6, 30 bitop3:0x78
	v_mul_f32_e32 v3, v9, v7
	v_mul_f32_e32 v4, v10, v7
	v_mul_f32_e32 v5, v11, v7
	v_lshl_add_u32 v77, v8, 4, v1
	v_add_u32_e32 v8, 22, v128
	ds_write_b128 v76, v[2:5]
	v_mul_f32_e32 v2, v12, v7
	v_mul_f32_e32 v3, v13, v7
	v_mul_f32_e32 v4, v14, v7
	v_mul_f32_e32 v5, v15, v7
	v_bitop3_b32 v8, v8, v6, 30 bitop3:0x78
	ds_write_b128 v77, v[2:5]
	v_mul_f32_e32 v2, v16, v7
	v_mul_f32_e32 v3, v17, v7
	v_mul_f32_e32 v4, v18, v7
	v_mul_f32_e32 v5, v19, v7
	v_lshl_add_u32 v78, v8, 4, v1
	v_add_u32_e32 v20, 24, v128
	ds_write_b128 v78, v[2:5]
	v_accvgpr_read_b32 v2, a96
	v_accvgpr_read_b32 v3, a97
	v_accvgpr_read_b32 v4, a98
	v_accvgpr_read_b32 v5, a99
	v_accvgpr_read_b32 v8, a100
	v_accvgpr_read_b32 v9, a101
	v_accvgpr_read_b32 v10, a102
	v_accvgpr_read_b32 v11, a103
	v_accvgpr_read_b32 v12, a104
	v_accvgpr_read_b32 v13, a105
	v_accvgpr_read_b32 v14, a106
	v_accvgpr_read_b32 v15, a107
	v_accvgpr_read_b32 v16, a108
	v_accvgpr_read_b32 v17, a109
	v_accvgpr_read_b32 v18, a110
	v_accvgpr_read_b32 v19, a111

	v_bitop3_b32 v20, v20, v6, 30 bitop3:0x78
	v_mul_f32_e32 v2, v2, v7
	v_lshl_add_u32 v79, v20, 4, v1
	v_mul_f32_e32 v3, v3, v7
	v_mul_f32_e32 v4, v4, v7
	v_mul_f32_e32 v5, v5, v7
	ds_write_b128 v79, v[2:5]
	v_mul_f32_e32 v2, v8, v7
	v_add_u32_e32 v8, 26, v128
	v_bitop3_b32 v8, v8, v6, 30 bitop3:0x78
	v_lshl_add_u32 v80, v8, 4, v1
	v_add_u32_e32 v8, 28, v128
	v_mul_f32_e32 v3, v9, v7
	v_mul_f32_e32 v4, v10, v7
	v_mul_f32_e32 v5, v11, v7
	v_bitop3_b32 v8, v8, v6, 30 bitop3:0x78
	ds_write_b128 v80, v[2:5]
	v_mul_f32_e32 v2, v12, v7
	v_mul_f32_e32 v3, v13, v7
	v_mul_f32_e32 v4, v14, v7
	v_mul_f32_e32 v5, v15, v7
	v_lshl_add_u32 v81, v8, 4, v1
	ds_write_b128 v81, v[2:5]
	v_mul_f32_e32 v2, v16, v7
	v_mul_f32_e32 v3, v17, v7
	v_mul_f32_e32 v4, v18, v7
	v_mul_f32_e32 v5, v19, v7
	v_add_u32_e32 v7, 30, v128
	v_bitop3_b32 v6, v7, v6, 30 bitop3:0x78
	v_lshl_add_u32 v1, v6, 4, v1
	ds_write_b128 v1, v[2:5]
	v_xor_b32_e32 v3, v202, v204
	v_lshlrev_b32_e32 v3, 5, v3
	v_xor_b32_e32 v11, v203, v204
	v_lshlrev_b32_e32 v2, 9, v202
	v_and_b32_e32 v34, 0x1e0, v3
	v_lshlrev_b32_e32 v11, 5, v11
	v_xor_b32_e32 v19, v205, v204
	s_waitcnt lgkmcnt(0)
	v_add3_u32 v82, v201, v2, v34
	v_lshlrev_b32_e32 v10, 9, v203
	v_and_b32_e32 v11, 0x1e0, v11
	v_lshlrev_b32_e32 v19, 5, v19
	ds_read_b128 v[2:5], v82
	ds_read_b128 v[6:9], v82 offset:16
	v_add3_u32 v83, v201, v10, v11
	v_lshlrev_b32_e32 v18, 9, v205
	v_and_b32_e32 v19, 0x1e0, v19
	ds_read_b128 v[10:13], v83
	ds_read_b128 v[14:17], v83 offset:16
	v_add3_u32 v84, v201, v18, v19
	ds_read_b128 v[18:21], v84
	ds_read_b128 v[22:25], v84 offset:16
	ds_read_b128 v[26:29], v85
	ds_read_b128 v[30:33], v85 offset:16
	v_add3_u32 v86, v201, v35, v34
	ds_read_b128 v[34:37], v86
	ds_read_b128 v[38:41], v86 offset:16
	v_lshlrev_b32_e32 v0, 4, v204
	ds_read_b128 v[42:45], v87
	ds_read_b128 v[46:49], v87 offset:16
	s_waitcnt lgkmcnt(11)
	v_cvt_pk_bf16_f32 v2, v2, v3
	v_cvt_pk_bf16_f32 v3, v4, v5
	s_waitcnt lgkmcnt(10)
	v_cvt_pk_bf16_f32 v4, v6, v7
	v_cvt_pk_bf16_f32 v5, v8, v9
	ds_read_b128 v[50:53], v88
	ds_read_b128 v[54:57], v88 offset:16
	ds_read_b128 v[58:61], v89
	ds_read_b128 v[66:69], v89 offset:16
	buffer_store_dwordx4 v[2:5], v0, s[8:11], s0 offen sc1
	s_waitcnt lgkmcnt(13)
	v_cvt_pk_bf16_f32 v2, v10, v11
	v_cvt_pk_bf16_f32 v3, v12, v13
	s_waitcnt lgkmcnt(12)
	v_cvt_pk_bf16_f32 v4, v14, v15
	v_cvt_pk_bf16_f32 v5, v16, v17
	buffer_store_dwordx4 v[2:5], v0, s[8:11], s1 offen sc1
	s_or_b32 s1, s0, 0x800
	s_waitcnt lgkmcnt(11)
	v_cvt_pk_bf16_f32 v2, v18, v19
	v_cvt_pk_bf16_f32 v3, v20, v21
	s_waitcnt lgkmcnt(10)
	v_cvt_pk_bf16_f32 v4, v22, v23
	v_cvt_pk_bf16_f32 v5, v24, v25
	buffer_store_dwordx4 v[2:5], v0, s[8:11], s1 offen sc1
	s_or_b32 s1, s0, 0xc00
	s_waitcnt lgkmcnt(9)
	v_cvt_pk_bf16_f32 v2, v26, v27
	v_cvt_pk_bf16_f32 v3, v28, v29
	s_waitcnt lgkmcnt(8)
	v_cvt_pk_bf16_f32 v4, v30, v31
	v_cvt_pk_bf16_f32 v5, v32, v33
	buffer_store_dwordx4 v[2:5], v0, s[8:11], s1 offen sc1
	s_or_b32 s1, s0, 0x1000
	s_waitcnt lgkmcnt(7)
	v_cvt_pk_bf16_f32 v2, v34, v35
	v_cvt_pk_bf16_f32 v3, v36, v37
	s_waitcnt lgkmcnt(6)
	v_cvt_pk_bf16_f32 v4, v38, v39
	v_cvt_pk_bf16_f32 v5, v40, v41
	buffer_store_dwordx4 v[2:5], v0, s[8:11], s1 offen sc1
	s_or_b32 s1, s0, 0x1400
	s_waitcnt lgkmcnt(5)
	v_cvt_pk_bf16_f32 v2, v42, v43
	v_cvt_pk_bf16_f32 v3, v44, v45
	s_waitcnt lgkmcnt(4)
	v_cvt_pk_bf16_f32 v4, v46, v47
	v_cvt_pk_bf16_f32 v5, v48, v49
	buffer_store_dwordx4 v[2:5], v0, s[8:11], s1 offen sc1
	s_or_b32 s1, s0, 0x1800
	s_waitcnt lgkmcnt(3)
	v_cvt_pk_bf16_f32 v2, v50, v51
	v_cvt_pk_bf16_f32 v3, v52, v53
	s_waitcnt lgkmcnt(2)
	v_cvt_pk_bf16_f32 v4, v54, v55
	v_cvt_pk_bf16_f32 v5, v56, v57
	v_rcp_f32_e32 v6, v64
	buffer_store_dwordx4 v[2:5], v0, s[8:11], s1 offen sc1
	s_or_b32 s1, s0, 0x1c00
	s_waitcnt lgkmcnt(1)
	v_cvt_pk_bf16_f32 v2, v58, v59
	v_cvt_pk_bf16_f32 v3, v60, v61
	s_waitcnt lgkmcnt(0)
	v_cvt_pk_bf16_f32 v4, v66, v67
	v_cvt_pk_bf16_f32 v5, v68, v69
	buffer_store_dwordx4 v[2:5], v0, s[8:11], s1 offen sc1
	s_waitcnt lgkmcnt(0)
	v_cmp_lt_f32_e32 vcc, 0, v64
	v_accvgpr_read_b32 v2, a16
	v_accvgpr_read_b32 v3, a17
	v_accvgpr_read_b32 v4, a18
	v_accvgpr_read_b32 v5, a19
	v_accvgpr_read_b32 v7, a20
	v_accvgpr_read_b32 v8, a21
	v_accvgpr_read_b32 v9, a22
	v_accvgpr_read_b32 v10, a23
	v_accvgpr_read_b32 v11, a24
	v_accvgpr_read_b32 v12, a25
	v_accvgpr_read_b32 v13, a26
	v_accvgpr_read_b32 v14, a27
	v_accvgpr_read_b32 v15, a28
	v_accvgpr_read_b32 v16, a29
	v_accvgpr_read_b32 v17, a30
	v_accvgpr_read_b32 v18, a31

	s_or_b32 s1, s0, 0x2000
	v_cndmask_b32_e32 v6, 0, v6, vcc
	v_mul_f32_e32 v2, v2, v6
	v_mul_f32_e32 v3, v3, v6
	v_mul_f32_e32 v4, v4, v6
	v_mul_f32_e32 v5, v5, v6
	ds_write_b128 v62, v[2:5]
	v_mul_f32_e32 v2, v7, v6
	v_mul_f32_e32 v3, v8, v6
	v_mul_f32_e32 v4, v9, v6
	v_mul_f32_e32 v5, v10, v6
	ds_write_b128 v63, v[2:5]
	v_mul_f32_e32 v2, v11, v6
	v_mul_f32_e32 v3, v12, v6
	v_mul_f32_e32 v4, v13, v6
	v_mul_f32_e32 v5, v14, v6
	ds_write_b128 v65, v[2:5]
	v_mul_f32_e32 v2, v15, v6
	v_mul_f32_e32 v3, v16, v6
	v_mul_f32_e32 v4, v17, v6
	v_mul_f32_e32 v5, v18, v6
	ds_write_b128 v70, v[2:5]
	v_accvgpr_read_b32 v2, a48
	v_accvgpr_read_b32 v3, a49
	v_accvgpr_read_b32 v4, a50
	v_accvgpr_read_b32 v5, a51
	v_accvgpr_read_b32 v7, a52
	v_accvgpr_read_b32 v8, a53
	v_accvgpr_read_b32 v9, a54
	v_accvgpr_read_b32 v10, a55
	v_accvgpr_read_b32 v11, a56
	v_accvgpr_read_b32 v12, a57
	v_accvgpr_read_b32 v13, a58
	v_accvgpr_read_b32 v14, a59
	v_accvgpr_read_b32 v15, a60
	v_accvgpr_read_b32 v16, a61
	v_accvgpr_read_b32 v17, a62
	v_accvgpr_read_b32 v18, a63

	v_mul_f32_e32 v2, v2, v6
	v_mul_f32_e32 v3, v3, v6
	v_mul_f32_e32 v4, v4, v6
	v_mul_f32_e32 v5, v5, v6
	ds_write_b128 v71, v[2:5]
	v_mul_f32_e32 v2, v7, v6
	v_mul_f32_e32 v3, v8, v6
	v_mul_f32_e32 v4, v9, v6
	v_mul_f32_e32 v5, v10, v6
	ds_write_b128 v72, v[2:5]
	v_mul_f32_e32 v2, v11, v6
	v_mul_f32_e32 v3, v12, v6
	v_mul_f32_e32 v4, v13, v6
	v_mul_f32_e32 v5, v14, v6
	ds_write_b128 v73, v[2:5]
	v_mul_f32_e32 v2, v15, v6
	v_mul_f32_e32 v3, v16, v6
	v_mul_f32_e32 v4, v17, v6
	v_mul_f32_e32 v5, v18, v6
	ds_write_b128 v74, v[2:5]
	v_accvgpr_read_b32 v2, a80
	v_accvgpr_read_b32 v3, a81
	v_accvgpr_read_b32 v4, a82
	v_accvgpr_read_b32 v5, a83
	v_accvgpr_read_b32 v7, a84
	v_accvgpr_read_b32 v8, a85
	v_accvgpr_read_b32 v9, a86
	v_accvgpr_read_b32 v10, a87
	v_accvgpr_read_b32 v11, a88
	v_accvgpr_read_b32 v12, a89
	v_accvgpr_read_b32 v13, a90
	v_accvgpr_read_b32 v14, a91
	v_accvgpr_read_b32 v15, a92
	v_accvgpr_read_b32 v16, a93
	v_accvgpr_read_b32 v17, a94
	v_accvgpr_read_b32 v18, a95

	v_mul_f32_e32 v2, v2, v6
	v_mul_f32_e32 v3, v3, v6
	v_mul_f32_e32 v4, v4, v6
	v_mul_f32_e32 v5, v5, v6
	ds_write_b128 v75, v[2:5]
	v_mul_f32_e32 v2, v7, v6
	v_mul_f32_e32 v3, v8, v6
	v_mul_f32_e32 v4, v9, v6
	v_mul_f32_e32 v5, v10, v6
	ds_write_b128 v76, v[2:5]
	v_mul_f32_e32 v2, v11, v6
	v_mul_f32_e32 v3, v12, v6
	v_mul_f32_e32 v4, v13, v6
	v_mul_f32_e32 v5, v14, v6
	ds_write_b128 v77, v[2:5]
	v_mul_f32_e32 v2, v15, v6
	v_mul_f32_e32 v3, v16, v6
	v_mul_f32_e32 v4, v17, v6
	v_mul_f32_e32 v5, v18, v6
	ds_write_b128 v78, v[2:5]
	v_accvgpr_read_b32 v2, a112
	v_accvgpr_read_b32 v3, a113
	v_accvgpr_read_b32 v4, a114
	v_accvgpr_read_b32 v5, a115
	v_accvgpr_read_b32 v7, a116
	v_accvgpr_read_b32 v8, a117
	v_accvgpr_read_b32 v9, a118
	v_accvgpr_read_b32 v10, a119
	v_accvgpr_read_b32 v11, a120
	v_accvgpr_read_b32 v12, a121
	v_accvgpr_read_b32 v13, a122
	v_accvgpr_read_b32 v14, a123
	v_accvgpr_read_b32 v15, a124
	v_accvgpr_read_b32 v16, a125
	v_accvgpr_read_b32 v17, a126
	v_accvgpr_read_b32 v18, a127

	v_mul_f32_e32 v2, v2, v6
	v_mul_f32_e32 v3, v3, v6
	v_mul_f32_e32 v4, v4, v6
	v_mul_f32_e32 v5, v5, v6
	ds_write_b128 v79, v[2:5]
	v_mul_f32_e32 v2, v7, v6
	v_mul_f32_e32 v3, v8, v6
	v_mul_f32_e32 v4, v9, v6
	v_mul_f32_e32 v5, v10, v6
	ds_write_b128 v80, v[2:5]
	v_mul_f32_e32 v2, v11, v6
	v_mul_f32_e32 v3, v12, v6
	v_mul_f32_e32 v4, v13, v6
	v_mul_f32_e32 v5, v14, v6
	ds_write_b128 v81, v[2:5]
	v_mul_f32_e32 v2, v15, v6
	v_mul_f32_e32 v3, v16, v6
	v_mul_f32_e32 v4, v17, v6
	v_mul_f32_e32 v5, v18, v6
	ds_write_b128 v1, v[2:5]
	s_waitcnt lgkmcnt(0)
	ds_read_b128 v[2:5], v82
	ds_read_b128 v[6:9], v82 offset:16
	ds_read_b128 v[10:13], v83
	ds_read_b128 v[14:17], v83 offset:16
	ds_read_b128 v[18:21], v84
	ds_read_b128 v[22:25], v84 offset:16
	ds_read_b128 v[26:29], v85
	ds_read_b128 v[30:33], v85 offset:16
	ds_read_b128 v[34:37], v86
	ds_read_b128 v[38:41], v86 offset:16
	ds_read_b128 v[42:45], v87
	ds_read_b128 v[46:49], v87 offset:16
	ds_read_b128 v[50:53], v88
	ds_read_b128 v[54:57], v88 offset:16
	ds_read_b128 v[58:61], v89
	ds_read_b128 v[62:65], v89 offset:16
	s_waitcnt lgkmcnt(14)
	v_cvt_pk_bf16_f32 v2, v2, v3
	v_cvt_pk_bf16_f32 v3, v4, v5
	v_cvt_pk_bf16_f32 v4, v6, v7
	v_cvt_pk_bf16_f32 v5, v8, v9
	buffer_store_dwordx4 v[2:5], v0, s[8:11], s1 offen sc1
	s_or_b32 s1, s0, 0x2400
	s_waitcnt lgkmcnt(13)
	v_cvt_pk_bf16_f32 v2, v10, v11
	v_cvt_pk_bf16_f32 v3, v12, v13
	s_waitcnt lgkmcnt(12)
	v_cvt_pk_bf16_f32 v4, v14, v15
	v_cvt_pk_bf16_f32 v5, v16, v17
	buffer_store_dwordx4 v[2:5], v0, s[8:11], s1 offen sc1
	s_or_b32 s1, s0, 0x2800
	s_waitcnt lgkmcnt(11)
	v_cvt_pk_bf16_f32 v2, v18, v19
	v_cvt_pk_bf16_f32 v3, v20, v21
	s_waitcnt lgkmcnt(10)
	v_cvt_pk_bf16_f32 v4, v22, v23
	v_cvt_pk_bf16_f32 v5, v24, v25
	buffer_store_dwordx4 v[2:5], v0, s[8:11], s1 offen sc1
	s_or_b32 s1, s0, 0x2c00
	s_waitcnt lgkmcnt(9)
	v_cvt_pk_bf16_f32 v2, v26, v27
	v_cvt_pk_bf16_f32 v3, v28, v29
	s_waitcnt lgkmcnt(8)
	v_cvt_pk_bf16_f32 v4, v30, v31
	v_cvt_pk_bf16_f32 v5, v32, v33
	buffer_store_dwordx4 v[2:5], v0, s[8:11], s1 offen sc1
	s_or_b32 s1, s0, 0x3000
	s_waitcnt lgkmcnt(7)
	v_cvt_pk_bf16_f32 v2, v34, v35
	v_cvt_pk_bf16_f32 v3, v36, v37
	s_waitcnt lgkmcnt(6)
	v_cvt_pk_bf16_f32 v4, v38, v39
	v_cvt_pk_bf16_f32 v5, v40, v41
	buffer_store_dwordx4 v[2:5], v0, s[8:11], s1 offen sc1
	s_or_b32 s1, s0, 0x3400
	s_waitcnt lgkmcnt(5)
	v_cvt_pk_bf16_f32 v2, v42, v43
	v_cvt_pk_bf16_f32 v3, v44, v45
	s_waitcnt lgkmcnt(4)
	v_cvt_pk_bf16_f32 v4, v46, v47
	v_cvt_pk_bf16_f32 v5, v48, v49
	buffer_store_dwordx4 v[2:5], v0, s[8:11], s1 offen sc1
	s_or_b32 s1, s0, 0x3800
	s_waitcnt lgkmcnt(3)
	v_cvt_pk_bf16_f32 v2, v50, v51
	v_cvt_pk_bf16_f32 v3, v52, v53
	s_waitcnt lgkmcnt(2)
	v_cvt_pk_bf16_f32 v4, v54, v55
	v_cvt_pk_bf16_f32 v5, v56, v57
	buffer_store_dwordx4 v[2:5], v0, s[8:11], s1 offen sc1
	s_or_b32 s0, s0, 0x3c00
	s_waitcnt lgkmcnt(1)
	v_cvt_pk_bf16_f32 v2, v58, v59
	v_cvt_pk_bf16_f32 v3, v60, v61
	s_waitcnt lgkmcnt(0)
	v_cvt_pk_bf16_f32 v4, v62, v63
	v_cvt_pk_bf16_f32 v5, v64, v65
	buffer_store_dwordx4 v[2:5], v0, s[8:11], s0 offen sc1
	s_waitcnt lgkmcnt(0)
	s_endpgm

	.amdhsa_kernel attn_fwd_pwg4x64
		.amdhsa_group_segment_fixed_size 0
		.amdhsa_private_segment_fixed_size 0
		.amdhsa_kernarg_size 72
		.amdhsa_user_sgpr_count 2
		.amdhsa_user_sgpr_dispatch_ptr 0
		.amdhsa_user_sgpr_queue_ptr 0
		.amdhsa_user_sgpr_kernarg_segment_ptr 1
		.amdhsa_user_sgpr_dispatch_id 0
		.amdhsa_user_sgpr_kernarg_preload_length 0
		.amdhsa_user_sgpr_kernarg_preload_offset 0
		.amdhsa_user_sgpr_private_segment_size 0
		.amdhsa_uses_dynamic_stack 0
		.amdhsa_enable_private_segment 0
		.amdhsa_system_sgpr_workgroup_id_x 1
		.amdhsa_system_sgpr_workgroup_id_y 0
		.amdhsa_system_sgpr_workgroup_id_z 0
		.amdhsa_system_sgpr_workgroup_info 0
		.amdhsa_system_vgpr_workitem_id 0
		.amdhsa_next_free_vgpr 512
		.amdhsa_next_free_sgpr 74
		.amdhsa_accum_offset 256
		.amdhsa_reserve_vcc 1
		.amdhsa_float_round_mode_32 0
		.amdhsa_float_round_mode_16_64 0
		.amdhsa_float_denorm_mode_32 3
		.amdhsa_float_denorm_mode_16_64 3
		.amdhsa_dx10_clamp 1
		.amdhsa_ieee_mode 1
		.amdhsa_fp16_overflow 0
		.amdhsa_tg_split 0
		.amdhsa_exception_fp_ieee_invalid_op 0
		.amdhsa_exception_fp_denorm_src 0
		.amdhsa_exception_fp_ieee_div_zero 0
		.amdhsa_exception_fp_ieee_overflow 0
		.amdhsa_exception_fp_ieee_underflow 0
		.amdhsa_exception_fp_ieee_inexact 0
		.amdhsa_exception_int_div_zero 0
	.end_amdhsa_kernel

_Z14headsum_kernelPKtPKfPjPf:
	s_load_dwordx2 s[4:5], s[0:1], 0x0
	s_mov_b32 s3, 0
	s_cmp_lg_u32 s2, 0
	v_mov_b32_e32 v69, 0
	s_cbranch_scc1 .LBB1_2
	s_load_dwordx2 s[6:7], s[0:1], 0x10
	v_lshlrev_b32_e32 v1, 2, v0
	s_waitcnt lgkmcnt(0)
	global_store_dword v1, v69, s[6:7]
	global_store_dword v1, v69, s[6:7] offset:1024
	global_store_dword v1, v69, s[6:7] offset:2048

amdhsa.kernels:
  - .agpr_count:     256
    .args:
      - .actual_access:  read_only
        .address_space:  global
        .offset:         0
        .size:           8
        .value_kind:     global_buffer
      - .address_space:  global
        .offset:         8
        .size:           8
        .value_kind:     global_buffer
      - .address_space:  global
        .offset:         16
        .size:           8
        .value_kind:     global_buffer
      - .actual_access:  write_only
        .address_space:  global
        .offset:         24
        .size:           8
        .value_kind:     global_buffer
      - .actual_access:  read_only
        .address_space:  global
        .offset:         32
        .size:           8
        .value_kind:     global_buffer
      - .actual_access:  read_only
        .address_space:  global
        .offset:         40
        .size:           8
        .value_kind:     global_buffer
      - .address_space:  global
        .offset:         48
        .size:           8
        .value_kind:     global_buffer
      - .address_space:  global
        .offset:         56
        .size:           8
        .value_kind:     global_buffer
      - .actual_access:  write_only
        .address_space:  global
        .offset:         64
        .size:           8
        .value_kind:     global_buffer
    .group_segment_fixed_size: 0
    .kernarg_segment_align: 8
    .kernarg_segment_size: 72
    .language:       OpenCL C
    .language_version:
      - 2
      - 0
    .max_flat_workgroup_size: 256
    .name:           attn_fwd_pwg4x64
    .private_segment_fixed_size: 0
    .sgpr_count:     80
    .sgpr_spill_count: 0
    .symbol:         attn_fwd_pwg4x64.kd
    .uniform_work_group_size: 1
    .uses_dynamic_stack: false
    .vgpr_count:     512
    .vgpr_spill_count: 0
    .wavefront_size: 64
  - .agpr_count:     0
    .args:
      - .actual_access:  read_only
        .address_space:  global
        .offset:         0
        .size:           8
        .value_kind:     global_buffer
      - .actual_access:  read_only
        .address_space:  global
        .offset:         8
        .size:           8
        .value_kind:     global_buffer
      - .actual_access:  write_only
        .address_space:  global
        .offset:         16
        .size:           8
        .value_kind:     global_buffer
      - .actual_access:  write_only
        .address_space:  global
        .offset:         24
        .size:           8
        .value_kind:     global_buffer
    .group_segment_fixed_size: 512
    .kernarg_segment_align: 8
    .kernarg_segment_size: 32
    .language:       OpenCL C
    .language_version:
      - 2
      - 0
    .max_flat_workgroup_size: 256
    .name:           _Z14headsum_kernelPKtPKfPjPf
    .private_segment_fixed_size: 0
    .sgpr_count:     18
    .sgpr_spill_count: 0
    .symbol:         _Z14headsum_kernelPKtPKfPjPf.kd
    .uniform_work_group_size: 1
    .uses_dynamic_stack: false
    .vgpr_count:     88
    .vgpr_spill_count: 0
    .wavefront_size: 64
